# combined: GEMM first-trip peel (no per-unit accumulator zeroing) + redundant post-barrier lgkmcnt removed in K-loops + SSD scan first-trip-only head waits dropped, all on the s_setprio-free build
# speedup vs baseline: 1.0010x; 1.0010x over previous
; #define LAS __attribute__((address_space(3)))
;     __device__ __forceinline__ bool next(int i, Unit& u) const { if (i >= per * reps) return false; return StaticOrder::next(i % per, u); }
; #define PG8_STAGE_A(bufoff, base_, nx_, kb_, h_) do { if (GATHER) { if (nx_) PG8_STAGE_G(bufoff, kb_, goN, h_); else PG8_STAGE_G(bufoff, kb_, goC, h_); } \
;         else PG8_STAGE(bufoff, (base_) + (kb_) + (h_) * hstep, voffA); } while (0)
; #define PG8_STAGE(bufoff, gbase, voff) do { _Pragma("unroll") for (int _i = 0; _i < 2; ++_i) \
;         __builtin_amdgcn_global_load_lds((const unsigned*)((const char*)(gbase) + (voff)[_i]), (LAS unsigned*)(lds + (bufoff) + ldsw + _i * 8192), 16, 0, 0); } while (0)
; #define PG8_WAIT_V(n) asm volatile("s_waitcnt vmcnt(" #n ")" ::: "memory")
; #define PG8_WAIT_L(n) asm volatile("s_waitcnt lgkmcnt(" #n ")" ::: "memory")
; template <class Epi, class Sched, bool GATHER = false>
; __device__ __forceinline__ void gemm_phase(LAS unsigned char* lds, const Gemm g, const Sched& S, const Epi& E, const int tid) {
;     ...
;         const bool has_next = S.next(ui + 1, nxt);
;         const char* nA = has_next ? (const char*)g.A + (size_t)nxt.pm * tstep : cA; const char* nB = has_next ? (const char*)g.Bt + (size_t)nxt.pb * tstep : cB;
;         if (GATHER && has_next && wid < 4) __builtin_amdgcn_global_load_lds((const unsigned*)(g.rowmap + nxt.rb + tid), (LAS unsigned*)(lds + STAGE_BYTES + ((ui + 1) & 1) * 1024 + wid * 256), 4, 0, 0);
;         for (int t = 0; t < nt; t += 2) {
;             const bool last = (t == nt - 2);
;             const char* a1 = cA + (size_t)(t + 1) * kstep;
;             const char* a2 = last ? nA : cA + (size_t)(t + 2) * kstep; const char* b2 = last ? nB : cB + (size_t)(t + 2) * kstep;
;             const char* a3 = a2 + kstep; const char* b3 = b2 + kstep;
;     ...
;             PG8_LDB(B0, 0, 0); PG8_LDB(B1, 0, 1); PG8_SCHED; PG8_LDA(At, 0, 0); PG8_STAGE_A(PG8_SA(1, 1), cA, false, kb1, 1);
;             PG8_WAIT_V(8); PG8_WAIT_L(0); PG8_BAR; PG8_MMA(0, 0, At, B0); PG8_MMA(0, 1, At, B1); PG8_BAR; PG8_SCHED;
;             PG8_LDA(At, 0, 1); PG8_STAGE(PG8_SB(0, 0), b2, voffB); PG8_STAGE(PG8_SB(0, 1), b2 + hstep, voffB); PG8_STAGE_A(PG8_SA(0, 0), (last ? nA : cA), last, kb2, 0);
;             PG8_WAIT_V(8); PG8_WAIT_L(0); PG8_BAR; PG8_MMA(1, 0, At, B0); PG8_MMA(1, 1, At, B1); PG8_BAR; PG8_SCHED;
.LBB0_246:
	s_ashr_i32 s15, s14, 31
	s_lshl_b64 s[18:19], s[14:15], 20
	s_add_u32 s18, s31, s18
	s_addc_u32 s19, s33, s19
	s_ashr_i32 s13, s12, 31
	s_lshl_b64 s[20:21], s[12:13], 20
	s_add_u32 s20, s36, s20
	s_addc_u32 s21, s37, s21
	s_and_b64 s[24:25], s[4:5], exec
	s_cselect_b32 s13, s21, s23
	s_cselect_b32 s15, s20, s22
	s_add_u32 s49, s22, 0x100
	s_addc_u32 s50, s23, 0
	s_add_u32 s22, s16, 0x80080
	s_addc_u32 s23, s17, 0
	v_lshl_add_u64 v[4:5], s[22:23], 0, v[142:143]
	v_lshl_add_u64 v[146:147], s[22:23], 0, v[144:145]
	s_mov_b32 s51, -2
	s_mov_b64 s[28:29], 0
	s_add_u32 s22, s28, 0x100
	s_addc_u32 s23, s29, 0
	s_add_u32 s54, s49, s28
	s_addc_u32 s55, s50, s29
	s_add_i32 s24, 0, 0x10000
	s_add_i32 s56, 0, 0x14000
	v_add_u32_e32 v2, s24, v1
	ds_read_b128 v[152:155], v2
	ds_read_b128 v[156:159], v2 offset:1024
	ds_read_b128 v[160:163], v2 offset:2048
	ds_read_b128 v[164:167], v2 offset:3072
	v_add_u32_e32 v2, s56, v1
	ds_read_b128 v[168:171], v2
	ds_read_b128 v[172:175], v2 offset:1024
	ds_read_b128 v[176:179], v2 offset:2048
	ds_read_b128 v[180:183], v2 offset:3072
	s_add_i32 s58, s24, s38
	s_add_i32 m0, s11, 0xc000
	s_add_i32 s57, s11, 0xe000
	s_add_i32 s59, s58, 0x2000
	s_cmp_eq_u32 s51, 28
	s_cselect_b64 s[52:53], -1, 0
	s_and_b64 s[24:25], s[52:53], exec
	s_cselect_b32 s25, s13, s55
	s_cselect_b32 s24, s15, s54
	v_lshl_add_u64 v[218:219], v[4:5], 0, s[28:29]
	ds_read_b128 v[184:187], v150
	ds_read_b128 v[188:191], v150 offset:1024
	ds_read_b128 v[192:195], v150 offset:2048
	ds_read_b128 v[196:199], v150 offset:3072
	ds_read_b128 v[202:205], v150 offset:4096
	ds_read_b128 v[206:209], v150 offset:5120
	ds_read_b128 v[210:213], v150 offset:6144
	ds_read_b128 v[214:217], v150 offset:7168
	global_load_lds_dwordx4 v[218:219], off
	v_lshl_add_u64 v[218:219], v[146:147], 0, s[28:29]
	s_mov_b32 m0, s57
	s_nop 0
	global_load_lds_dwordx4 v[218:219], off
	s_waitcnt vmcnt(8)
	s_waitcnt lgkmcnt(0)
	s_barrier
	v_mfma_f32_16x16x32_bf16 v[14:17], v[152:155], v[184:187], 0
	v_mfma_f32_16x16x32_bf16 v[10:13], v[160:163], v[184:187], 0
	v_mfma_f32_16x16x32_bf16 v[6:9], v[152:155], v[192:195], 0
	v_mfma_f32_16x16x32_bf16 v[18:21], v[160:163], v[192:195], 0
	v_mfma_f32_16x16x32_bf16 v[22:25], v[152:155], v[202:205], 0
	v_mfma_f32_16x16x32_bf16 v[34:37], v[160:163], v[202:205], 0
	v_mfma_f32_16x16x32_bf16 v[26:29], v[152:155], v[210:213], 0
	v_mfma_f32_16x16x32_bf16 v[30:33], v[160:163], v[210:213], 0
	v_mfma_f32_16x16x32_bf16 v[14:17], v[156:159], v[188:191], v[14:17]
	v_mfma_f32_16x16x32_bf16 v[10:13], v[164:167], v[188:191], v[10:13]
	v_mfma_f32_16x16x32_bf16 v[6:9], v[156:159], v[196:199], v[6:9]
	v_mfma_f32_16x16x32_bf16 v[18:21], v[164:167], v[196:199], v[18:21]
	v_mfma_f32_16x16x32_bf16 v[22:25], v[156:159], v[206:209], v[22:25]
	v_mfma_f32_16x16x32_bf16 v[34:37], v[164:167], v[206:209], v[34:37]
	v_mfma_f32_16x16x32_bf16 v[26:29], v[156:159], v[214:217], v[26:29]
	v_mfma_f32_16x16x32_bf16 v[30:33], v[164:167], v[214:217], v[30:33]
	v_mfma_f32_16x16x32_bf16 v[66:69], v[168:171], v[184:187], 0
	v_mfma_f32_16x16x32_bf16 v[98:101], v[176:179], v[184:187], 0
	v_mfma_f32_16x16x32_bf16 v[62:65], v[168:171], v[192:195], 0
	v_mfma_f32_16x16x32_bf16 v[94:97], v[176:179], v[192:195], 0
	v_mfma_f32_16x16x32_bf16 v[58:61], v[168:171], v[202:205], 0
	v_mfma_f32_16x16x32_bf16 v[90:93], v[176:179], v[202:205], 0
	v_mfma_f32_16x16x32_bf16 v[54:57], v[168:171], v[210:213], 0
	v_mfma_f32_16x16x32_bf16 v[86:89], v[176:179], v[210:213], 0
	v_mfma_f32_16x16x32_bf16 v[66:69], v[172:175], v[188:191], v[66:69]
	v_mfma_f32_16x16x32_bf16 v[98:101], v[180:183], v[188:191], v[98:101]
	v_mfma_f32_16x16x32_bf16 v[62:65], v[172:175], v[196:199], v[62:65]
	v_mfma_f32_16x16x32_bf16 v[94:97], v[180:183], v[196:199], v[94:97]
	v_mfma_f32_16x16x32_bf16 v[58:61], v[172:175], v[206:209], v[58:61]
	v_mfma_f32_16x16x32_bf16 v[90:93], v[180:183], v[206:209], v[90:93]
	v_mfma_f32_16x16x32_bf16 v[54:57], v[172:175], v[214:217], v[54:57]
	v_mfma_f32_16x16x32_bf16 v[86:89], v[180:183], v[214:217], v[86:89]
	s_barrier
	s_mov_b32 m0, s58
	v_lshl_add_u64 v[218:219], s[24:25], 0, v[138:139]
	s_cselect_b32 s54, 0, s23
	s_cselect_b32 s55, 0, s22
	s_add_u32 s28, s24, 0x80000
	ds_read_b128 v[184:187], v150 offset:16384
	ds_read_b128 v[188:191], v150 offset:17408
	ds_read_b128 v[192:195], v150 offset:18432
	ds_read_b128 v[196:199], v150 offset:19456
	ds_read_b128 v[202:205], v150 offset:20480
	ds_read_b128 v[206:209], v150 offset:21504
	ds_read_b128 v[210:213], v150 offset:22528
	ds_read_b128 v[214:217], v150 offset:23552
	global_load_lds_dwordx4 v[218:219], off
	v_lshl_add_u64 v[220:221], s[24:25], 0, v[134:135]
	s_mov_b32 m0, s59
	s_addc_u32 s29, s25, 0
	s_add_i32 s56, s56, s38
	global_load_lds_dwordx4 v[220:221], off
	v_lshl_add_u64 v[222:223], s[28:29], 0, v[138:139]
	s_mov_b32 m0, s56
	s_nop 0
	global_load_lds_dwordx4 v[222:223], off
	v_lshl_add_u64 v[222:223], s[28:29], 0, v[134:135]
	s_add_i32 m0, s56, 0x2000
	s_and_b64 s[28:29], s[52:53], s[4:5]
	s_and_b64 s[28:29], s[28:29], exec
	s_cselect_b32 s28, s18, s16
	s_cselect_b32 s29, s19, s17
	s_add_u32 s28, s28, s55
	s_addc_u32 s29, s29, s54
	global_load_lds_dwordx4 v[222:223], off
	v_lshl_add_u64 v[222:223], s[28:29], 0, v[140:141]
	s_mov_b32 m0, s11
	v_lshl_add_u64 v[224:225], s[28:29], 0, v[136:137]
	global_load_lds_dwordx4 v[222:223], off
	s_mov_b32 m0, s40
	s_nop 0
	global_load_lds_dwordx4 v[224:225], off
	s_waitcnt vmcnt(8)
	s_waitcnt lgkmcnt(0)
	s_barrier
; #define PG8_STAGE_A(bufoff, base_, nx_, kb_, h_) do { if (GATHER) { if (nx_) PG8_STAGE_G(bufoff, kb_, goN, h_); else PG8_STAGE_G(bufoff, kb_, goC, h_); } \
;         else PG8_STAGE(bufoff, (base_) + (kb_) + (h_) * hstep, voffA); } while (0)
; #define PG8_LDA(dst, b, h) do { _Pragma("unroll") for (int m = 0; m < 4; ++m) _Pragma("unroll") for (int k = 0; k < 2; ++k) dst[m][k] = *(const LAS bf16x8*)(lds + PG8_SA(b, h) + aoff + m * 2048 + k * 1024); } while (0)
; #define PG8_LDB(dst, b, h) do { _Pragma("unroll") for (int n = 0; n < 2; ++n) _Pragma("unroll") for (int k = 0; k < 2; ++k) dst[n][k] = *(const LAS bf16x8*)(lds + PG8_SB(b, h) + boff + n * 2048 + k * 1024); } while (0)
; #define PG8_MMA(ai, bj, At, Bt) do { __builtin_amdgcn_s_setprio(1); _Pragma("unroll") for (int m = 0; m < 4; ++m) _Pragma("unroll") for (int n = 0; n < 2; ++n) _Pragma("unroll") for (int k = 0; k < 2; ++k) \
;         acc[ai][bj][m][n] = __builtin_amdgcn_mfma_f32_16x16x32_bf16(Bt[n][k], At[m][k], acc[ai][bj][m][n], 0, 0, 0); __builtin_amdgcn_s_setprio(0); } while (0)
; #define PG8_WAIT_V(n) asm volatile("s_waitcnt vmcnt(" #n ")" ::: "memory")
; #define PG8_WAIT_L(n) asm volatile("s_waitcnt lgkmcnt(" #n ")" ::: "memory")
; #define PG8_BAR __builtin_amdgcn_s_barrier()
; #define PG8_SCHED __builtin_amdgcn_sched_barrier(0)
; template <class Epi, class Sched, bool GATHER = false>
; __device__ __forceinline__ void gemm_phase(LAS unsigned char* lds, const Gemm g, const Sched& S, const Epi& E, const int tid) {
;     ...
;             PG8_WAIT_V(8); PG8_WAIT_L(0); PG8_BAR; PG8_MMA(1, 0, At, B0); PG8_MMA(1, 1, At, B1); PG8_BAR; PG8_SCHED;
;             PG8_LDB(B0, 1, 0); PG8_LDB(B1, 1, 1); PG8_SCHED; PG8_LDA(At, 1, 0); PG8_STAGE_A(PG8_SA(0, 1), (last ? nA : cA), last, kb2, 1);
;             PG8_WAIT_V(8); PG8_WAIT_L(0); PG8_BAR; PG8_MMA(0, 0, At, B0); PG8_MMA(0, 1, At, B1); PG8_BAR; PG8_SCHED;
	v_mfma_f32_16x16x32_bf16 v[50:53], v[152:155], v[184:187], 0
	v_mfma_f32_16x16x32_bf16 v[82:85], v[160:163], v[184:187], 0
	v_mfma_f32_16x16x32_bf16 v[46:49], v[152:155], v[192:195], 0
	v_mfma_f32_16x16x32_bf16 v[78:81], v[160:163], v[192:195], 0
	v_mfma_f32_16x16x32_bf16 v[42:45], v[152:155], v[202:205], 0
	v_mfma_f32_16x16x32_bf16 v[74:77], v[160:163], v[202:205], 0
	v_mfma_f32_16x16x32_bf16 v[38:41], v[152:155], v[210:213], 0
	v_mfma_f32_16x16x32_bf16 v[70:73], v[160:163], v[210:213], 0
	v_mfma_f32_16x16x32_bf16 v[50:53], v[156:159], v[188:191], v[50:53]
	v_mfma_f32_16x16x32_bf16 v[82:85], v[164:167], v[188:191], v[82:85]
	v_mfma_f32_16x16x32_bf16 v[46:49], v[156:159], v[196:199], v[46:49]
	v_mfma_f32_16x16x32_bf16 v[78:81], v[164:167], v[196:199], v[78:81]
	v_mfma_f32_16x16x32_bf16 v[42:45], v[156:159], v[206:209], v[42:45]
	v_mfma_f32_16x16x32_bf16 v[74:77], v[164:167], v[206:209], v[74:77]
	v_mfma_f32_16x16x32_bf16 v[38:41], v[156:159], v[214:217], v[38:41]
	v_mfma_f32_16x16x32_bf16 v[70:73], v[164:167], v[214:217], v[70:73]
	v_mfma_f32_16x16x32_bf16 v[114:117], v[168:171], v[184:187], 0
	v_mfma_f32_16x16x32_bf16 v[130:133], v[176:179], v[184:187], 0
	v_mfma_f32_16x16x32_bf16 v[110:113], v[168:171], v[192:195], 0
	v_mfma_f32_16x16x32_bf16 v[126:129], v[176:179], v[192:195], 0
	v_mfma_f32_16x16x32_bf16 v[106:109], v[168:171], v[202:205], 0
	v_mfma_f32_16x16x32_bf16 v[122:125], v[176:179], v[202:205], 0
	v_mfma_f32_16x16x32_bf16 v[102:105], v[168:171], v[210:213], 0
	v_mfma_f32_16x16x32_bf16 v[118:121], v[176:179], v[210:213], 0
	v_mfma_f32_16x16x32_bf16 v[114:117], v[172:175], v[188:191], v[114:117]
	v_mfma_f32_16x16x32_bf16 v[130:133], v[180:183], v[188:191], v[130:133]
	v_mfma_f32_16x16x32_bf16 v[110:113], v[172:175], v[196:199], v[110:113]
	v_mfma_f32_16x16x32_bf16 v[126:129], v[180:183], v[196:199], v[126:129]
	v_mfma_f32_16x16x32_bf16 v[106:109], v[172:175], v[206:209], v[106:109]
	v_mfma_f32_16x16x32_bf16 v[122:125], v[180:183], v[206:209], v[122:125]
	v_mfma_f32_16x16x32_bf16 v[102:105], v[172:175], v[214:217], v[102:105]
	v_mfma_f32_16x16x32_bf16 v[118:121], v[180:183], v[214:217], v[118:121]
	s_barrier
	s_add_i32 s52, 0, 0x18000
	v_add_u32_e32 v2, s52, v1
	s_add_i32 s53, 0, 0x1c000
	ds_read_b128 v[152:155], v2
	ds_read_b128 v[156:159], v2 offset:1024
	ds_read_b128 v[160:163], v2 offset:2048
	ds_read_b128 v[164:167], v2 offset:3072
	v_add_u32_e32 v2, s53, v1
	ds_read_b128 v[168:171], v2
	ds_read_b128 v[172:175], v2 offset:1024
	ds_read_b128 v[176:179], v2 offset:2048
	ds_read_b128 v[180:183], v2 offset:3072
	s_add_u32 s28, s28, 0x80000
	s_addc_u32 s29, s29, 0
	s_mov_b32 m0, s41
	v_lshl_add_u64 v[226:227], s[28:29], 0, v[140:141]
	ds_read_b128 v[184:187], v150 offset:32768
	ds_read_b128 v[188:191], v150 offset:33792
	ds_read_b128 v[192:195], v150 offset:34816
	ds_read_b128 v[196:199], v150 offset:35840
	ds_read_b128 v[202:205], v150 offset:36864
	ds_read_b128 v[206:209], v150 offset:37888
	ds_read_b128 v[210:213], v150 offset:38912
	ds_read_b128 v[214:217], v150 offset:39936
	global_load_lds_dwordx4 v[226:227], off
	v_lshl_add_u64 v[226:227], s[28:29], 0, v[136:137]
	s_mov_b32 m0, s42
	s_nop 0
	global_load_lds_dwordx4 v[226:227], off
	s_waitcnt vmcnt(8)
	s_waitcnt lgkmcnt(0)
	s_barrier
	v_mfma_f32_16x16x32_bf16 v[14:17], v[152:155], v[184:187], v[14:17]
	v_mfma_f32_16x16x32_bf16 v[10:13], v[160:163], v[184:187], v[10:13]
	v_mfma_f32_16x16x32_bf16 v[6:9], v[152:155], v[192:195], v[6:9]
	v_mfma_f32_16x16x32_bf16 v[18:21], v[160:163], v[192:195], v[18:21]
	v_mfma_f32_16x16x32_bf16 v[22:25], v[152:155], v[202:205], v[22:25]
	v_mfma_f32_16x16x32_bf16 v[34:37], v[160:163], v[202:205], v[34:37]
	v_mfma_f32_16x16x32_bf16 v[26:29], v[152:155], v[210:213], v[26:29]
	v_mfma_f32_16x16x32_bf16 v[30:33], v[160:163], v[210:213], v[30:33]
	v_mfma_f32_16x16x32_bf16 v[14:17], v[156:159], v[188:191], v[14:17]
	v_mfma_f32_16x16x32_bf16 v[10:13], v[164:167], v[188:191], v[10:13]
	v_mfma_f32_16x16x32_bf16 v[6:9], v[156:159], v[196:199], v[6:9]
	v_mfma_f32_16x16x32_bf16 v[18:21], v[164:167], v[196:199], v[18:21]
	v_mfma_f32_16x16x32_bf16 v[22:25], v[156:159], v[206:209], v[22:25]
	v_mfma_f32_16x16x32_bf16 v[34:37], v[164:167], v[206:209], v[34:37]
	v_mfma_f32_16x16x32_bf16 v[26:29], v[156:159], v[214:217], v[26:29]
	v_mfma_f32_16x16x32_bf16 v[30:33], v[164:167], v[214:217], v[30:33]
	v_mfma_f32_16x16x32_bf16 v[66:69], v[168:171], v[184:187], v[66:69]
	v_mfma_f32_16x16x32_bf16 v[98:101], v[176:179], v[184:187], v[98:101]
	v_mfma_f32_16x16x32_bf16 v[62:65], v[168:171], v[192:195], v[62:65]
	v_mfma_f32_16x16x32_bf16 v[94:97], v[176:179], v[192:195], v[94:97]
	v_mfma_f32_16x16x32_bf16 v[58:61], v[168:171], v[202:205], v[58:61]
	v_mfma_f32_16x16x32_bf16 v[90:93], v[176:179], v[202:205], v[90:93]
	v_mfma_f32_16x16x32_bf16 v[54:57], v[168:171], v[210:213], v[54:57]
	v_mfma_f32_16x16x32_bf16 v[86:89], v[176:179], v[210:213], v[86:89]
	v_mfma_f32_16x16x32_bf16 v[66:69], v[172:175], v[188:191], v[66:69]
	v_mfma_f32_16x16x32_bf16 v[98:101], v[180:183], v[188:191], v[98:101]
	v_mfma_f32_16x16x32_bf16 v[62:65], v[172:175], v[196:199], v[62:65]
	v_mfma_f32_16x16x32_bf16 v[94:97], v[180:183], v[196:199], v[94:97]
	v_mfma_f32_16x16x32_bf16 v[58:61], v[172:175], v[206:209], v[58:61]
	v_mfma_f32_16x16x32_bf16 v[90:93], v[180:183], v[206:209], v[90:93]
	v_mfma_f32_16x16x32_bf16 v[54:57], v[172:175], v[214:217], v[54:57]
	v_mfma_f32_16x16x32_bf16 v[86:89], v[180:183], v[214:217], v[86:89]
	s_barrier
; #define PG8_STAGE_A(bufoff, base_, nx_, kb_, h_) do { if (GATHER) { if (nx_) PG8_STAGE_G(bufoff, kb_, goN, h_); else PG8_STAGE_G(bufoff, kb_, goC, h_); } \
;         else PG8_STAGE(bufoff, (base_) + (kb_) + (h_) * hstep, voffA); } while (0)
; #define PG8_STAGE(bufoff, gbase, voff) do { _Pragma("unroll") for (int _i = 0; _i < 2; ++_i) \
;         __builtin_amdgcn_global_load_lds((const unsigned*)((const char*)(gbase) + (voff)[_i]), (LAS unsigned*)(lds + (bufoff) + ldsw + _i * 8192), 16, 0, 0); } while (0)
; #define PG8_LDA(dst, b, h) do { _Pragma("unroll") for (int m = 0; m < 4; ++m) _Pragma("unroll") for (int k = 0; k < 2; ++k) dst[m][k] = *(const LAS bf16x8*)(lds + PG8_SA(b, h) + aoff + m * 2048 + k * 1024); } while (0)
; #define PG8_LDB(dst, b, h) do { _Pragma("unroll") for (int n = 0; n < 2; ++n) _Pragma("unroll") for (int k = 0; k < 2; ++k) dst[n][k] = *(const LAS bf16x8*)(lds + PG8_SB(b, h) + boff + n * 2048 + k * 1024); } while (0)
; #define PG8_WAIT_V(n) asm volatile("s_waitcnt vmcnt(" #n ")" ::: "memory")
; #define PG8_WAIT_L(n) asm volatile("s_waitcnt lgkmcnt(" #n ")" ::: "memory")
; template <class Epi, class Sched, bool GATHER = false>
; __device__ __forceinline__ void gemm_phase(LAS unsigned char* lds, const Gemm g, const Sched& S, const Epi& E, const int tid) {
;     ...
;             PG8_LDB(B0, 0, 0); PG8_LDB(B1, 0, 1); PG8_SCHED; PG8_LDA(At, 0, 0); PG8_STAGE_A(PG8_SA(1, 1), cA, false, kb1, 1);
;             PG8_WAIT_V(8); PG8_WAIT_L(0); PG8_BAR; PG8_MMA(0, 0, At, B0); PG8_MMA(0, 1, At, B1); PG8_BAR; PG8_SCHED;
;             PG8_LDA(At, 0, 1); PG8_STAGE(PG8_SB(0, 0), b2, voffB); PG8_STAGE(PG8_SB(0, 1), b2 + hstep, voffB); PG8_STAGE_A(PG8_SA(0, 0), (last ? nA : cA), last, kb2, 0);
;             PG8_WAIT_V(8); PG8_WAIT_L(0); PG8_BAR; PG8_MMA(1, 0, At, B0); PG8_MMA(1, 1, At, B1); PG8_BAR; PG8_SCHED;
;             PG8_LDB(B0, 1, 0); PG8_LDB(B1, 1, 1); PG8_SCHED; PG8_LDA(At, 1, 0); PG8_STAGE_A(PG8_SA(0, 1), (last ? nA : cA), last, kb2, 1);
;             PG8_WAIT_V(8); PG8_WAIT_L(0); PG8_BAR; PG8_MMA(0, 0, At, B0); PG8_MMA(0, 1, At, B1); PG8_BAR; PG8_SCHED;
;             PG8_LDA(At, 1, 1); PG8_STAGE(PG8_SB(1, 0), b3, voffB); PG8_STAGE(PG8_SB(1, 1), b3 + hstep, voffB); PG8_STAGE_A(PG8_SA(1, 0), (last ? nA : cA), last, kb3, 0);
;             PG8_WAIT_V(8); PG8_WAIT_L(0); PG8_BAR; PG8_MMA(1, 0, At, B0); PG8_MMA(1, 1, At, B1); PG8_BAR; PG8_SCHED;
	s_add_i32 s28, s52, s38
	v_lshl_add_u64 v[218:219], v[218:219], 0, s[0:1]
	s_mov_b32 m0, s28
	ds_read_b128 v[184:187], v150 offset:49152
	ds_read_b128 v[188:191], v150 offset:50176
	ds_read_b128 v[192:195], v150 offset:51200
	ds_read_b128 v[196:199], v150 offset:52224
	ds_read_b128 v[202:205], v150 offset:53248
	ds_read_b128 v[206:209], v150 offset:54272
	ds_read_b128 v[210:213], v150 offset:55296
	ds_read_b128 v[214:217], v150 offset:56320
	global_load_lds_dwordx4 v[218:219], off
	s_add_i32 m0, s28, 0x2000
	s_add_u32 s24, s24, 0x80080
	v_lshl_add_u64 v[218:219], v[220:221], 0, s[0:1]
	s_addc_u32 s25, s25, 0
	s_add_i32 s28, s53, s38
	global_load_lds_dwordx4 v[218:219], off
	v_lshl_add_u64 v[218:219], s[24:25], 0, v[138:139]
	s_mov_b32 m0, s28
	s_nop 0
	global_load_lds_dwordx4 v[218:219], off
	v_lshl_add_u64 v[218:219], s[24:25], 0, v[134:135]
	s_add_i32 m0, s28, 0x2000
	s_nop 0
	global_load_lds_dwordx4 v[218:219], off
	v_lshl_add_u64 v[218:219], v[222:223], 0, s[0:1]
	s_mov_b32 m0, s44
	s_nop 0
	global_load_lds_dwordx4 v[218:219], off
	v_lshl_add_u64 v[218:219], v[224:225], 0, s[0:1]
	s_mov_b32 m0, s45
	s_nop 0
	global_load_lds_dwordx4 v[218:219], off
	s_waitcnt vmcnt(8)
	s_waitcnt lgkmcnt(0)
	s_barrier
	v_mfma_f32_16x16x32_bf16 v[50:53], v[152:155], v[184:187], v[50:53]
	v_mfma_f32_16x16x32_bf16 v[82:85], v[160:163], v[184:187], v[82:85]
	v_mfma_f32_16x16x32_bf16 v[46:49], v[152:155], v[192:195], v[46:49]
	v_mfma_f32_16x16x32_bf16 v[78:81], v[160:163], v[192:195], v[78:81]
	v_mfma_f32_16x16x32_bf16 v[42:45], v[152:155], v[202:205], v[42:45]
	v_mfma_f32_16x16x32_bf16 v[74:77], v[160:163], v[202:205], v[74:77]
	v_mfma_f32_16x16x32_bf16 v[38:41], v[152:155], v[210:213], v[38:41]
	v_mfma_f32_16x16x32_bf16 v[70:73], v[160:163], v[210:213], v[70:73]
	v_mfma_f32_16x16x32_bf16 v[50:53], v[156:159], v[188:191], v[50:53]
	v_mfma_f32_16x16x32_bf16 v[82:85], v[164:167], v[188:191], v[82:85]
	v_mfma_f32_16x16x32_bf16 v[46:49], v[156:159], v[196:199], v[46:49]
	v_mfma_f32_16x16x32_bf16 v[78:81], v[164:167], v[196:199], v[78:81]
	v_mfma_f32_16x16x32_bf16 v[42:45], v[156:159], v[206:209], v[42:45]
	v_mfma_f32_16x16x32_bf16 v[74:77], v[164:167], v[206:209], v[74:77]
	v_mfma_f32_16x16x32_bf16 v[38:41], v[156:159], v[214:217], v[38:41]
	v_mfma_f32_16x16x32_bf16 v[70:73], v[164:167], v[214:217], v[70:73]
	v_mfma_f32_16x16x32_bf16 v[114:117], v[168:171], v[184:187], v[114:117]
	v_mfma_f32_16x16x32_bf16 v[130:133], v[176:179], v[184:187], v[130:133]
	v_mfma_f32_16x16x32_bf16 v[110:113], v[168:171], v[192:195], v[110:113]
	v_mfma_f32_16x16x32_bf16 v[126:129], v[176:179], v[192:195], v[126:129]
	v_mfma_f32_16x16x32_bf16 v[106:109], v[168:171], v[202:205], v[106:109]
	v_mfma_f32_16x16x32_bf16 v[122:125], v[176:179], v[202:205], v[122:125]
	v_mfma_f32_16x16x32_bf16 v[102:105], v[168:171], v[210:213], v[102:105]
	v_mfma_f32_16x16x32_bf16 v[118:121], v[176:179], v[210:213], v[118:121]
	v_mfma_f32_16x16x32_bf16 v[114:117], v[172:175], v[188:191], v[114:117]
	v_mfma_f32_16x16x32_bf16 v[130:133], v[180:183], v[188:191], v[130:133]
	v_mfma_f32_16x16x32_bf16 v[110:113], v[172:175], v[196:199], v[110:113]
	v_mfma_f32_16x16x32_bf16 v[126:129], v[180:183], v[196:199], v[126:129]
	v_mfma_f32_16x16x32_bf16 v[106:109], v[172:175], v[206:209], v[106:109]
	v_mfma_f32_16x16x32_bf16 v[122:125], v[180:183], v[206:209], v[122:125]
	v_mfma_f32_16x16x32_bf16 v[102:105], v[172:175], v[214:217], v[102:105]
	v_mfma_f32_16x16x32_bf16 v[118:121], v[180:183], v[214:217], v[118:121]
	s_barrier
	s_add_i32 s51, s51, 2
	s_cmp_gt_u32 s51, 29
	s_mov_b64 s[28:29], s[22:23]
	s_cbranch_scc1 .Lpeel0_exit
.LBB0_247:
	s_add_u32 s22, s28, 0x100
	s_addc_u32 s23, s29, 0
	s_add_u32 s54, s49, s28
	s_addc_u32 s55, s50, s29
	s_add_i32 s24, 0, 0x10000
	s_add_i32 s56, 0, 0x14000
	v_add_u32_e32 v2, s24, v1
	ds_read_b128 v[152:155], v2
	ds_read_b128 v[156:159], v2 offset:1024
	ds_read_b128 v[160:163], v2 offset:2048
	ds_read_b128 v[164:167], v2 offset:3072
	v_add_u32_e32 v2, s56, v1
	ds_read_b128 v[168:171], v2
	ds_read_b128 v[172:175], v2 offset:1024
	ds_read_b128 v[176:179], v2 offset:2048
	ds_read_b128 v[180:183], v2 offset:3072
	s_add_i32 s58, s24, s38
	s_add_i32 m0, s11, 0xc000
	s_add_i32 s57, s11, 0xe000
	s_add_i32 s59, s58, 0x2000
	s_cmp_eq_u32 s51, 28
	s_cselect_b64 s[52:53], -1, 0
	s_and_b64 s[24:25], s[52:53], exec
	s_cselect_b32 s25, s13, s55
	s_cselect_b32 s24, s15, s54
	v_lshl_add_u64 v[218:219], v[4:5], 0, s[28:29]
	ds_read_b128 v[184:187], v150
	ds_read_b128 v[188:191], v150 offset:1024
	ds_read_b128 v[192:195], v150 offset:2048
	ds_read_b128 v[196:199], v150 offset:3072
	ds_read_b128 v[202:205], v150 offset:4096
	ds_read_b128 v[206:209], v150 offset:5120
	ds_read_b128 v[210:213], v150 offset:6144
	ds_read_b128 v[214:217], v150 offset:7168
	global_load_lds_dwordx4 v[218:219], off
	v_lshl_add_u64 v[218:219], v[146:147], 0, s[28:29]
	s_mov_b32 m0, s57
	s_nop 0
	global_load_lds_dwordx4 v[218:219], off
	s_waitcnt vmcnt(8)
	s_waitcnt lgkmcnt(0)
	s_barrier
; #define PG8_STAGE_A(bufoff, base_, nx_, kb_, h_) do { if (GATHER) { if (nx_) PG8_STAGE_G(bufoff, kb_, goN, h_); else PG8_STAGE_G(bufoff, kb_, goC, h_); } \
;         else PG8_STAGE(bufoff, (base_) + (kb_) + (h_) * hstep, voffA); } while (0)
; #define PG8_STAGE(bufoff, gbase, voff) do { _Pragma("unroll") for (int _i = 0; _i < 2; ++_i) \
;         __builtin_amdgcn_global_load_lds((const unsigned*)((const char*)(gbase) + (voff)[_i]), (LAS unsigned*)(lds + (bufoff) + ldsw + _i * 8192), 16, 0, 0); } while (0)
; #define PG8_LDA(dst, b, h) do { _Pragma("unroll") for (int m = 0; m < 4; ++m) _Pragma("unroll") for (int k = 0; k < 2; ++k) dst[m][k] = *(const LAS bf16x8*)(lds + PG8_SA(b, h) + aoff + m * 2048 + k * 1024); } while (0)
; #define PG8_LDB(dst, b, h) do { _Pragma("unroll") for (int n = 0; n < 2; ++n) _Pragma("unroll") for (int k = 0; k < 2; ++k) dst[n][k] = *(const LAS bf16x8*)(lds + PG8_SB(b, h) + boff + n * 2048 + k * 1024); } while (0)
; #define PG8_MMA(ai, bj, At, Bt) do { __builtin_amdgcn_s_setprio(1); _Pragma("unroll") for (int m = 0; m < 4; ++m) _Pragma("unroll") for (int n = 0; n < 2; ++n) _Pragma("unroll") for (int k = 0; k < 2; ++k) \
;         acc[ai][bj][m][n] = __builtin_amdgcn_mfma_f32_16x16x32_bf16(Bt[n][k], At[m][k], acc[ai][bj][m][n], 0, 0, 0); __builtin_amdgcn_s_setprio(0); } while (0)
; #define PG8_WAIT_V(n) asm volatile("s_waitcnt vmcnt(" #n ")" ::: "memory")
; #define PG8_WAIT_L(n) asm volatile("s_waitcnt lgkmcnt(" #n ")" ::: "memory")
; #define PG8_BAR __builtin_amdgcn_s_barrier()
; #define PG8_SCHED __builtin_amdgcn_sched_barrier(0)
; template <class Epi, class Sched, bool GATHER = false>
; __device__ __forceinline__ void gemm_phase(LAS unsigned char* lds, const Gemm g, const Sched& S, const Epi& E, const int tid) {
;     ...
;             PG8_WAIT_V(8); PG8_WAIT_L(0); PG8_BAR; PG8_MMA(0, 0, At, B0); PG8_MMA(0, 1, At, B1); PG8_BAR; PG8_SCHED;
;             PG8_LDA(At, 0, 1); PG8_STAGE(PG8_SB(0, 0), b2, voffB); PG8_STAGE(PG8_SB(0, 1), b2 + hstep, voffB); PG8_STAGE_A(PG8_SA(0, 0), (last ? nA : cA), last, kb2, 0);
;             PG8_WAIT_V(8); PG8_WAIT_L(0); PG8_BAR; PG8_MMA(1, 0, At, B0); PG8_MMA(1, 1, At, B1); PG8_BAR; PG8_SCHED;
;             PG8_LDB(B0, 1, 0); PG8_LDB(B1, 1, 1); PG8_SCHED; PG8_LDA(At, 1, 0); PG8_STAGE_A(PG8_SA(0, 1), (last ? nA : cA), last, kb2, 1);
	v_mfma_f32_16x16x32_bf16 v[14:17], v[152:155], v[184:187], v[14:17]
	v_mfma_f32_16x16x32_bf16 v[10:13], v[160:163], v[184:187], v[10:13]
	v_mfma_f32_16x16x32_bf16 v[6:9], v[152:155], v[192:195], v[6:9]
	v_mfma_f32_16x16x32_bf16 v[18:21], v[160:163], v[192:195], v[18:21]
	v_mfma_f32_16x16x32_bf16 v[22:25], v[152:155], v[202:205], v[22:25]
	v_mfma_f32_16x16x32_bf16 v[34:37], v[160:163], v[202:205], v[34:37]
	v_mfma_f32_16x16x32_bf16 v[26:29], v[152:155], v[210:213], v[26:29]
	v_mfma_f32_16x16x32_bf16 v[30:33], v[160:163], v[210:213], v[30:33]
	v_mfma_f32_16x16x32_bf16 v[14:17], v[156:159], v[188:191], v[14:17]
	v_mfma_f32_16x16x32_bf16 v[10:13], v[164:167], v[188:191], v[10:13]
	v_mfma_f32_16x16x32_bf16 v[6:9], v[156:159], v[196:199], v[6:9]
	v_mfma_f32_16x16x32_bf16 v[18:21], v[164:167], v[196:199], v[18:21]
	v_mfma_f32_16x16x32_bf16 v[22:25], v[156:159], v[206:209], v[22:25]
	v_mfma_f32_16x16x32_bf16 v[34:37], v[164:167], v[206:209], v[34:37]
	v_mfma_f32_16x16x32_bf16 v[26:29], v[156:159], v[214:217], v[26:29]
	v_mfma_f32_16x16x32_bf16 v[30:33], v[164:167], v[214:217], v[30:33]
	v_mfma_f32_16x16x32_bf16 v[66:69], v[168:171], v[184:187], v[66:69]
	v_mfma_f32_16x16x32_bf16 v[98:101], v[176:179], v[184:187], v[98:101]
	v_mfma_f32_16x16x32_bf16 v[62:65], v[168:171], v[192:195], v[62:65]
	v_mfma_f32_16x16x32_bf16 v[94:97], v[176:179], v[192:195], v[94:97]
	v_mfma_f32_16x16x32_bf16 v[58:61], v[168:171], v[202:205], v[58:61]
	v_mfma_f32_16x16x32_bf16 v[90:93], v[176:179], v[202:205], v[90:93]
	v_mfma_f32_16x16x32_bf16 v[54:57], v[168:171], v[210:213], v[54:57]
	v_mfma_f32_16x16x32_bf16 v[86:89], v[176:179], v[210:213], v[86:89]
	v_mfma_f32_16x16x32_bf16 v[66:69], v[172:175], v[188:191], v[66:69]
	v_mfma_f32_16x16x32_bf16 v[98:101], v[180:183], v[188:191], v[98:101]
	v_mfma_f32_16x16x32_bf16 v[62:65], v[172:175], v[196:199], v[62:65]
	v_mfma_f32_16x16x32_bf16 v[94:97], v[180:183], v[196:199], v[94:97]
	v_mfma_f32_16x16x32_bf16 v[58:61], v[172:175], v[206:209], v[58:61]
	v_mfma_f32_16x16x32_bf16 v[90:93], v[180:183], v[206:209], v[90:93]
	v_mfma_f32_16x16x32_bf16 v[54:57], v[172:175], v[214:217], v[54:57]
	v_mfma_f32_16x16x32_bf16 v[86:89], v[180:183], v[214:217], v[86:89]
	s_barrier
	s_mov_b32 m0, s58
	v_lshl_add_u64 v[218:219], s[24:25], 0, v[138:139]
	s_cselect_b32 s54, 0, s23
	s_cselect_b32 s55, 0, s22
	s_add_u32 s28, s24, 0x80000
	ds_read_b128 v[184:187], v150 offset:16384
	ds_read_b128 v[188:191], v150 offset:17408
	ds_read_b128 v[192:195], v150 offset:18432
	ds_read_b128 v[196:199], v150 offset:19456
	ds_read_b128 v[202:205], v150 offset:20480
	ds_read_b128 v[206:209], v150 offset:21504
	ds_read_b128 v[210:213], v150 offset:22528
	ds_read_b128 v[214:217], v150 offset:23552
	global_load_lds_dwordx4 v[218:219], off
	v_lshl_add_u64 v[220:221], s[24:25], 0, v[134:135]
	s_mov_b32 m0, s59
	s_addc_u32 s29, s25, 0
	s_add_i32 s56, s56, s38
	global_load_lds_dwordx4 v[220:221], off
	v_lshl_add_u64 v[222:223], s[28:29], 0, v[138:139]
	s_mov_b32 m0, s56
	s_nop 0
	global_load_lds_dwordx4 v[222:223], off
	v_lshl_add_u64 v[222:223], s[28:29], 0, v[134:135]
	s_add_i32 m0, s56, 0x2000
	s_and_b64 s[28:29], s[52:53], s[4:5]
	s_and_b64 s[28:29], s[28:29], exec
	s_cselect_b32 s28, s18, s16
	s_cselect_b32 s29, s19, s17
	s_add_u32 s28, s28, s55
	s_addc_u32 s29, s29, s54
	global_load_lds_dwordx4 v[222:223], off
	v_lshl_add_u64 v[222:223], s[28:29], 0, v[140:141]
	s_mov_b32 m0, s11
	v_lshl_add_u64 v[224:225], s[28:29], 0, v[136:137]
	global_load_lds_dwordx4 v[222:223], off
	s_mov_b32 m0, s40
	s_nop 0
	global_load_lds_dwordx4 v[224:225], off
	s_waitcnt vmcnt(8)
	s_waitcnt lgkmcnt(0)
	s_barrier
	v_mfma_f32_16x16x32_bf16 v[50:53], v[152:155], v[184:187], v[50:53]
	v_mfma_f32_16x16x32_bf16 v[82:85], v[160:163], v[184:187], v[82:85]
	v_mfma_f32_16x16x32_bf16 v[46:49], v[152:155], v[192:195], v[46:49]
	v_mfma_f32_16x16x32_bf16 v[78:81], v[160:163], v[192:195], v[78:81]
	v_mfma_f32_16x16x32_bf16 v[42:45], v[152:155], v[202:205], v[42:45]
	v_mfma_f32_16x16x32_bf16 v[74:77], v[160:163], v[202:205], v[74:77]
	v_mfma_f32_16x16x32_bf16 v[38:41], v[152:155], v[210:213], v[38:41]
	v_mfma_f32_16x16x32_bf16 v[70:73], v[160:163], v[210:213], v[70:73]
	v_mfma_f32_16x16x32_bf16 v[50:53], v[156:159], v[188:191], v[50:53]
	v_mfma_f32_16x16x32_bf16 v[82:85], v[164:167], v[188:191], v[82:85]
	v_mfma_f32_16x16x32_bf16 v[46:49], v[156:159], v[196:199], v[46:49]
	v_mfma_f32_16x16x32_bf16 v[78:81], v[164:167], v[196:199], v[78:81]
	v_mfma_f32_16x16x32_bf16 v[42:45], v[156:159], v[206:209], v[42:45]
	v_mfma_f32_16x16x32_bf16 v[74:77], v[164:167], v[206:209], v[74:77]
	v_mfma_f32_16x16x32_bf16 v[38:41], v[156:159], v[214:217], v[38:41]
	v_mfma_f32_16x16x32_bf16 v[70:73], v[164:167], v[214:217], v[70:73]
	v_mfma_f32_16x16x32_bf16 v[114:117], v[168:171], v[184:187], v[114:117]
	v_mfma_f32_16x16x32_bf16 v[130:133], v[176:179], v[184:187], v[130:133]
	v_mfma_f32_16x16x32_bf16 v[110:113], v[168:171], v[192:195], v[110:113]
	v_mfma_f32_16x16x32_bf16 v[126:129], v[176:179], v[192:195], v[126:129]
	v_mfma_f32_16x16x32_bf16 v[106:109], v[168:171], v[202:205], v[106:109]
	v_mfma_f32_16x16x32_bf16 v[122:125], v[176:179], v[202:205], v[122:125]
	v_mfma_f32_16x16x32_bf16 v[102:105], v[168:171], v[210:213], v[102:105]
	v_mfma_f32_16x16x32_bf16 v[118:121], v[176:179], v[210:213], v[118:121]
	v_mfma_f32_16x16x32_bf16 v[114:117], v[172:175], v[188:191], v[114:117]
	v_mfma_f32_16x16x32_bf16 v[130:133], v[180:183], v[188:191], v[130:133]
	v_mfma_f32_16x16x32_bf16 v[110:113], v[172:175], v[196:199], v[110:113]
	v_mfma_f32_16x16x32_bf16 v[126:129], v[180:183], v[196:199], v[126:129]
	v_mfma_f32_16x16x32_bf16 v[106:109], v[172:175], v[206:209], v[106:109]
	v_mfma_f32_16x16x32_bf16 v[122:125], v[180:183], v[206:209], v[122:125]
	v_mfma_f32_16x16x32_bf16 v[102:105], v[172:175], v[214:217], v[102:105]
	v_mfma_f32_16x16x32_bf16 v[118:121], v[180:183], v[214:217], v[118:121]
	s_barrier
; #define PG8_STAGE_A(bufoff, base_, nx_, kb_, h_) do { if (GATHER) { if (nx_) PG8_STAGE_G(bufoff, kb_, goN, h_); else PG8_STAGE_G(bufoff, kb_, goC, h_); } \
;         else PG8_STAGE(bufoff, (base_) + (kb_) + (h_) * hstep, voffA); } while (0)
; #define PG8_STAGE(bufoff, gbase, voff) do { _Pragma("unroll") for (int _i = 0; _i < 2; ++_i) \
;         __builtin_amdgcn_global_load_lds((const unsigned*)((const char*)(gbase) + (voff)[_i]), (LAS unsigned*)(lds + (bufoff) + ldsw + _i * 8192), 16, 0, 0); } while (0)
; #define PG8_LDA(dst, b, h) do { _Pragma("unroll") for (int m = 0; m < 4; ++m) _Pragma("unroll") for (int k = 0; k < 2; ++k) dst[m][k] = *(const LAS bf16x8*)(lds + PG8_SA(b, h) + aoff + m * 2048 + k * 1024); } while (0)
; #define PG8_LDB(dst, b, h) do { _Pragma("unroll") for (int n = 0; n < 2; ++n) _Pragma("unroll") for (int k = 0; k < 2; ++k) dst[n][k] = *(const LAS bf16x8*)(lds + PG8_SB(b, h) + boff + n * 2048 + k * 1024); } while (0)
; #define PG8_MMA(ai, bj, At, Bt) do { __builtin_amdgcn_s_setprio(1); _Pragma("unroll") for (int m = 0; m < 4; ++m) _Pragma("unroll") for (int n = 0; n < 2; ++n) _Pragma("unroll") for (int k = 0; k < 2; ++k) \
;         acc[ai][bj][m][n] = __builtin_amdgcn_mfma_f32_16x16x32_bf16(Bt[n][k], At[m][k], acc[ai][bj][m][n], 0, 0, 0); __builtin_amdgcn_s_setprio(0); } while (0)
; #define PG8_WAIT_V(n) asm volatile("s_waitcnt vmcnt(" #n ")" ::: "memory")
; #define PG8_WAIT_L(n) asm volatile("s_waitcnt lgkmcnt(" #n ")" ::: "memory")
; #define PG8_BAR __builtin_amdgcn_s_barrier()
; #define PG8_SCHED __builtin_amdgcn_sched_barrier(0)
; template <class Epi, class Sched, bool GATHER = false>
; __device__ __forceinline__ void gemm_phase(LAS unsigned char* lds, const Gemm g, const Sched& S, const Epi& E, const int tid) {
;     ...
;             PG8_LDB(B0, 1, 0); PG8_LDB(B1, 1, 1); PG8_SCHED; PG8_LDA(At, 1, 0); PG8_STAGE_A(PG8_SA(0, 1), (last ? nA : cA), last, kb2, 1);
;             PG8_WAIT_V(8); PG8_WAIT_L(0); PG8_BAR; PG8_MMA(0, 0, At, B0); PG8_MMA(0, 1, At, B1); PG8_BAR; PG8_SCHED;
;             PG8_LDA(At, 1, 1); PG8_STAGE(PG8_SB(1, 0), b3, voffB); PG8_STAGE(PG8_SB(1, 1), b3 + hstep, voffB); PG8_STAGE_A(PG8_SA(1, 0), (last ? nA : cA), last, kb3, 0);
;             PG8_WAIT_V(8); PG8_WAIT_L(0); PG8_BAR; PG8_MMA(1, 0, At, B0); PG8_MMA(1, 1, At, B1); PG8_BAR; PG8_SCHED;
	s_add_i32 s52, 0, 0x18000
	v_add_u32_e32 v2, s52, v1
	s_add_i32 s53, 0, 0x1c000
	ds_read_b128 v[152:155], v2
	ds_read_b128 v[156:159], v2 offset:1024
	ds_read_b128 v[160:163], v2 offset:2048
	ds_read_b128 v[164:167], v2 offset:3072
	v_add_u32_e32 v2, s53, v1
	ds_read_b128 v[168:171], v2
	ds_read_b128 v[172:175], v2 offset:1024
	ds_read_b128 v[176:179], v2 offset:2048
	ds_read_b128 v[180:183], v2 offset:3072
	s_add_u32 s28, s28, 0x80000
	s_addc_u32 s29, s29, 0
	s_mov_b32 m0, s41
	v_lshl_add_u64 v[226:227], s[28:29], 0, v[140:141]
	ds_read_b128 v[184:187], v150 offset:32768
	ds_read_b128 v[188:191], v150 offset:33792
	ds_read_b128 v[192:195], v150 offset:34816
	ds_read_b128 v[196:199], v150 offset:35840
	ds_read_b128 v[202:205], v150 offset:36864
	ds_read_b128 v[206:209], v150 offset:37888
	ds_read_b128 v[210:213], v150 offset:38912
	ds_read_b128 v[214:217], v150 offset:39936
	global_load_lds_dwordx4 v[226:227], off
	v_lshl_add_u64 v[226:227], s[28:29], 0, v[136:137]
	s_mov_b32 m0, s42
	s_nop 0
	global_load_lds_dwordx4 v[226:227], off
	s_waitcnt vmcnt(8)
	s_waitcnt lgkmcnt(0)
	s_barrier
	v_mfma_f32_16x16x32_bf16 v[14:17], v[152:155], v[184:187], v[14:17]
	v_mfma_f32_16x16x32_bf16 v[10:13], v[160:163], v[184:187], v[10:13]
	v_mfma_f32_16x16x32_bf16 v[6:9], v[152:155], v[192:195], v[6:9]
	v_mfma_f32_16x16x32_bf16 v[18:21], v[160:163], v[192:195], v[18:21]
	v_mfma_f32_16x16x32_bf16 v[22:25], v[152:155], v[202:205], v[22:25]
	v_mfma_f32_16x16x32_bf16 v[34:37], v[160:163], v[202:205], v[34:37]
	v_mfma_f32_16x16x32_bf16 v[26:29], v[152:155], v[210:213], v[26:29]
	v_mfma_f32_16x16x32_bf16 v[30:33], v[160:163], v[210:213], v[30:33]
	v_mfma_f32_16x16x32_bf16 v[14:17], v[156:159], v[188:191], v[14:17]
	v_mfma_f32_16x16x32_bf16 v[10:13], v[164:167], v[188:191], v[10:13]
	v_mfma_f32_16x16x32_bf16 v[6:9], v[156:159], v[196:199], v[6:9]
	v_mfma_f32_16x16x32_bf16 v[18:21], v[164:167], v[196:199], v[18:21]
	v_mfma_f32_16x16x32_bf16 v[22:25], v[156:159], v[206:209], v[22:25]
	v_mfma_f32_16x16x32_bf16 v[34:37], v[164:167], v[206:209], v[34:37]
	v_mfma_f32_16x16x32_bf16 v[26:29], v[156:159], v[214:217], v[26:29]
	v_mfma_f32_16x16x32_bf16 v[30:33], v[164:167], v[214:217], v[30:33]
	v_mfma_f32_16x16x32_bf16 v[66:69], v[168:171], v[184:187], v[66:69]
	v_mfma_f32_16x16x32_bf16 v[98:101], v[176:179], v[184:187], v[98:101]
	v_mfma_f32_16x16x32_bf16 v[62:65], v[168:171], v[192:195], v[62:65]
	v_mfma_f32_16x16x32_bf16 v[94:97], v[176:179], v[192:195], v[94:97]
	v_mfma_f32_16x16x32_bf16 v[58:61], v[168:171], v[202:205], v[58:61]
	v_mfma_f32_16x16x32_bf16 v[90:93], v[176:179], v[202:205], v[90:93]
	v_mfma_f32_16x16x32_bf16 v[54:57], v[168:171], v[210:213], v[54:57]
	v_mfma_f32_16x16x32_bf16 v[86:89], v[176:179], v[210:213], v[86:89]
	v_mfma_f32_16x16x32_bf16 v[66:69], v[172:175], v[188:191], v[66:69]
	v_mfma_f32_16x16x32_bf16 v[98:101], v[180:183], v[188:191], v[98:101]
	v_mfma_f32_16x16x32_bf16 v[62:65], v[172:175], v[196:199], v[62:65]
	v_mfma_f32_16x16x32_bf16 v[94:97], v[180:183], v[196:199], v[94:97]
	v_mfma_f32_16x16x32_bf16 v[58:61], v[172:175], v[206:209], v[58:61]
	v_mfma_f32_16x16x32_bf16 v[90:93], v[180:183], v[206:209], v[90:93]
	v_mfma_f32_16x16x32_bf16 v[54:57], v[172:175], v[214:217], v[54:57]
	v_mfma_f32_16x16x32_bf16 v[86:89], v[180:183], v[214:217], v[86:89]
	s_barrier
	s_add_i32 s28, s52, s38
	v_lshl_add_u64 v[218:219], v[218:219], 0, s[0:1]
	s_mov_b32 m0, s28
	ds_read_b128 v[184:187], v150 offset:49152
	ds_read_b128 v[188:191], v150 offset:50176
	ds_read_b128 v[192:195], v150 offset:51200
	ds_read_b128 v[196:199], v150 offset:52224
	ds_read_b128 v[202:205], v150 offset:53248
	ds_read_b128 v[206:209], v150 offset:54272
	ds_read_b128 v[210:213], v150 offset:55296
	ds_read_b128 v[214:217], v150 offset:56320
	global_load_lds_dwordx4 v[218:219], off
	s_add_i32 m0, s28, 0x2000
	s_add_u32 s24, s24, 0x80080
	v_lshl_add_u64 v[218:219], v[220:221], 0, s[0:1]
	s_addc_u32 s25, s25, 0
	s_add_i32 s28, s53, s38
	global_load_lds_dwordx4 v[218:219], off
	v_lshl_add_u64 v[218:219], s[24:25], 0, v[138:139]
	s_mov_b32 m0, s28
	s_nop 0
	global_load_lds_dwordx4 v[218:219], off
	v_lshl_add_u64 v[218:219], s[24:25], 0, v[134:135]
	s_add_i32 m0, s28, 0x2000
	s_nop 0
	global_load_lds_dwordx4 v[218:219], off
	v_lshl_add_u64 v[218:219], v[222:223], 0, s[0:1]
	s_mov_b32 m0, s44
	s_nop 0
	global_load_lds_dwordx4 v[218:219], off
	v_lshl_add_u64 v[218:219], v[224:225], 0, s[0:1]
	s_mov_b32 m0, s45
	s_nop 0
	global_load_lds_dwordx4 v[218:219], off
	s_waitcnt vmcnt(8)
	s_waitcnt lgkmcnt(0)
	s_barrier
	v_mfma_f32_16x16x32_bf16 v[50:53], v[152:155], v[184:187], v[50:53]
	v_mfma_f32_16x16x32_bf16 v[82:85], v[160:163], v[184:187], v[82:85]
	v_mfma_f32_16x16x32_bf16 v[46:49], v[152:155], v[192:195], v[46:49]
	v_mfma_f32_16x16x32_bf16 v[78:81], v[160:163], v[192:195], v[78:81]
	v_mfma_f32_16x16x32_bf16 v[42:45], v[152:155], v[202:205], v[42:45]
	v_mfma_f32_16x16x32_bf16 v[74:77], v[160:163], v[202:205], v[74:77]
	v_mfma_f32_16x16x32_bf16 v[38:41], v[152:155], v[210:213], v[38:41]
	v_mfma_f32_16x16x32_bf16 v[70:73], v[160:163], v[210:213], v[70:73]
	v_mfma_f32_16x16x32_bf16 v[50:53], v[156:159], v[188:191], v[50:53]
	v_mfma_f32_16x16x32_bf16 v[82:85], v[164:167], v[188:191], v[82:85]
	v_mfma_f32_16x16x32_bf16 v[46:49], v[156:159], v[196:199], v[46:49]
	v_mfma_f32_16x16x32_bf16 v[78:81], v[164:167], v[196:199], v[78:81]
	v_mfma_f32_16x16x32_bf16 v[42:45], v[156:159], v[206:209], v[42:45]
	v_mfma_f32_16x16x32_bf16 v[74:77], v[164:167], v[206:209], v[74:77]
	v_mfma_f32_16x16x32_bf16 v[38:41], v[156:159], v[214:217], v[38:41]
	v_mfma_f32_16x16x32_bf16 v[70:73], v[164:167], v[214:217], v[70:73]
	v_mfma_f32_16x16x32_bf16 v[114:117], v[168:171], v[184:187], v[114:117]
	v_mfma_f32_16x16x32_bf16 v[130:133], v[176:179], v[184:187], v[130:133]
	v_mfma_f32_16x16x32_bf16 v[110:113], v[168:171], v[192:195], v[110:113]
	v_mfma_f32_16x16x32_bf16 v[126:129], v[176:179], v[192:195], v[126:129]
	v_mfma_f32_16x16x32_bf16 v[106:109], v[168:171], v[202:205], v[106:109]
	v_mfma_f32_16x16x32_bf16 v[122:125], v[176:179], v[202:205], v[122:125]
	v_mfma_f32_16x16x32_bf16 v[102:105], v[168:171], v[210:213], v[102:105]
	v_mfma_f32_16x16x32_bf16 v[118:121], v[176:179], v[210:213], v[118:121]
	v_mfma_f32_16x16x32_bf16 v[114:117], v[172:175], v[188:191], v[114:117]
	v_mfma_f32_16x16x32_bf16 v[130:133], v[180:183], v[188:191], v[130:133]
	v_mfma_f32_16x16x32_bf16 v[110:113], v[172:175], v[196:199], v[110:113]
	v_mfma_f32_16x16x32_bf16 v[126:129], v[180:183], v[196:199], v[126:129]
	v_mfma_f32_16x16x32_bf16 v[106:109], v[172:175], v[206:209], v[106:109]
	v_mfma_f32_16x16x32_bf16 v[122:125], v[180:183], v[206:209], v[122:125]
	v_mfma_f32_16x16x32_bf16 v[102:105], v[172:175], v[214:217], v[102:105]
	v_mfma_f32_16x16x32_bf16 v[118:121], v[180:183], v[214:217], v[118:121]
	s_barrier
	s_add_i32 s51, s51, 2
	s_cmp_gt_u32 s51, 29
	s_mov_b64 s[28:29], s[22:23]
	s_cbranch_scc0 .LBB0_247

; template <class Epi, class Sched, bool GATHER = false>
; __device__ __forceinline__ void gemm_phase(LAS unsigned char* lds, const Gemm g, const Sched& S, const Epi& E, const int tid) {
;     ...
;         const bool has_next = S.next(ui + 1, nxt);
;         const char* nA = has_next ? (const char*)g.A + (size_t)nxt.pm * tstep : cA; const char* nB = has_next ? (const char*)g.Bt + (size_t)nxt.pb * tstep : cB;
;         if (GATHER && has_next && wid < 4) __builtin_amdgcn_global_load_lds((const unsigned*)(g.rowmap + nxt.rb + tid), (LAS unsigned*)(lds + STAGE_BYTES + ((ui + 1) & 1) * 1024 + wid * 256), 4, 0, 0);
;         for (int t = 0; t < nt; t += 2) {
;             const bool last = (t == nt - 2);
;             const char* a1 = cA + (size_t)(t + 1) * kstep;
;             const char* a2 = last ? nA : cA + (size_t)(t + 2) * kstep; const char* b2 = last ? nB : cB + (size_t)(t + 2) * kstep;
;             const char* a3 = a2 + kstep; const char* b3 = b2 + kstep;
;     ...
;             PG8_LDB(B0, 0, 0); PG8_SCHED; PG8_LDA(At, 0, 0); PG8_STAGE(PG8_SA(1, 1), a1 + hstep, voffA);
;             PG8_WAIT_L(8); PG8_BAR; PG8_WAIT_L(0); PG8_MMA(0, 0, At, B0); PG8_BAR; PG8_SCHED;
;             PG8_LDB(B1, 0, 1); PG8_STAGE(PG8_SB(0, 0), b2, voffB);
;             PG8_BAR; PG8_WAIT_L(0); PG8_MMA(0, 1, At, B1); PG8_BAR;
;             PG8_LDA(At, 0, 1); PG8_STAGE(PG8_SA(0, 0), a2, voffA);
;             PG8_BAR; PG8_WAIT_L(0); PG8_MMA(1, 0, At, B0); PG8_BAR; PG8_SCHED;
;             PG8_STAGE(PG8_SB(0, 1), b2 + hstep, voffB);
;             PG8_WAIT_V(6); PG8_BAR; PG8_MMA(1, 1, At, B1); PG8_BAR;
;             PG8_LDB(B0, 1, 0); PG8_SCHED; PG8_LDA(At, 1, 0); PG8_STAGE(PG8_SA(0, 1), a2 + hstep, voffA);
;             PG8_WAIT_L(8); PG8_BAR; PG8_WAIT_L(0); PG8_MMA(0, 0, At, B0); PG8_BAR; PG8_SCHED;
;             PG8_LDB(B1, 1, 1); PG8_STAGE(PG8_SB(1, 0), b3, voffB);
;             PG8_BAR; PG8_WAIT_L(0); PG8_MMA(0, 1, At, B1); PG8_BAR;
;             PG8_LDA(At, 1, 1); PG8_STAGE(PG8_SA(1, 0), a3, voffA);
;             PG8_BAR; PG8_WAIT_L(0); PG8_MMA(1, 0, At, B0); PG8_BAR; PG8_SCHED;
;             PG8_STAGE(PG8_SB(1, 1), b3 + hstep, voffB);
;             PG8_WAIT_V(6); PG8_BAR; PG8_MMA(1, 1, At, B1); PG8_BAR;
;     ...
;             if (GATHER && last && has_next) {
;                 const LAS int* ib_ = (const LAS int*)(lds + STAGE_BYTES + ((ui + 1) & 1) * 1024);
; #pragma unroll
.LBB0_1127:
	s_ashr_i32 s17, s16, 31
	s_lshl_b64 s[18:19], s[16:17], 20
	s_add_u32 s18, s34, s18
	s_addc_u32 s19, s35, s19
	s_ashr_i32 s15, s14, 31
	s_lshl_b64 s[20:21], s[14:15], 20
	s_add_u32 s20, s36, s20
	s_addc_u32 s21, s37, s21
	s_and_b64 s[24:25], s[4:5], exec
	s_cselect_b32 s15, s21, s23
	s_cselect_b32 s17, s20, s22
	s_add_u32 s47, s22, 0x100
	s_addc_u32 s48, s23, 0
	s_add_u32 s22, s10, 0x80080
	s_addc_u32 s23, s11, 0
	v_lshl_add_u64 v[4:5], s[22:23], 0, v[142:143]
	v_lshl_add_u64 v[146:147], s[22:23], 0, v[144:145]
	s_mov_b32 s49, -2
	s_mov_b64 s[28:29], 0
	s_add_u32 s22, s28, 0x100
	s_addc_u32 s23, s29, 0
	s_add_u32 s52, s47, s28
	s_addc_u32 s53, s48, s29
	s_add_i32 s24, 0, 0x10000
	s_add_i32 s54, 0, 0x14000
	v_add_u32_e32 v2, s24, v148
	ds_read_b128 v[152:155], v2
	ds_read_b128 v[156:159], v2 offset:1024
	ds_read_b128 v[160:163], v2 offset:2048
	ds_read_b128 v[164:167], v2 offset:3072
	v_add_u32_e32 v2, s54, v148
	ds_read_b128 v[168:171], v2
	ds_read_b128 v[172:175], v2 offset:1024
	ds_read_b128 v[176:179], v2 offset:2048
	ds_read_b128 v[180:183], v2 offset:3072
	s_add_i32 s56, s24, s33
	s_add_i32 m0, s9, 0xc000
	s_add_i32 s55, s9, 0xe000
	s_add_i32 s57, s56, 0x2000
	s_cmp_eq_u32 s49, 28
	s_cselect_b64 s[50:51], -1, 0
	s_and_b64 s[24:25], s[50:51], exec
	s_cselect_b32 s25, s15, s53
	s_cselect_b32 s24, s17, s52
	v_lshl_add_u64 v[218:219], v[4:5], 0, s[28:29]
	ds_read_b128 v[184:187], v150
	ds_read_b128 v[188:191], v150 offset:1024
	ds_read_b128 v[192:195], v150 offset:2048
	ds_read_b128 v[196:199], v150 offset:3072
	ds_read_b128 v[202:205], v150 offset:4096
	ds_read_b128 v[206:209], v150 offset:5120
	ds_read_b128 v[210:213], v150 offset:6144
	ds_read_b128 v[214:217], v150 offset:7168
	global_load_lds_dwordx4 v[218:219], off
	v_lshl_add_u64 v[218:219], v[146:147], 0, s[28:29]
	s_mov_b32 m0, s55
	s_nop 0
	global_load_lds_dwordx4 v[218:219], off
	s_waitcnt vmcnt(8)
	s_waitcnt lgkmcnt(0)
	s_barrier
	v_mfma_f32_16x16x32_bf16 v[86:89], v[152:155], v[184:187], 0
	v_mfma_f32_16x16x32_bf16 v[18:21], v[160:163], v[184:187], 0
	v_mfma_f32_16x16x32_bf16 v[6:9], v[152:155], v[192:195], 0
	v_mfma_f32_16x16x32_bf16 v[22:25], v[160:163], v[192:195], 0
	v_mfma_f32_16x16x32_bf16 v[10:13], v[152:155], v[202:205], 0
	v_mfma_f32_16x16x32_bf16 v[26:29], v[160:163], v[202:205], 0
	v_mfma_f32_16x16x32_bf16 v[14:17], v[152:155], v[210:213], 0
	v_mfma_f32_16x16x32_bf16 v[30:33], v[160:163], v[210:213], 0
	v_mfma_f32_16x16x32_bf16 v[86:89], v[156:159], v[188:191], v[86:89]
	v_mfma_f32_16x16x32_bf16 v[18:21], v[164:167], v[188:191], v[18:21]
	v_mfma_f32_16x16x32_bf16 v[6:9], v[156:159], v[196:199], v[6:9]
	v_mfma_f32_16x16x32_bf16 v[22:25], v[164:167], v[196:199], v[22:25]
	v_mfma_f32_16x16x32_bf16 v[10:13], v[156:159], v[206:209], v[10:13]
	v_mfma_f32_16x16x32_bf16 v[26:29], v[164:167], v[206:209], v[26:29]
	v_mfma_f32_16x16x32_bf16 v[14:17], v[156:159], v[214:217], v[14:17]
	v_mfma_f32_16x16x32_bf16 v[30:33], v[164:167], v[214:217], v[30:33]
	v_mfma_f32_16x16x32_bf16 v[34:37], v[168:171], v[184:187], 0
	v_mfma_f32_16x16x32_bf16 v[50:53], v[176:179], v[184:187], 0
	v_mfma_f32_16x16x32_bf16 v[38:41], v[168:171], v[192:195], 0
	v_mfma_f32_16x16x32_bf16 v[58:61], v[176:179], v[192:195], 0
	v_mfma_f32_16x16x32_bf16 v[42:45], v[168:171], v[202:205], 0
	v_mfma_f32_16x16x32_bf16 v[66:69], v[176:179], v[202:205], 0
	v_mfma_f32_16x16x32_bf16 v[46:49], v[168:171], v[210:213], 0
	v_mfma_f32_16x16x32_bf16 v[74:77], v[176:179], v[210:213], 0
	v_mfma_f32_16x16x32_bf16 v[34:37], v[172:175], v[188:191], v[34:37]
	v_mfma_f32_16x16x32_bf16 v[50:53], v[180:183], v[188:191], v[50:53]
	v_mfma_f32_16x16x32_bf16 v[38:41], v[172:175], v[196:199], v[38:41]
	v_mfma_f32_16x16x32_bf16 v[58:61], v[180:183], v[196:199], v[58:61]
	v_mfma_f32_16x16x32_bf16 v[42:45], v[172:175], v[206:209], v[42:45]
	v_mfma_f32_16x16x32_bf16 v[66:69], v[180:183], v[206:209], v[66:69]
	v_mfma_f32_16x16x32_bf16 v[46:49], v[172:175], v[214:217], v[46:49]
	v_mfma_f32_16x16x32_bf16 v[74:77], v[180:183], v[214:217], v[74:77]
	s_barrier
	s_mov_b32 m0, s56
	v_lshl_add_u64 v[218:219], s[24:25], 0, v[136:137]
	s_cselect_b32 s52, 0, s23
	s_cselect_b32 s53, 0, s22
	s_add_u32 s28, s24, 0x80000
	ds_read_b128 v[184:187], v150 offset:16384
	ds_read_b128 v[188:191], v150 offset:17408
	ds_read_b128 v[192:195], v150 offset:18432
	ds_read_b128 v[196:199], v150 offset:19456
	ds_read_b128 v[202:205], v150 offset:20480
	ds_read_b128 v[206:209], v150 offset:21504
	ds_read_b128 v[210:213], v150 offset:22528
	ds_read_b128 v[214:217], v150 offset:23552
	global_load_lds_dwordx4 v[218:219], off
	v_lshl_add_u64 v[220:221], s[24:25], 0, v[140:141]
	s_mov_b32 m0, s57
	s_addc_u32 s29, s25, 0
	s_add_i32 s54, s54, s33
	global_load_lds_dwordx4 v[220:221], off
	v_lshl_add_u64 v[222:223], s[28:29], 0, v[136:137]
	s_mov_b32 m0, s54
	s_nop 0
	global_load_lds_dwordx4 v[222:223], off
	v_lshl_add_u64 v[222:223], s[28:29], 0, v[140:141]
	s_add_i32 m0, s54, 0x2000
	s_and_b64 s[28:29], s[50:51], s[4:5]
	s_and_b64 s[28:29], s[28:29], exec
	s_cselect_b32 s28, s18, s10
	s_cselect_b32 s29, s19, s11
	s_add_u32 s28, s28, s53
	s_addc_u32 s29, s29, s52
	global_load_lds_dwordx4 v[222:223], off
	v_lshl_add_u64 v[222:223], s[28:29], 0, v[134:135]
	s_mov_b32 m0, s9
	v_lshl_add_u64 v[224:225], s[28:29], 0, v[138:139]
	global_load_lds_dwordx4 v[222:223], off
	s_mov_b32 m0, s38
	s_nop 0
	global_load_lds_dwordx4 v[224:225], off
	s_waitcnt vmcnt(8)
	s_waitcnt lgkmcnt(0)
	s_barrier
; #define PG8_STAGE_A(bufoff, base_, nx_, kb_, h_) do { if (GATHER) { if (nx_) PG8_STAGE_G(bufoff, kb_, goN, h_); else PG8_STAGE_G(bufoff, kb_, goC, h_); } \
;         else PG8_STAGE(bufoff, (base_) + (kb_) + (h_) * hstep, voffA); } while (0)
; #define PG8_STAGE(bufoff, gbase, voff) do { _Pragma("unroll") for (int _i = 0; _i < 2; ++_i) \
;         __builtin_amdgcn_global_load_lds((const unsigned*)((const char*)(gbase) + (voff)[_i]), (LAS unsigned*)(lds + (bufoff) + ldsw + _i * 8192), 16, 0, 0); } while (0)
; #define PG8_LDA(dst, b, h) do { _Pragma("unroll") for (int m = 0; m < 4; ++m) _Pragma("unroll") for (int k = 0; k < 2; ++k) dst[m][k] = *(const LAS bf16x8*)(lds + PG8_SA(b, h) + aoff + m * 2048 + k * 1024); } while (0)
; #define PG8_LDB(dst, b, h) do { _Pragma("unroll") for (int n = 0; n < 2; ++n) _Pragma("unroll") for (int k = 0; k < 2; ++k) dst[n][k] = *(const LAS bf16x8*)(lds + PG8_SB(b, h) + boff + n * 2048 + k * 1024); } while (0)
; #define PG8_WAIT_V(n) asm volatile("s_waitcnt vmcnt(" #n ")" ::: "memory")
; #define PG8_WAIT_L(n) asm volatile("s_waitcnt lgkmcnt(" #n ")" ::: "memory")
; template <class Epi, class Sched, bool GATHER = false>
; __device__ __forceinline__ void gemm_phase(LAS unsigned char* lds, const Gemm g, const Sched& S, const Epi& E, const int tid) {
;     ...
;             PG8_LDB(B0, 0, 0); PG8_LDB(B1, 0, 1); PG8_SCHED; PG8_LDA(At, 0, 0); PG8_STAGE_A(PG8_SA(1, 1), cA, false, kb1, 1);
;             PG8_WAIT_V(8); PG8_WAIT_L(0); PG8_BAR; PG8_MMA(0, 0, At, B0); PG8_MMA(0, 1, At, B1); PG8_BAR; PG8_SCHED;
;             PG8_LDA(At, 0, 1); PG8_STAGE(PG8_SB(0, 0), b2, voffB); PG8_STAGE(PG8_SB(0, 1), b2 + hstep, voffB); PG8_STAGE_A(PG8_SA(0, 0), (last ? nA : cA), last, kb2, 0);
;             PG8_WAIT_V(8); PG8_WAIT_L(0); PG8_BAR; PG8_MMA(1, 0, At, B0); PG8_MMA(1, 1, At, B1); PG8_BAR; PG8_SCHED;
;             PG8_LDB(B0, 1, 0); PG8_LDB(B1, 1, 1); PG8_SCHED; PG8_LDA(At, 1, 0); PG8_STAGE_A(PG8_SA(0, 1), (last ? nA : cA), last, kb2, 1);
;             PG8_WAIT_V(8); PG8_WAIT_L(0); PG8_BAR; PG8_MMA(0, 0, At, B0); PG8_MMA(0, 1, At, B1); PG8_BAR; PG8_SCHED;
;             PG8_LDA(At, 1, 1); PG8_STAGE(PG8_SB(1, 0), b3, voffB); PG8_STAGE(PG8_SB(1, 1), b3 + hstep, voffB); PG8_STAGE_A(PG8_SA(1, 0), (last ? nA : cA), last, kb3, 0);
;             PG8_WAIT_V(8); PG8_WAIT_L(0); PG8_BAR; PG8_MMA(1, 0, At, B0); PG8_MMA(1, 1, At, B1); PG8_BAR; PG8_SCHED;
	v_mfma_f32_16x16x32_bf16 v[54:57], v[152:155], v[184:187], 0
	v_mfma_f32_16x16x32_bf16 v[78:81], v[160:163], v[184:187], 0
	v_mfma_f32_16x16x32_bf16 v[62:65], v[152:155], v[192:195], 0
	v_mfma_f32_16x16x32_bf16 v[82:85], v[160:163], v[192:195], 0
	v_mfma_f32_16x16x32_bf16 v[70:73], v[152:155], v[202:205], 0
	v_mfma_f32_16x16x32_bf16 v[98:101], v[160:163], v[202:205], 0
	v_mfma_f32_16x16x32_bf16 v[90:93], v[152:155], v[210:213], 0
	v_mfma_f32_16x16x32_bf16 v[94:97], v[160:163], v[210:213], 0
	v_mfma_f32_16x16x32_bf16 v[54:57], v[156:159], v[188:191], v[54:57]
	v_mfma_f32_16x16x32_bf16 v[78:81], v[164:167], v[188:191], v[78:81]
	v_mfma_f32_16x16x32_bf16 v[62:65], v[156:159], v[196:199], v[62:65]
	v_mfma_f32_16x16x32_bf16 v[82:85], v[164:167], v[196:199], v[82:85]
	v_mfma_f32_16x16x32_bf16 v[70:73], v[156:159], v[206:209], v[70:73]
	v_mfma_f32_16x16x32_bf16 v[98:101], v[164:167], v[206:209], v[98:101]
	v_mfma_f32_16x16x32_bf16 v[90:93], v[156:159], v[214:217], v[90:93]
	v_mfma_f32_16x16x32_bf16 v[94:97], v[164:167], v[214:217], v[94:97]
	v_mfma_f32_16x16x32_bf16 v[114:117], v[168:171], v[184:187], 0
	v_mfma_f32_16x16x32_bf16 v[130:133], v[176:179], v[184:187], 0
	v_mfma_f32_16x16x32_bf16 v[110:113], v[168:171], v[192:195], 0
	v_mfma_f32_16x16x32_bf16 v[126:129], v[176:179], v[192:195], 0
	v_mfma_f32_16x16x32_bf16 v[106:109], v[168:171], v[202:205], 0
	v_mfma_f32_16x16x32_bf16 v[122:125], v[176:179], v[202:205], 0
	v_mfma_f32_16x16x32_bf16 v[102:105], v[168:171], v[210:213], 0
	v_mfma_f32_16x16x32_bf16 v[118:121], v[176:179], v[210:213], 0
	v_mfma_f32_16x16x32_bf16 v[114:117], v[172:175], v[188:191], v[114:117]
	v_mfma_f32_16x16x32_bf16 v[130:133], v[180:183], v[188:191], v[130:133]
	v_mfma_f32_16x16x32_bf16 v[110:113], v[172:175], v[196:199], v[110:113]
	v_mfma_f32_16x16x32_bf16 v[126:129], v[180:183], v[196:199], v[126:129]
	v_mfma_f32_16x16x32_bf16 v[106:109], v[172:175], v[206:209], v[106:109]
	v_mfma_f32_16x16x32_bf16 v[122:125], v[180:183], v[206:209], v[122:125]
	v_mfma_f32_16x16x32_bf16 v[102:105], v[172:175], v[214:217], v[102:105]
	v_mfma_f32_16x16x32_bf16 v[118:121], v[180:183], v[214:217], v[118:121]
	s_barrier
	s_add_i32 s50, 0, 0x18000
	v_add_u32_e32 v2, s50, v148
	s_add_i32 s51, 0, 0x1c000
	ds_read_b128 v[152:155], v2
	ds_read_b128 v[156:159], v2 offset:1024
	ds_read_b128 v[160:163], v2 offset:2048
	ds_read_b128 v[164:167], v2 offset:3072
	v_add_u32_e32 v2, s51, v148
	ds_read_b128 v[168:171], v2
	ds_read_b128 v[172:175], v2 offset:1024
	ds_read_b128 v[176:179], v2 offset:2048
	ds_read_b128 v[180:183], v2 offset:3072
	s_add_u32 s28, s28, 0x80000
	s_addc_u32 s29, s29, 0
	s_mov_b32 m0, s39
	v_lshl_add_u64 v[226:227], s[28:29], 0, v[134:135]
	ds_read_b128 v[184:187], v150 offset:32768
	ds_read_b128 v[188:191], v150 offset:33792
	ds_read_b128 v[192:195], v150 offset:34816
	ds_read_b128 v[196:199], v150 offset:35840
	ds_read_b128 v[202:205], v150 offset:36864
	ds_read_b128 v[206:209], v150 offset:37888
	ds_read_b128 v[210:213], v150 offset:38912
	ds_read_b128 v[214:217], v150 offset:39936
	global_load_lds_dwordx4 v[226:227], off
	v_lshl_add_u64 v[226:227], s[28:29], 0, v[138:139]
	s_mov_b32 m0, s40
	s_nop 0
	global_load_lds_dwordx4 v[226:227], off
	s_waitcnt vmcnt(8)
	s_waitcnt lgkmcnt(0)
	s_barrier
	v_mfma_f32_16x16x32_bf16 v[86:89], v[152:155], v[184:187], v[86:89]
	v_mfma_f32_16x16x32_bf16 v[18:21], v[160:163], v[184:187], v[18:21]
	v_mfma_f32_16x16x32_bf16 v[6:9], v[152:155], v[192:195], v[6:9]
	v_mfma_f32_16x16x32_bf16 v[22:25], v[160:163], v[192:195], v[22:25]
	v_mfma_f32_16x16x32_bf16 v[10:13], v[152:155], v[202:205], v[10:13]
	v_mfma_f32_16x16x32_bf16 v[26:29], v[160:163], v[202:205], v[26:29]
	v_mfma_f32_16x16x32_bf16 v[14:17], v[152:155], v[210:213], v[14:17]
	v_mfma_f32_16x16x32_bf16 v[30:33], v[160:163], v[210:213], v[30:33]
	v_mfma_f32_16x16x32_bf16 v[86:89], v[156:159], v[188:191], v[86:89]
	v_mfma_f32_16x16x32_bf16 v[18:21], v[164:167], v[188:191], v[18:21]
	v_mfma_f32_16x16x32_bf16 v[6:9], v[156:159], v[196:199], v[6:9]
	v_mfma_f32_16x16x32_bf16 v[22:25], v[164:167], v[196:199], v[22:25]
	v_mfma_f32_16x16x32_bf16 v[10:13], v[156:159], v[206:209], v[10:13]
	v_mfma_f32_16x16x32_bf16 v[26:29], v[164:167], v[206:209], v[26:29]
	v_mfma_f32_16x16x32_bf16 v[14:17], v[156:159], v[214:217], v[14:17]
	v_mfma_f32_16x16x32_bf16 v[30:33], v[164:167], v[214:217], v[30:33]
	v_mfma_f32_16x16x32_bf16 v[34:37], v[168:171], v[184:187], v[34:37]
	v_mfma_f32_16x16x32_bf16 v[50:53], v[176:179], v[184:187], v[50:53]
	v_mfma_f32_16x16x32_bf16 v[38:41], v[168:171], v[192:195], v[38:41]
	v_mfma_f32_16x16x32_bf16 v[58:61], v[176:179], v[192:195], v[58:61]
	v_mfma_f32_16x16x32_bf16 v[42:45], v[168:171], v[202:205], v[42:45]
	v_mfma_f32_16x16x32_bf16 v[66:69], v[176:179], v[202:205], v[66:69]
	v_mfma_f32_16x16x32_bf16 v[46:49], v[168:171], v[210:213], v[46:49]
	v_mfma_f32_16x16x32_bf16 v[74:77], v[176:179], v[210:213], v[74:77]
	v_mfma_f32_16x16x32_bf16 v[34:37], v[172:175], v[188:191], v[34:37]
	v_mfma_f32_16x16x32_bf16 v[50:53], v[180:183], v[188:191], v[50:53]
	v_mfma_f32_16x16x32_bf16 v[38:41], v[172:175], v[196:199], v[38:41]
	v_mfma_f32_16x16x32_bf16 v[58:61], v[180:183], v[196:199], v[58:61]
	v_mfma_f32_16x16x32_bf16 v[42:45], v[172:175], v[206:209], v[42:45]
	v_mfma_f32_16x16x32_bf16 v[66:69], v[180:183], v[206:209], v[66:69]
	v_mfma_f32_16x16x32_bf16 v[46:49], v[172:175], v[214:217], v[46:49]
	v_mfma_f32_16x16x32_bf16 v[74:77], v[180:183], v[214:217], v[74:77]
	s_barrier
; #define PG8_STAGE_A(bufoff, base_, nx_, kb_, h_) do { if (GATHER) { if (nx_) PG8_STAGE_G(bufoff, kb_, goN, h_); else PG8_STAGE_G(bufoff, kb_, goC, h_); } \
;         else PG8_STAGE(bufoff, (base_) + (kb_) + (h_) * hstep, voffA); } while (0)
; #define PG8_STAGE(bufoff, gbase, voff) do { _Pragma("unroll") for (int _i = 0; _i < 2; ++_i) \
;         __builtin_amdgcn_global_load_lds((const unsigned*)((const char*)(gbase) + (voff)[_i]), (LAS unsigned*)(lds + (bufoff) + ldsw + _i * 8192), 16, 0, 0); } while (0)
; #define PG8_LDA(dst, b, h) do { _Pragma("unroll") for (int m = 0; m < 4; ++m) _Pragma("unroll") for (int k = 0; k < 2; ++k) dst[m][k] = *(const LAS bf16x8*)(lds + PG8_SA(b, h) + aoff + m * 2048 + k * 1024); } while (0)
; #define PG8_MMA(ai, bj, At, Bt) do { __builtin_amdgcn_s_setprio(1); _Pragma("unroll") for (int m = 0; m < 4; ++m) _Pragma("unroll") for (int n = 0; n < 2; ++n) _Pragma("unroll") for (int k = 0; k < 2; ++k) \
;         acc[ai][bj][m][n] = __builtin_amdgcn_mfma_f32_16x16x32_bf16(Bt[n][k], At[m][k], acc[ai][bj][m][n], 0, 0, 0); __builtin_amdgcn_s_setprio(0); } while (0)
; #define PG8_WAIT_V(n) asm volatile("s_waitcnt vmcnt(" #n ")" ::: "memory")
; #define PG8_WAIT_L(n) asm volatile("s_waitcnt lgkmcnt(" #n ")" ::: "memory")
; #define PG8_BAR __builtin_amdgcn_s_barrier()
; #define PG8_SCHED __builtin_amdgcn_sched_barrier(0)
; template <class Epi, class Sched, bool GATHER = false>
; __device__ __forceinline__ void gemm_phase(LAS unsigned char* lds, const Gemm g, const Sched& S, const Epi& E, const int tid) {
;     ...
;         for (int t = 0; t < nt; t += 2) {
;             const bool last = (t == nt - 2);
;             const char* a1 = cA + (size_t)(t + 1) * kstep;
;             const char* a2 = last ? nA : cA + (size_t)(t + 2) * kstep; const char* b2 = last ? nB : cB + (size_t)(t + 2) * kstep;
;             const char* a3 = a2 + kstep; const char* b3 = b2 + kstep;
;     ...
;             PG8_LDA(At, 1, 1); PG8_STAGE(PG8_SB(1, 0), b3, voffB); PG8_STAGE(PG8_SB(1, 1), b3 + hstep, voffB); PG8_STAGE_A(PG8_SA(1, 0), (last ? nA : cA), last, kb3, 0);
;             PG8_WAIT_V(8); PG8_WAIT_L(0); PG8_BAR; PG8_MMA(1, 0, At, B0); PG8_MMA(1, 1, At, B1); PG8_BAR; PG8_SCHED;
	s_add_i32 s28, s50, s33
	v_lshl_add_u64 v[218:219], v[218:219], 0, s[0:1]
	s_mov_b32 m0, s28
	ds_read_b128 v[184:187], v150 offset:49152
	ds_read_b128 v[188:191], v150 offset:50176
	ds_read_b128 v[192:195], v150 offset:51200
	ds_read_b128 v[196:199], v150 offset:52224
	ds_read_b128 v[202:205], v150 offset:53248
	ds_read_b128 v[206:209], v150 offset:54272
	ds_read_b128 v[210:213], v150 offset:55296
	ds_read_b128 v[214:217], v150 offset:56320
	global_load_lds_dwordx4 v[218:219], off
	s_add_i32 m0, s28, 0x2000
	s_add_u32 s24, s24, 0x80080
	v_lshl_add_u64 v[218:219], v[220:221], 0, s[0:1]
	s_addc_u32 s25, s25, 0
	s_add_i32 s28, s51, s33
	global_load_lds_dwordx4 v[218:219], off
	v_lshl_add_u64 v[218:219], s[24:25], 0, v[136:137]
	s_mov_b32 m0, s28
	s_nop 0
	global_load_lds_dwordx4 v[218:219], off
	v_lshl_add_u64 v[218:219], s[24:25], 0, v[140:141]
	s_add_i32 m0, s28, 0x2000
	s_nop 0
	global_load_lds_dwordx4 v[218:219], off
	v_lshl_add_u64 v[218:219], v[222:223], 0, s[0:1]
	s_mov_b32 m0, s42
	s_nop 0
	global_load_lds_dwordx4 v[218:219], off
	v_lshl_add_u64 v[218:219], v[224:225], 0, s[0:1]
	s_mov_b32 m0, s43
	s_nop 0
	global_load_lds_dwordx4 v[218:219], off
	s_waitcnt vmcnt(8)
	s_waitcnt lgkmcnt(0)
	s_barrier
	v_mfma_f32_16x16x32_bf16 v[54:57], v[152:155], v[184:187], v[54:57]
	v_mfma_f32_16x16x32_bf16 v[78:81], v[160:163], v[184:187], v[78:81]
	v_mfma_f32_16x16x32_bf16 v[62:65], v[152:155], v[192:195], v[62:65]
	v_mfma_f32_16x16x32_bf16 v[82:85], v[160:163], v[192:195], v[82:85]
	v_mfma_f32_16x16x32_bf16 v[70:73], v[152:155], v[202:205], v[70:73]
	v_mfma_f32_16x16x32_bf16 v[98:101], v[160:163], v[202:205], v[98:101]
	v_mfma_f32_16x16x32_bf16 v[90:93], v[152:155], v[210:213], v[90:93]
	v_mfma_f32_16x16x32_bf16 v[94:97], v[160:163], v[210:213], v[94:97]
	v_mfma_f32_16x16x32_bf16 v[54:57], v[156:159], v[188:191], v[54:57]
	v_mfma_f32_16x16x32_bf16 v[78:81], v[164:167], v[188:191], v[78:81]
	v_mfma_f32_16x16x32_bf16 v[62:65], v[156:159], v[196:199], v[62:65]
	v_mfma_f32_16x16x32_bf16 v[82:85], v[164:167], v[196:199], v[82:85]
	v_mfma_f32_16x16x32_bf16 v[70:73], v[156:159], v[206:209], v[70:73]
	v_mfma_f32_16x16x32_bf16 v[98:101], v[164:167], v[206:209], v[98:101]
	v_mfma_f32_16x16x32_bf16 v[90:93], v[156:159], v[214:217], v[90:93]
	v_mfma_f32_16x16x32_bf16 v[94:97], v[164:167], v[214:217], v[94:97]
	v_mfma_f32_16x16x32_bf16 v[114:117], v[168:171], v[184:187], v[114:117]
	v_mfma_f32_16x16x32_bf16 v[130:133], v[176:179], v[184:187], v[130:133]
	v_mfma_f32_16x16x32_bf16 v[110:113], v[168:171], v[192:195], v[110:113]
	v_mfma_f32_16x16x32_bf16 v[126:129], v[176:179], v[192:195], v[126:129]
	v_mfma_f32_16x16x32_bf16 v[106:109], v[168:171], v[202:205], v[106:109]
	v_mfma_f32_16x16x32_bf16 v[122:125], v[176:179], v[202:205], v[122:125]
	v_mfma_f32_16x16x32_bf16 v[102:105], v[168:171], v[210:213], v[102:105]
	v_mfma_f32_16x16x32_bf16 v[118:121], v[176:179], v[210:213], v[118:121]
	v_mfma_f32_16x16x32_bf16 v[114:117], v[172:175], v[188:191], v[114:117]
	v_mfma_f32_16x16x32_bf16 v[130:133], v[180:183], v[188:191], v[130:133]
	v_mfma_f32_16x16x32_bf16 v[110:113], v[172:175], v[196:199], v[110:113]
	v_mfma_f32_16x16x32_bf16 v[126:129], v[180:183], v[196:199], v[126:129]
	v_mfma_f32_16x16x32_bf16 v[106:109], v[172:175], v[206:209], v[106:109]
	v_mfma_f32_16x16x32_bf16 v[122:125], v[180:183], v[206:209], v[122:125]
	v_mfma_f32_16x16x32_bf16 v[102:105], v[172:175], v[214:217], v[102:105]
	v_mfma_f32_16x16x32_bf16 v[118:121], v[180:183], v[214:217], v[118:121]
	s_barrier
	s_add_i32 s49, s49, 2
	s_cmp_gt_u32 s49, 29
	s_mov_b64 s[28:29], s[22:23]
	s_cbranch_scc1 .Lpeel1_exit
.LBB0_1128:
	s_add_u32 s22, s28, 0x100
	s_addc_u32 s23, s29, 0
	s_add_u32 s52, s47, s28
	s_addc_u32 s53, s48, s29
	s_add_i32 s24, 0, 0x10000
	s_add_i32 s54, 0, 0x14000
	v_add_u32_e32 v2, s24, v148
	ds_read_b128 v[152:155], v2
	ds_read_b128 v[156:159], v2 offset:1024
	ds_read_b128 v[160:163], v2 offset:2048
	ds_read_b128 v[164:167], v2 offset:3072
	v_add_u32_e32 v2, s54, v148
	ds_read_b128 v[168:171], v2
	ds_read_b128 v[172:175], v2 offset:1024
	ds_read_b128 v[176:179], v2 offset:2048
	ds_read_b128 v[180:183], v2 offset:3072
	s_add_i32 s56, s24, s33
	s_add_i32 m0, s9, 0xc000
	s_add_i32 s55, s9, 0xe000
	s_add_i32 s57, s56, 0x2000
	s_cmp_eq_u32 s49, 28
	s_cselect_b64 s[50:51], -1, 0
	s_and_b64 s[24:25], s[50:51], exec
	s_cselect_b32 s25, s15, s53
	s_cselect_b32 s24, s17, s52
	v_lshl_add_u64 v[218:219], v[4:5], 0, s[28:29]
	ds_read_b128 v[184:187], v150
	ds_read_b128 v[188:191], v150 offset:1024
	ds_read_b128 v[192:195], v150 offset:2048
	ds_read_b128 v[196:199], v150 offset:3072
	ds_read_b128 v[202:205], v150 offset:4096
	ds_read_b128 v[206:209], v150 offset:5120
	ds_read_b128 v[210:213], v150 offset:6144
	ds_read_b128 v[214:217], v150 offset:7168
	global_load_lds_dwordx4 v[218:219], off
	v_lshl_add_u64 v[218:219], v[146:147], 0, s[28:29]
	s_mov_b32 m0, s55
	s_nop 0
	global_load_lds_dwordx4 v[218:219], off
	s_waitcnt vmcnt(8)
	s_waitcnt lgkmcnt(0)
	s_barrier
; #define PG8_STAGE_A(bufoff, base_, nx_, kb_, h_) do { if (GATHER) { if (nx_) PG8_STAGE_G(bufoff, kb_, goN, h_); else PG8_STAGE_G(bufoff, kb_, goC, h_); } \
;         else PG8_STAGE(bufoff, (base_) + (kb_) + (h_) * hstep, voffA); } while (0)
; #define PG8_STAGE(bufoff, gbase, voff) do { _Pragma("unroll") for (int _i = 0; _i < 2; ++_i) \
;         __builtin_amdgcn_global_load_lds((const unsigned*)((const char*)(gbase) + (voff)[_i]), (LAS unsigned*)(lds + (bufoff) + ldsw + _i * 8192), 16, 0, 0); } while (0)
; #define PG8_LDA(dst, b, h) do { _Pragma("unroll") for (int m = 0; m < 4; ++m) _Pragma("unroll") for (int k = 0; k < 2; ++k) dst[m][k] = *(const LAS bf16x8*)(lds + PG8_SA(b, h) + aoff + m * 2048 + k * 1024); } while (0)
; #define PG8_LDB(dst, b, h) do { _Pragma("unroll") for (int n = 0; n < 2; ++n) _Pragma("unroll") for (int k = 0; k < 2; ++k) dst[n][k] = *(const LAS bf16x8*)(lds + PG8_SB(b, h) + boff + n * 2048 + k * 1024); } while (0)
; #define PG8_WAIT_V(n) asm volatile("s_waitcnt vmcnt(" #n ")" ::: "memory")
; #define PG8_WAIT_L(n) asm volatile("s_waitcnt lgkmcnt(" #n ")" ::: "memory")
; template <class Epi, class Sched, bool GATHER = false>
; __device__ __forceinline__ void gemm_phase(LAS unsigned char* lds, const Gemm g, const Sched& S, const Epi& E, const int tid) {
;     ...
;             PG8_LDB(B0, 0, 0); PG8_LDB(B1, 0, 1); PG8_SCHED; PG8_LDA(At, 0, 0); PG8_STAGE_A(PG8_SA(1, 1), cA, false, kb1, 1);
;             PG8_WAIT_V(8); PG8_WAIT_L(0); PG8_BAR; PG8_MMA(0, 0, At, B0); PG8_MMA(0, 1, At, B1); PG8_BAR; PG8_SCHED;
;             PG8_LDA(At, 0, 1); PG8_STAGE(PG8_SB(0, 0), b2, voffB); PG8_STAGE(PG8_SB(0, 1), b2 + hstep, voffB); PG8_STAGE_A(PG8_SA(0, 0), (last ? nA : cA), last, kb2, 0);
;             PG8_WAIT_V(8); PG8_WAIT_L(0); PG8_BAR; PG8_MMA(1, 0, At, B0); PG8_MMA(1, 1, At, B1); PG8_BAR; PG8_SCHED;
;             PG8_LDB(B0, 1, 0); PG8_LDB(B1, 1, 1); PG8_SCHED; PG8_LDA(At, 1, 0); PG8_STAGE_A(PG8_SA(0, 1), (last ? nA : cA), last, kb2, 1);
;             PG8_WAIT_V(8); PG8_WAIT_L(0); PG8_BAR; PG8_MMA(0, 0, At, B0); PG8_MMA(0, 1, At, B1); PG8_BAR; PG8_SCHED;
;             PG8_LDA(At, 1, 1); PG8_STAGE(PG8_SB(1, 0), b3, voffB); PG8_STAGE(PG8_SB(1, 1), b3 + hstep, voffB); PG8_STAGE_A(PG8_SA(1, 0), (last ? nA : cA), last, kb3, 0);
;             PG8_WAIT_V(8); PG8_WAIT_L(0); PG8_BAR; PG8_MMA(1, 0, At, B0); PG8_MMA(1, 1, At, B1); PG8_BAR; PG8_SCHED;
	v_mfma_f32_16x16x32_bf16 v[86:89], v[152:155], v[184:187], v[86:89]
	v_mfma_f32_16x16x32_bf16 v[18:21], v[160:163], v[184:187], v[18:21]
	v_mfma_f32_16x16x32_bf16 v[6:9], v[152:155], v[192:195], v[6:9]
	v_mfma_f32_16x16x32_bf16 v[22:25], v[160:163], v[192:195], v[22:25]
	v_mfma_f32_16x16x32_bf16 v[10:13], v[152:155], v[202:205], v[10:13]
	v_mfma_f32_16x16x32_bf16 v[26:29], v[160:163], v[202:205], v[26:29]
	v_mfma_f32_16x16x32_bf16 v[14:17], v[152:155], v[210:213], v[14:17]
	v_mfma_f32_16x16x32_bf16 v[30:33], v[160:163], v[210:213], v[30:33]
	v_mfma_f32_16x16x32_bf16 v[86:89], v[156:159], v[188:191], v[86:89]
	v_mfma_f32_16x16x32_bf16 v[18:21], v[164:167], v[188:191], v[18:21]
	v_mfma_f32_16x16x32_bf16 v[6:9], v[156:159], v[196:199], v[6:9]
	v_mfma_f32_16x16x32_bf16 v[22:25], v[164:167], v[196:199], v[22:25]
	v_mfma_f32_16x16x32_bf16 v[10:13], v[156:159], v[206:209], v[10:13]
	v_mfma_f32_16x16x32_bf16 v[26:29], v[164:167], v[206:209], v[26:29]
	v_mfma_f32_16x16x32_bf16 v[14:17], v[156:159], v[214:217], v[14:17]
	v_mfma_f32_16x16x32_bf16 v[30:33], v[164:167], v[214:217], v[30:33]
	v_mfma_f32_16x16x32_bf16 v[34:37], v[168:171], v[184:187], v[34:37]
	v_mfma_f32_16x16x32_bf16 v[50:53], v[176:179], v[184:187], v[50:53]
	v_mfma_f32_16x16x32_bf16 v[38:41], v[168:171], v[192:195], v[38:41]
	v_mfma_f32_16x16x32_bf16 v[58:61], v[176:179], v[192:195], v[58:61]
	v_mfma_f32_16x16x32_bf16 v[42:45], v[168:171], v[202:205], v[42:45]
	v_mfma_f32_16x16x32_bf16 v[66:69], v[176:179], v[202:205], v[66:69]
	v_mfma_f32_16x16x32_bf16 v[46:49], v[168:171], v[210:213], v[46:49]
	v_mfma_f32_16x16x32_bf16 v[74:77], v[176:179], v[210:213], v[74:77]
	v_mfma_f32_16x16x32_bf16 v[34:37], v[172:175], v[188:191], v[34:37]
	v_mfma_f32_16x16x32_bf16 v[50:53], v[180:183], v[188:191], v[50:53]
	v_mfma_f32_16x16x32_bf16 v[38:41], v[172:175], v[196:199], v[38:41]
	v_mfma_f32_16x16x32_bf16 v[58:61], v[180:183], v[196:199], v[58:61]
	v_mfma_f32_16x16x32_bf16 v[42:45], v[172:175], v[206:209], v[42:45]
	v_mfma_f32_16x16x32_bf16 v[66:69], v[180:183], v[206:209], v[66:69]
	v_mfma_f32_16x16x32_bf16 v[46:49], v[172:175], v[214:217], v[46:49]
	v_mfma_f32_16x16x32_bf16 v[74:77], v[180:183], v[214:217], v[74:77]
	s_barrier
	s_mov_b32 m0, s56
	v_lshl_add_u64 v[218:219], s[24:25], 0, v[136:137]
	s_cselect_b32 s52, 0, s23
	s_cselect_b32 s53, 0, s22
	s_add_u32 s28, s24, 0x80000
	ds_read_b128 v[184:187], v150 offset:16384
	ds_read_b128 v[188:191], v150 offset:17408
	ds_read_b128 v[192:195], v150 offset:18432
	ds_read_b128 v[196:199], v150 offset:19456
	ds_read_b128 v[202:205], v150 offset:20480
	ds_read_b128 v[206:209], v150 offset:21504
	ds_read_b128 v[210:213], v150 offset:22528
	ds_read_b128 v[214:217], v150 offset:23552
	global_load_lds_dwordx4 v[218:219], off
	v_lshl_add_u64 v[220:221], s[24:25], 0, v[140:141]
	s_mov_b32 m0, s57
	s_addc_u32 s29, s25, 0
	s_add_i32 s54, s54, s33
	global_load_lds_dwordx4 v[220:221], off
	v_lshl_add_u64 v[222:223], s[28:29], 0, v[136:137]
	s_mov_b32 m0, s54
	s_nop 0
	global_load_lds_dwordx4 v[222:223], off
	v_lshl_add_u64 v[222:223], s[28:29], 0, v[140:141]
	s_add_i32 m0, s54, 0x2000
	s_and_b64 s[28:29], s[50:51], s[4:5]
	s_and_b64 s[28:29], s[28:29], exec
	s_cselect_b32 s28, s18, s10
	s_cselect_b32 s29, s19, s11
	s_add_u32 s28, s28, s53
	s_addc_u32 s29, s29, s52
	global_load_lds_dwordx4 v[222:223], off
	v_lshl_add_u64 v[222:223], s[28:29], 0, v[134:135]
	s_mov_b32 m0, s9
	v_lshl_add_u64 v[224:225], s[28:29], 0, v[138:139]
	global_load_lds_dwordx4 v[222:223], off
	s_mov_b32 m0, s38
	s_nop 0
	global_load_lds_dwordx4 v[224:225], off
	s_waitcnt vmcnt(8)
	s_waitcnt lgkmcnt(0)
	s_barrier
	v_mfma_f32_16x16x32_bf16 v[54:57], v[152:155], v[184:187], v[54:57]
	v_mfma_f32_16x16x32_bf16 v[78:81], v[160:163], v[184:187], v[78:81]
	v_mfma_f32_16x16x32_bf16 v[62:65], v[152:155], v[192:195], v[62:65]
	v_mfma_f32_16x16x32_bf16 v[82:85], v[160:163], v[192:195], v[82:85]
	v_mfma_f32_16x16x32_bf16 v[70:73], v[152:155], v[202:205], v[70:73]
	v_mfma_f32_16x16x32_bf16 v[98:101], v[160:163], v[202:205], v[98:101]
	v_mfma_f32_16x16x32_bf16 v[90:93], v[152:155], v[210:213], v[90:93]
	v_mfma_f32_16x16x32_bf16 v[94:97], v[160:163], v[210:213], v[94:97]
	v_mfma_f32_16x16x32_bf16 v[54:57], v[156:159], v[188:191], v[54:57]
	v_mfma_f32_16x16x32_bf16 v[78:81], v[164:167], v[188:191], v[78:81]
	v_mfma_f32_16x16x32_bf16 v[62:65], v[156:159], v[196:199], v[62:65]
	v_mfma_f32_16x16x32_bf16 v[82:85], v[164:167], v[196:199], v[82:85]
	v_mfma_f32_16x16x32_bf16 v[70:73], v[156:159], v[206:209], v[70:73]
	v_mfma_f32_16x16x32_bf16 v[98:101], v[164:167], v[206:209], v[98:101]
	v_mfma_f32_16x16x32_bf16 v[90:93], v[156:159], v[214:217], v[90:93]
	v_mfma_f32_16x16x32_bf16 v[94:97], v[164:167], v[214:217], v[94:97]
	v_mfma_f32_16x16x32_bf16 v[114:117], v[168:171], v[184:187], v[114:117]
	v_mfma_f32_16x16x32_bf16 v[130:133], v[176:179], v[184:187], v[130:133]
	v_mfma_f32_16x16x32_bf16 v[110:113], v[168:171], v[192:195], v[110:113]
	v_mfma_f32_16x16x32_bf16 v[126:129], v[176:179], v[192:195], v[126:129]
	v_mfma_f32_16x16x32_bf16 v[106:109], v[168:171], v[202:205], v[106:109]
	v_mfma_f32_16x16x32_bf16 v[122:125], v[176:179], v[202:205], v[122:125]
	v_mfma_f32_16x16x32_bf16 v[102:105], v[168:171], v[210:213], v[102:105]
	v_mfma_f32_16x16x32_bf16 v[118:121], v[176:179], v[210:213], v[118:121]
	v_mfma_f32_16x16x32_bf16 v[114:117], v[172:175], v[188:191], v[114:117]
	v_mfma_f32_16x16x32_bf16 v[130:133], v[180:183], v[188:191], v[130:133]
	v_mfma_f32_16x16x32_bf16 v[110:113], v[172:175], v[196:199], v[110:113]
	v_mfma_f32_16x16x32_bf16 v[126:129], v[180:183], v[196:199], v[126:129]
	v_mfma_f32_16x16x32_bf16 v[106:109], v[172:175], v[206:209], v[106:109]
	v_mfma_f32_16x16x32_bf16 v[122:125], v[180:183], v[206:209], v[122:125]
	v_mfma_f32_16x16x32_bf16 v[102:105], v[172:175], v[214:217], v[102:105]
	v_mfma_f32_16x16x32_bf16 v[118:121], v[180:183], v[214:217], v[118:121]
	s_barrier
; #define PG8_STAGE_A(bufoff, base_, nx_, kb_, h_) do { if (GATHER) { if (nx_) PG8_STAGE_G(bufoff, kb_, goN, h_); else PG8_STAGE_G(bufoff, kb_, goC, h_); } \
;         else PG8_STAGE(bufoff, (base_) + (kb_) + (h_) * hstep, voffA); } while (0)
; #define PG8_STAGE(bufoff, gbase, voff) do { _Pragma("unroll") for (int _i = 0; _i < 2; ++_i) \
;         __builtin_amdgcn_global_load_lds((const unsigned*)((const char*)(gbase) + (voff)[_i]), (LAS unsigned*)(lds + (bufoff) + ldsw + _i * 8192), 16, 0, 0); } while (0)
; #define PG8_LDA(dst, b, h) do { _Pragma("unroll") for (int m = 0; m < 4; ++m) _Pragma("unroll") for (int k = 0; k < 2; ++k) dst[m][k] = *(const LAS bf16x8*)(lds + PG8_SA(b, h) + aoff + m * 2048 + k * 1024); } while (0)
; #define PG8_LDB(dst, b, h) do { _Pragma("unroll") for (int n = 0; n < 2; ++n) _Pragma("unroll") for (int k = 0; k < 2; ++k) dst[n][k] = *(const LAS bf16x8*)(lds + PG8_SB(b, h) + boff + n * 2048 + k * 1024); } while (0)
; #define PG8_MMA(ai, bj, At, Bt) do { __builtin_amdgcn_s_setprio(1); _Pragma("unroll") for (int m = 0; m < 4; ++m) _Pragma("unroll") for (int n = 0; n < 2; ++n) _Pragma("unroll") for (int k = 0; k < 2; ++k) \
;         acc[ai][bj][m][n] = __builtin_amdgcn_mfma_f32_16x16x32_bf16(Bt[n][k], At[m][k], acc[ai][bj][m][n], 0, 0, 0); __builtin_amdgcn_s_setprio(0); } while (0)
; #define PG8_WAIT_V(n) asm volatile("s_waitcnt vmcnt(" #n ")" ::: "memory")
; #define PG8_WAIT_L(n) asm volatile("s_waitcnt lgkmcnt(" #n ")" ::: "memory")
; #define PG8_BAR __builtin_amdgcn_s_barrier()
; #define PG8_SCHED __builtin_amdgcn_sched_barrier(0)
; template <class Epi, class Sched, bool GATHER = false>
; __device__ __forceinline__ void gemm_phase(LAS unsigned char* lds, const Gemm g, const Sched& S, const Epi& E, const int tid) {
;     ...
;             PG8_LDB(B0, 1, 0); PG8_LDB(B1, 1, 1); PG8_SCHED; PG8_LDA(At, 1, 0); PG8_STAGE_A(PG8_SA(0, 1), (last ? nA : cA), last, kb2, 1);
;             PG8_WAIT_V(8); PG8_WAIT_L(0); PG8_BAR; PG8_MMA(0, 0, At, B0); PG8_MMA(0, 1, At, B1); PG8_BAR; PG8_SCHED;
;             PG8_LDA(At, 1, 1); PG8_STAGE(PG8_SB(1, 0), b3, voffB); PG8_STAGE(PG8_SB(1, 1), b3 + hstep, voffB); PG8_STAGE_A(PG8_SA(1, 0), (last ? nA : cA), last, kb3, 0);
;             PG8_WAIT_V(8); PG8_WAIT_L(0); PG8_BAR; PG8_MMA(1, 0, At, B0); PG8_MMA(1, 1, At, B1); PG8_BAR; PG8_SCHED;
	s_add_i32 s50, 0, 0x18000
	v_add_u32_e32 v2, s50, v148
	s_add_i32 s51, 0, 0x1c000
	ds_read_b128 v[152:155], v2
	ds_read_b128 v[156:159], v2 offset:1024
	ds_read_b128 v[160:163], v2 offset:2048
	ds_read_b128 v[164:167], v2 offset:3072
	v_add_u32_e32 v2, s51, v148
	ds_read_b128 v[168:171], v2
	ds_read_b128 v[172:175], v2 offset:1024
	ds_read_b128 v[176:179], v2 offset:2048
	ds_read_b128 v[180:183], v2 offset:3072
	s_add_u32 s28, s28, 0x80000
	s_addc_u32 s29, s29, 0
	s_mov_b32 m0, s39
	v_lshl_add_u64 v[226:227], s[28:29], 0, v[134:135]
	ds_read_b128 v[184:187], v150 offset:32768
	ds_read_b128 v[188:191], v150 offset:33792
	ds_read_b128 v[192:195], v150 offset:34816
	ds_read_b128 v[196:199], v150 offset:35840
	ds_read_b128 v[202:205], v150 offset:36864
	ds_read_b128 v[206:209], v150 offset:37888
	ds_read_b128 v[210:213], v150 offset:38912
	ds_read_b128 v[214:217], v150 offset:39936
	global_load_lds_dwordx4 v[226:227], off
	v_lshl_add_u64 v[226:227], s[28:29], 0, v[138:139]
	s_mov_b32 m0, s40
	s_nop 0
	global_load_lds_dwordx4 v[226:227], off
	s_waitcnt vmcnt(8)
	s_waitcnt lgkmcnt(0)
	s_barrier
	v_mfma_f32_16x16x32_bf16 v[86:89], v[152:155], v[184:187], v[86:89]
	v_mfma_f32_16x16x32_bf16 v[18:21], v[160:163], v[184:187], v[18:21]
	v_mfma_f32_16x16x32_bf16 v[6:9], v[152:155], v[192:195], v[6:9]
	v_mfma_f32_16x16x32_bf16 v[22:25], v[160:163], v[192:195], v[22:25]
	v_mfma_f32_16x16x32_bf16 v[10:13], v[152:155], v[202:205], v[10:13]
	v_mfma_f32_16x16x32_bf16 v[26:29], v[160:163], v[202:205], v[26:29]
	v_mfma_f32_16x16x32_bf16 v[14:17], v[152:155], v[210:213], v[14:17]
	v_mfma_f32_16x16x32_bf16 v[30:33], v[160:163], v[210:213], v[30:33]
	v_mfma_f32_16x16x32_bf16 v[86:89], v[156:159], v[188:191], v[86:89]
	v_mfma_f32_16x16x32_bf16 v[18:21], v[164:167], v[188:191], v[18:21]
	v_mfma_f32_16x16x32_bf16 v[6:9], v[156:159], v[196:199], v[6:9]
	v_mfma_f32_16x16x32_bf16 v[22:25], v[164:167], v[196:199], v[22:25]
	v_mfma_f32_16x16x32_bf16 v[10:13], v[156:159], v[206:209], v[10:13]
	v_mfma_f32_16x16x32_bf16 v[26:29], v[164:167], v[206:209], v[26:29]
	v_mfma_f32_16x16x32_bf16 v[14:17], v[156:159], v[214:217], v[14:17]
	v_mfma_f32_16x16x32_bf16 v[30:33], v[164:167], v[214:217], v[30:33]
	v_mfma_f32_16x16x32_bf16 v[34:37], v[168:171], v[184:187], v[34:37]
	v_mfma_f32_16x16x32_bf16 v[50:53], v[176:179], v[184:187], v[50:53]
	v_mfma_f32_16x16x32_bf16 v[38:41], v[168:171], v[192:195], v[38:41]
	v_mfma_f32_16x16x32_bf16 v[58:61], v[176:179], v[192:195], v[58:61]
	v_mfma_f32_16x16x32_bf16 v[42:45], v[168:171], v[202:205], v[42:45]
	v_mfma_f32_16x16x32_bf16 v[66:69], v[176:179], v[202:205], v[66:69]
	v_mfma_f32_16x16x32_bf16 v[46:49], v[168:171], v[210:213], v[46:49]
	v_mfma_f32_16x16x32_bf16 v[74:77], v[176:179], v[210:213], v[74:77]
	v_mfma_f32_16x16x32_bf16 v[34:37], v[172:175], v[188:191], v[34:37]
	v_mfma_f32_16x16x32_bf16 v[50:53], v[180:183], v[188:191], v[50:53]
	v_mfma_f32_16x16x32_bf16 v[38:41], v[172:175], v[196:199], v[38:41]
	v_mfma_f32_16x16x32_bf16 v[58:61], v[180:183], v[196:199], v[58:61]
	v_mfma_f32_16x16x32_bf16 v[42:45], v[172:175], v[206:209], v[42:45]
	v_mfma_f32_16x16x32_bf16 v[66:69], v[180:183], v[206:209], v[66:69]
	v_mfma_f32_16x16x32_bf16 v[46:49], v[172:175], v[214:217], v[46:49]
	v_mfma_f32_16x16x32_bf16 v[74:77], v[180:183], v[214:217], v[74:77]
	s_barrier
	s_add_i32 s28, s50, s33
	v_lshl_add_u64 v[218:219], v[218:219], 0, s[0:1]
	s_mov_b32 m0, s28
	ds_read_b128 v[184:187], v150 offset:49152
	ds_read_b128 v[188:191], v150 offset:50176
	ds_read_b128 v[192:195], v150 offset:51200
	ds_read_b128 v[196:199], v150 offset:52224
	ds_read_b128 v[202:205], v150 offset:53248
	ds_read_b128 v[206:209], v150 offset:54272
	ds_read_b128 v[210:213], v150 offset:55296
	ds_read_b128 v[214:217], v150 offset:56320
	global_load_lds_dwordx4 v[218:219], off
	s_add_i32 m0, s28, 0x2000
	s_add_u32 s24, s24, 0x80080
	v_lshl_add_u64 v[218:219], v[220:221], 0, s[0:1]
	s_addc_u32 s25, s25, 0
	s_add_i32 s28, s51, s33
	global_load_lds_dwordx4 v[218:219], off
	v_lshl_add_u64 v[218:219], s[24:25], 0, v[136:137]
	s_mov_b32 m0, s28
	s_nop 0
	global_load_lds_dwordx4 v[218:219], off
	v_lshl_add_u64 v[218:219], s[24:25], 0, v[140:141]
	s_add_i32 m0, s28, 0x2000
	s_nop 0
	global_load_lds_dwordx4 v[218:219], off
	v_lshl_add_u64 v[218:219], v[222:223], 0, s[0:1]
	s_mov_b32 m0, s42
	s_nop 0
	global_load_lds_dwordx4 v[218:219], off
	v_lshl_add_u64 v[218:219], v[224:225], 0, s[0:1]
	s_mov_b32 m0, s43
	s_nop 0
	global_load_lds_dwordx4 v[218:219], off
	s_waitcnt vmcnt(8)
	s_waitcnt lgkmcnt(0)
	s_barrier
	v_mfma_f32_16x16x32_bf16 v[54:57], v[152:155], v[184:187], v[54:57]
	v_mfma_f32_16x16x32_bf16 v[78:81], v[160:163], v[184:187], v[78:81]
	v_mfma_f32_16x16x32_bf16 v[62:65], v[152:155], v[192:195], v[62:65]
	v_mfma_f32_16x16x32_bf16 v[82:85], v[160:163], v[192:195], v[82:85]
	v_mfma_f32_16x16x32_bf16 v[70:73], v[152:155], v[202:205], v[70:73]
	v_mfma_f32_16x16x32_bf16 v[98:101], v[160:163], v[202:205], v[98:101]
	v_mfma_f32_16x16x32_bf16 v[90:93], v[152:155], v[210:213], v[90:93]
	v_mfma_f32_16x16x32_bf16 v[94:97], v[160:163], v[210:213], v[94:97]
	v_mfma_f32_16x16x32_bf16 v[54:57], v[156:159], v[188:191], v[54:57]
	v_mfma_f32_16x16x32_bf16 v[78:81], v[164:167], v[188:191], v[78:81]
	v_mfma_f32_16x16x32_bf16 v[62:65], v[156:159], v[196:199], v[62:65]
	v_mfma_f32_16x16x32_bf16 v[82:85], v[164:167], v[196:199], v[82:85]
	v_mfma_f32_16x16x32_bf16 v[70:73], v[156:159], v[206:209], v[70:73]
	v_mfma_f32_16x16x32_bf16 v[98:101], v[164:167], v[206:209], v[98:101]
	v_mfma_f32_16x16x32_bf16 v[90:93], v[156:159], v[214:217], v[90:93]
	v_mfma_f32_16x16x32_bf16 v[94:97], v[164:167], v[214:217], v[94:97]
	v_mfma_f32_16x16x32_bf16 v[114:117], v[168:171], v[184:187], v[114:117]
	v_mfma_f32_16x16x32_bf16 v[130:133], v[176:179], v[184:187], v[130:133]
	v_mfma_f32_16x16x32_bf16 v[110:113], v[168:171], v[192:195], v[110:113]
	v_mfma_f32_16x16x32_bf16 v[126:129], v[176:179], v[192:195], v[126:129]
	v_mfma_f32_16x16x32_bf16 v[106:109], v[168:171], v[202:205], v[106:109]
	v_mfma_f32_16x16x32_bf16 v[122:125], v[176:179], v[202:205], v[122:125]
	v_mfma_f32_16x16x32_bf16 v[102:105], v[168:171], v[210:213], v[102:105]
	v_mfma_f32_16x16x32_bf16 v[118:121], v[176:179], v[210:213], v[118:121]
	v_mfma_f32_16x16x32_bf16 v[114:117], v[172:175], v[188:191], v[114:117]
	v_mfma_f32_16x16x32_bf16 v[130:133], v[180:183], v[188:191], v[130:133]
	v_mfma_f32_16x16x32_bf16 v[110:113], v[172:175], v[196:199], v[110:113]
	v_mfma_f32_16x16x32_bf16 v[126:129], v[180:183], v[196:199], v[126:129]
	v_mfma_f32_16x16x32_bf16 v[106:109], v[172:175], v[206:209], v[106:109]
	v_mfma_f32_16x16x32_bf16 v[122:125], v[180:183], v[206:209], v[122:125]
	v_mfma_f32_16x16x32_bf16 v[102:105], v[172:175], v[214:217], v[102:105]
	v_mfma_f32_16x16x32_bf16 v[118:121], v[180:183], v[214:217], v[118:121]
	s_barrier
	s_add_i32 s49, s49, 2
	s_cmp_gt_u32 s49, 29
	s_mov_b64 s[28:29], s[22:23]
	s_cbranch_scc0 .LBB0_1128

; template <class Epi, class Sched, bool GATHER = false>
; __device__ __forceinline__ void gemm_phase(LAS unsigned char* lds, const Gemm g, const Sched& S, const Epi& E, const int tid) {
;     ...
;         const bool has_next = S.next(ui + 1, nxt);
;         const char* nA = has_next ? (const char*)g.A + (size_t)nxt.pm * tstep : cA; const char* nB = has_next ? (const char*)g.Bt + (size_t)nxt.pb * tstep : cB;
;         if (GATHER && has_next && wid < 4) __builtin_amdgcn_global_load_lds((const unsigned*)(g.rowmap + nxt.rb + tid), (LAS unsigned*)(lds + STAGE_BYTES + ((ui + 1) & 1) * 1024 + wid * 256), 4, 0, 0);
;         for (int t = 0; t < nt; t += 2) {
;             const bool last = (t == nt - 2);
;             const char* a1 = cA + (size_t)(t + 1) * kstep;
;             const char* a2 = last ? nA : cA + (size_t)(t + 2) * kstep; const char* b2 = last ? nB : cB + (size_t)(t + 2) * kstep;
;             const char* a3 = a2 + kstep; const char* b3 = b2 + kstep;
;     ...
;             PG8_LDB(B0, 0, 0); PG8_SCHED; PG8_LDA(At, 0, 0); PG8_STAGE(PG8_SA(1, 1), a1 + hstep, voffA);
;             PG8_WAIT_L(8); PG8_BAR; PG8_WAIT_L(0); PG8_MMA(0, 0, At, B0); PG8_BAR; PG8_SCHED;
;             PG8_LDB(B1, 0, 1); PG8_STAGE(PG8_SB(0, 0), b2, voffB);
;             PG8_BAR; PG8_WAIT_L(0); PG8_MMA(0, 1, At, B1); PG8_BAR;
;             PG8_LDA(At, 0, 1); PG8_STAGE(PG8_SA(0, 0), a2, voffA);
;             PG8_BAR; PG8_WAIT_L(0); PG8_MMA(1, 0, At, B0); PG8_BAR; PG8_SCHED;
;             PG8_STAGE(PG8_SB(0, 1), b2 + hstep, voffB);
;             PG8_WAIT_V(6); PG8_BAR; PG8_MMA(1, 1, At, B1); PG8_BAR;
;             PG8_LDB(B0, 1, 0); PG8_SCHED; PG8_LDA(At, 1, 0); PG8_STAGE(PG8_SA(0, 1), a2 + hstep, voffA);
;             PG8_WAIT_L(8); PG8_BAR; PG8_WAIT_L(0); PG8_MMA(0, 0, At, B0); PG8_BAR; PG8_SCHED;
;             PG8_LDB(B1, 1, 1); PG8_STAGE(PG8_SB(1, 0), b3, voffB);
;             PG8_BAR; PG8_WAIT_L(0); PG8_MMA(0, 1, At, B1); PG8_BAR;
;             PG8_LDA(At, 1, 1); PG8_STAGE(PG8_SA(1, 0), a3, voffA);
;             PG8_BAR; PG8_WAIT_L(0); PG8_MMA(1, 0, At, B0); PG8_BAR; PG8_SCHED;
;             PG8_STAGE(PG8_SB(1, 1), b3 + hstep, voffB);
;             PG8_WAIT_V(6); PG8_BAR; PG8_MMA(1, 1, At, B1); PG8_BAR;
;     ...
;             if (GATHER && last && has_next) {
;                 const LAS int* ib_ = (const LAS int*)(lds + STAGE_BYTES + ((ui + 1) & 1) * 1024);
; #pragma unroll
.LBB0_1366:
	s_ashr_i32 s23, s22, 31
	s_lshl_b64 s[24:25], s[22:23], 20
	s_add_u32 s24, s12, s24
	s_addc_u32 s25, s13, s25
	s_ashr_i32 s21, s20, 31
	s_lshl_b64 s[28:29], s[20:21], 20
	s_add_u32 s28, s14, s28
	s_addc_u32 s29, s15, s29
	s_and_b64 s[38:39], s[8:9], exec
	s_cselect_b32 s21, s29, s37
	s_cselect_b32 s23, s28, s36
	s_add_u32 s59, s36, 0x100
	s_addc_u32 s60, s37, 0
	s_add_u32 s36, s34, 0x80080
	s_addc_u32 s37, s35, 0
	v_lshl_add_u64 v[4:5], s[36:37], 0, v[144:145]
	v_lshl_add_u64 v[148:149], s[36:37], 0, v[146:147]
	s_mov_b32 s61, -2
	s_mov_b64 s[40:41], 0
	s_add_u32 s62, s59, s40
	s_addc_u32 s63, s60, s41
	s_add_u32 s36, s40, 0x100
	s_addc_u32 s37, s41, 0
	s_cmp_eq_u32 s61, 28
	s_cselect_b64 s[42:43], -1, 0
	s_and_b64 s[38:39], s[42:43], exec
	s_cselect_b32 s39, s21, s63
	s_cselect_b32 s38, s23, s62
	s_cselect_b32 s62, 0, s36
	s_add_i32 s63, 0, 0x10000
	v_add_u32_e32 v2, s63, v135
	s_add_i32 s64, 0, 0x14000
	ds_read_b128 v[152:155], v2
	ds_read_b128 v[156:159], v2 offset:1024
	ds_read_b128 v[160:163], v2 offset:2048
	ds_read_b128 v[164:167], v2 offset:3072
	v_add_u32_e32 v2, s64, v135
	ds_read_b128 v[168:171], v2
	ds_read_b128 v[172:175], v2 offset:1024
	ds_read_b128 v[176:179], v2 offset:2048
	ds_read_b128 v[180:183], v2 offset:3072
	v_lshl_add_u64 v[218:219], v[4:5], 0, s[40:41]
	s_add_i32 m0, s31, 0xc000
	ds_read_b128 v[184:187], v151
	ds_read_b128 v[188:191], v151 offset:1024
	ds_read_b128 v[192:195], v151 offset:2048
	ds_read_b128 v[196:199], v151 offset:3072
	ds_read_b128 v[202:205], v151 offset:4096
	ds_read_b128 v[206:209], v151 offset:5120
	ds_read_b128 v[210:213], v151 offset:6144
	ds_read_b128 v[214:217], v151 offset:7168
	global_load_lds_dwordx4 v[218:219], off
	v_lshl_add_u64 v[218:219], v[148:149], 0, s[40:41]
	s_add_i32 m0, s31, 0xe000
	s_nop 0
	global_load_lds_dwordx4 v[218:219], off
	s_waitcnt vmcnt(8)
	s_waitcnt lgkmcnt(0)
	s_barrier
	v_mfma_f32_16x16x32_bf16 v[122:125], v[152:155], v[184:187], 0
	v_mfma_f32_16x16x32_bf16 v[74:77], v[160:163], v[184:187], 0
	v_mfma_f32_16x16x32_bf16 v[58:61], v[152:155], v[192:195], 0
	v_mfma_f32_16x16x32_bf16 v[50:53], v[160:163], v[192:195], 0
	v_mfma_f32_16x16x32_bf16 v[38:41], v[152:155], v[202:205], 0
	v_mfma_f32_16x16x32_bf16 v[34:37], v[160:163], v[202:205], 0
	v_mfma_f32_16x16x32_bf16 v[22:25], v[152:155], v[210:213], 0
	v_mfma_f32_16x16x32_bf16 v[18:21], v[160:163], v[210:213], 0
	v_mfma_f32_16x16x32_bf16 v[122:125], v[156:159], v[188:191], v[122:125]
	v_mfma_f32_16x16x32_bf16 v[74:77], v[164:167], v[188:191], v[74:77]
	v_mfma_f32_16x16x32_bf16 v[58:61], v[156:159], v[196:199], v[58:61]
	v_mfma_f32_16x16x32_bf16 v[50:53], v[164:167], v[196:199], v[50:53]
	v_mfma_f32_16x16x32_bf16 v[38:41], v[156:159], v[206:209], v[38:41]
	v_mfma_f32_16x16x32_bf16 v[34:37], v[164:167], v[206:209], v[34:37]
	v_mfma_f32_16x16x32_bf16 v[22:25], v[156:159], v[214:217], v[22:25]
	v_mfma_f32_16x16x32_bf16 v[18:21], v[164:167], v[214:217], v[18:21]
	v_mfma_f32_16x16x32_bf16 v[106:109], v[168:171], v[184:187], 0
	v_mfma_f32_16x16x32_bf16 v[110:113], v[176:179], v[184:187], 0
	v_mfma_f32_16x16x32_bf16 v[90:93], v[168:171], v[192:195], 0
	v_mfma_f32_16x16x32_bf16 v[94:97], v[176:179], v[192:195], 0
	v_mfma_f32_16x16x32_bf16 v[66:69], v[168:171], v[202:205], 0
	v_mfma_f32_16x16x32_bf16 v[70:73], v[176:179], v[202:205], 0
	v_mfma_f32_16x16x32_bf16 v[42:45], v[168:171], v[210:213], 0
	v_mfma_f32_16x16x32_bf16 v[46:49], v[176:179], v[210:213], 0
	v_mfma_f32_16x16x32_bf16 v[106:109], v[172:175], v[188:191], v[106:109]
	v_mfma_f32_16x16x32_bf16 v[110:113], v[180:183], v[188:191], v[110:113]
	v_mfma_f32_16x16x32_bf16 v[90:93], v[172:175], v[196:199], v[90:93]
	v_mfma_f32_16x16x32_bf16 v[94:97], v[180:183], v[196:199], v[94:97]
	v_mfma_f32_16x16x32_bf16 v[66:69], v[172:175], v[206:209], v[66:69]
	v_mfma_f32_16x16x32_bf16 v[70:73], v[180:183], v[206:209], v[70:73]
	v_mfma_f32_16x16x32_bf16 v[42:45], v[172:175], v[214:217], v[42:45]
	v_mfma_f32_16x16x32_bf16 v[46:49], v[180:183], v[214:217], v[46:49]
	s_barrier
	s_add_i32 s40, s63, s50
	v_lshl_add_u64 v[218:219], s[38:39], 0, v[140:141]
	s_mov_b32 m0, s40
	ds_read_b128 v[184:187], v151 offset:16384
	ds_read_b128 v[188:191], v151 offset:17408
	ds_read_b128 v[192:195], v151 offset:18432
	ds_read_b128 v[196:199], v151 offset:19456
	ds_read_b128 v[202:205], v151 offset:20480
	ds_read_b128 v[206:209], v151 offset:21504
	ds_read_b128 v[210:213], v151 offset:22528
	ds_read_b128 v[214:217], v151 offset:23552
	global_load_lds_dwordx4 v[218:219], off
	s_add_i32 m0, s40, 0x2000
	s_add_u32 s40, s38, 0x80000
	v_lshl_add_u64 v[220:221], s[38:39], 0, v[136:137]
	s_addc_u32 s41, s39, 0
	s_add_i32 s63, s64, s50
	global_load_lds_dwordx4 v[220:221], off
	v_lshl_add_u64 v[222:223], s[40:41], 0, v[140:141]
	s_mov_b32 m0, s63
	s_nop 0
	global_load_lds_dwordx4 v[222:223], off
	v_lshl_add_u64 v[222:223], s[40:41], 0, v[136:137]
	s_add_i32 m0, s63, 0x2000
	s_and_b64 s[40:41], s[8:9], s[42:43]
	s_and_b64 s[40:41], s[40:41], exec
	s_cselect_b32 s40, s24, s34
	s_cselect_b32 s41, s25, s35
	s_add_u32 s40, s40, s62
	s_addc_u32 s41, s41, 0
	global_load_lds_dwordx4 v[222:223], off
	v_lshl_add_u64 v[222:223], s[40:41], 0, v[142:143]
	s_mov_b32 m0, s31
	v_lshl_add_u64 v[224:225], s[40:41], 0, v[138:139]
	global_load_lds_dwordx4 v[222:223], off
	s_mov_b32 m0, s52
	s_nop 0
	global_load_lds_dwordx4 v[224:225], off
	s_waitcnt vmcnt(8)
	s_waitcnt lgkmcnt(0)
	s_barrier
; #define PG8_STAGE_A(bufoff, base_, nx_, kb_, h_) do { if (GATHER) { if (nx_) PG8_STAGE_G(bufoff, kb_, goN, h_); else PG8_STAGE_G(bufoff, kb_, goC, h_); } \
;         else PG8_STAGE(bufoff, (base_) + (kb_) + (h_) * hstep, voffA); } while (0)
; #define PG8_STAGE(bufoff, gbase, voff) do { _Pragma("unroll") for (int _i = 0; _i < 2; ++_i) \
;         __builtin_amdgcn_global_load_lds((const unsigned*)((const char*)(gbase) + (voff)[_i]), (LAS unsigned*)(lds + (bufoff) + ldsw + _i * 8192), 16, 0, 0); } while (0)
; #define PG8_LDA(dst, b, h) do { _Pragma("unroll") for (int m = 0; m < 4; ++m) _Pragma("unroll") for (int k = 0; k < 2; ++k) dst[m][k] = *(const LAS bf16x8*)(lds + PG8_SA(b, h) + aoff + m * 2048 + k * 1024); } while (0)
; #define PG8_LDB(dst, b, h) do { _Pragma("unroll") for (int n = 0; n < 2; ++n) _Pragma("unroll") for (int k = 0; k < 2; ++k) dst[n][k] = *(const LAS bf16x8*)(lds + PG8_SB(b, h) + boff + n * 2048 + k * 1024); } while (0)
; #define PG8_WAIT_V(n) asm volatile("s_waitcnt vmcnt(" #n ")" ::: "memory")
; #define PG8_WAIT_L(n) asm volatile("s_waitcnt lgkmcnt(" #n ")" ::: "memory")
; template <class Epi, class Sched, bool GATHER = false>
; __device__ __forceinline__ void gemm_phase(LAS unsigned char* lds, const Gemm g, const Sched& S, const Epi& E, const int tid) {
;     ...
;             PG8_LDB(B0, 0, 0); PG8_LDB(B1, 0, 1); PG8_SCHED; PG8_LDA(At, 0, 0); PG8_STAGE_A(PG8_SA(1, 1), cA, false, kb1, 1);
;             PG8_WAIT_V(8); PG8_WAIT_L(0); PG8_BAR; PG8_MMA(0, 0, At, B0); PG8_MMA(0, 1, At, B1); PG8_BAR; PG8_SCHED;
;             PG8_LDA(At, 0, 1); PG8_STAGE(PG8_SB(0, 0), b2, voffB); PG8_STAGE(PG8_SB(0, 1), b2 + hstep, voffB); PG8_STAGE_A(PG8_SA(0, 0), (last ? nA : cA), last, kb2, 0);
;             PG8_WAIT_V(8); PG8_WAIT_L(0); PG8_BAR; PG8_MMA(1, 0, At, B0); PG8_MMA(1, 1, At, B1); PG8_BAR; PG8_SCHED;
;             PG8_LDB(B0, 1, 0); PG8_LDB(B1, 1, 1); PG8_SCHED; PG8_LDA(At, 1, 0); PG8_STAGE_A(PG8_SA(0, 1), (last ? nA : cA), last, kb2, 1);
;             PG8_WAIT_V(8); PG8_WAIT_L(0); PG8_BAR; PG8_MMA(0, 0, At, B0); PG8_MMA(0, 1, At, B1); PG8_BAR; PG8_SCHED;
;             PG8_LDA(At, 1, 1); PG8_STAGE(PG8_SB(1, 0), b3, voffB); PG8_STAGE(PG8_SB(1, 1), b3 + hstep, voffB); PG8_STAGE_A(PG8_SA(1, 0), (last ? nA : cA), last, kb3, 0);
;             PG8_WAIT_V(8); PG8_WAIT_L(0); PG8_BAR; PG8_MMA(1, 0, At, B0); PG8_MMA(1, 1, At, B1); PG8_BAR; PG8_SCHED;
	v_mfma_f32_16x16x32_bf16 v[30:33], v[152:155], v[184:187], 0
	v_mfma_f32_16x16x32_bf16 v[26:29], v[160:163], v[184:187], 0
	v_mfma_f32_16x16x32_bf16 v[14:17], v[152:155], v[192:195], 0
	v_mfma_f32_16x16x32_bf16 v[10:13], v[160:163], v[192:195], 0
	v_mfma_f32_16x16x32_bf16 v[6:9], v[152:155], v[202:205], 0
	v_mfma_f32_16x16x32_bf16 v[78:81], v[160:163], v[202:205], 0
	v_mfma_f32_16x16x32_bf16 v[62:65], v[152:155], v[210:213], 0
	v_mfma_f32_16x16x32_bf16 v[54:57], v[160:163], v[210:213], 0
	v_mfma_f32_16x16x32_bf16 v[30:33], v[156:159], v[188:191], v[30:33]
	v_mfma_f32_16x16x32_bf16 v[26:29], v[164:167], v[188:191], v[26:29]
	v_mfma_f32_16x16x32_bf16 v[14:17], v[156:159], v[196:199], v[14:17]
	v_mfma_f32_16x16x32_bf16 v[10:13], v[164:167], v[196:199], v[10:13]
	v_mfma_f32_16x16x32_bf16 v[6:9], v[156:159], v[206:209], v[6:9]
	v_mfma_f32_16x16x32_bf16 v[78:81], v[164:167], v[206:209], v[78:81]
	v_mfma_f32_16x16x32_bf16 v[62:65], v[156:159], v[214:217], v[62:65]
	v_mfma_f32_16x16x32_bf16 v[54:57], v[164:167], v[214:217], v[54:57]
	v_mfma_f32_16x16x32_bf16 v[130:133], v[168:171], v[184:187], 0
	v_mfma_f32_16x16x32_bf16 v[126:129], v[176:179], v[184:187], 0
	v_mfma_f32_16x16x32_bf16 v[118:121], v[168:171], v[192:195], 0
	v_mfma_f32_16x16x32_bf16 v[114:117], v[176:179], v[192:195], 0
	v_mfma_f32_16x16x32_bf16 v[102:105], v[168:171], v[202:205], 0
	v_mfma_f32_16x16x32_bf16 v[98:101], v[176:179], v[202:205], 0
	v_mfma_f32_16x16x32_bf16 v[86:89], v[168:171], v[210:213], 0
	v_mfma_f32_16x16x32_bf16 v[82:85], v[176:179], v[210:213], 0
	v_mfma_f32_16x16x32_bf16 v[130:133], v[172:175], v[188:191], v[130:133]
	v_mfma_f32_16x16x32_bf16 v[126:129], v[180:183], v[188:191], v[126:129]
	v_mfma_f32_16x16x32_bf16 v[118:121], v[172:175], v[196:199], v[118:121]
	v_mfma_f32_16x16x32_bf16 v[114:117], v[180:183], v[196:199], v[114:117]
	v_mfma_f32_16x16x32_bf16 v[102:105], v[172:175], v[206:209], v[102:105]
	v_mfma_f32_16x16x32_bf16 v[98:101], v[180:183], v[206:209], v[98:101]
	v_mfma_f32_16x16x32_bf16 v[86:89], v[172:175], v[214:217], v[86:89]
	v_mfma_f32_16x16x32_bf16 v[82:85], v[180:183], v[214:217], v[82:85]
	s_barrier
	s_add_i32 s42, 0, 0x18000
	v_add_u32_e32 v2, s42, v135
	s_add_i32 s43, 0, 0x1c000
	ds_read_b128 v[152:155], v2
	ds_read_b128 v[156:159], v2 offset:1024
	ds_read_b128 v[160:163], v2 offset:2048
	ds_read_b128 v[164:167], v2 offset:3072
	v_add_u32_e32 v2, s43, v135
	ds_read_b128 v[168:171], v2
	ds_read_b128 v[172:175], v2 offset:1024
	ds_read_b128 v[176:179], v2 offset:2048
	ds_read_b128 v[180:183], v2 offset:3072
	s_add_u32 s40, s40, 0x80000
	s_addc_u32 s41, s41, 0
	s_mov_b32 m0, s53
	v_lshl_add_u64 v[226:227], s[40:41], 0, v[142:143]
	ds_read_b128 v[184:187], v151 offset:32768
	ds_read_b128 v[188:191], v151 offset:33792
	ds_read_b128 v[192:195], v151 offset:34816
	ds_read_b128 v[196:199], v151 offset:35840
	ds_read_b128 v[202:205], v151 offset:36864
	ds_read_b128 v[206:209], v151 offset:37888
	ds_read_b128 v[210:213], v151 offset:38912
	ds_read_b128 v[214:217], v151 offset:39936
	global_load_lds_dwordx4 v[226:227], off
	v_lshl_add_u64 v[226:227], s[40:41], 0, v[138:139]
	s_mov_b32 m0, s54
	s_nop 0
	global_load_lds_dwordx4 v[226:227], off
	s_waitcnt vmcnt(8)
	s_waitcnt lgkmcnt(0)
	s_barrier
	v_mfma_f32_16x16x32_bf16 v[122:125], v[152:155], v[184:187], v[122:125]
	v_mfma_f32_16x16x32_bf16 v[74:77], v[160:163], v[184:187], v[74:77]
	v_mfma_f32_16x16x32_bf16 v[58:61], v[152:155], v[192:195], v[58:61]
	v_mfma_f32_16x16x32_bf16 v[50:53], v[160:163], v[192:195], v[50:53]
	v_mfma_f32_16x16x32_bf16 v[38:41], v[152:155], v[202:205], v[38:41]
	v_mfma_f32_16x16x32_bf16 v[34:37], v[160:163], v[202:205], v[34:37]
	v_mfma_f32_16x16x32_bf16 v[22:25], v[152:155], v[210:213], v[22:25]
	v_mfma_f32_16x16x32_bf16 v[18:21], v[160:163], v[210:213], v[18:21]
	v_mfma_f32_16x16x32_bf16 v[122:125], v[156:159], v[188:191], v[122:125]
	v_mfma_f32_16x16x32_bf16 v[74:77], v[164:167], v[188:191], v[74:77]
	v_mfma_f32_16x16x32_bf16 v[58:61], v[156:159], v[196:199], v[58:61]
	v_mfma_f32_16x16x32_bf16 v[50:53], v[164:167], v[196:199], v[50:53]
	v_mfma_f32_16x16x32_bf16 v[38:41], v[156:159], v[206:209], v[38:41]
	v_mfma_f32_16x16x32_bf16 v[34:37], v[164:167], v[206:209], v[34:37]
	v_mfma_f32_16x16x32_bf16 v[22:25], v[156:159], v[214:217], v[22:25]
	v_mfma_f32_16x16x32_bf16 v[18:21], v[164:167], v[214:217], v[18:21]
	v_mfma_f32_16x16x32_bf16 v[106:109], v[168:171], v[184:187], v[106:109]
	v_mfma_f32_16x16x32_bf16 v[110:113], v[176:179], v[184:187], v[110:113]
	v_mfma_f32_16x16x32_bf16 v[90:93], v[168:171], v[192:195], v[90:93]
	v_mfma_f32_16x16x32_bf16 v[94:97], v[176:179], v[192:195], v[94:97]
	v_mfma_f32_16x16x32_bf16 v[66:69], v[168:171], v[202:205], v[66:69]
	v_mfma_f32_16x16x32_bf16 v[70:73], v[176:179], v[202:205], v[70:73]
	v_mfma_f32_16x16x32_bf16 v[42:45], v[168:171], v[210:213], v[42:45]
	v_mfma_f32_16x16x32_bf16 v[46:49], v[176:179], v[210:213], v[46:49]
	v_mfma_f32_16x16x32_bf16 v[106:109], v[172:175], v[188:191], v[106:109]
	v_mfma_f32_16x16x32_bf16 v[110:113], v[180:183], v[188:191], v[110:113]
	v_mfma_f32_16x16x32_bf16 v[90:93], v[172:175], v[196:199], v[90:93]
	v_mfma_f32_16x16x32_bf16 v[94:97], v[180:183], v[196:199], v[94:97]
	v_mfma_f32_16x16x32_bf16 v[66:69], v[172:175], v[206:209], v[66:69]
	v_mfma_f32_16x16x32_bf16 v[70:73], v[180:183], v[206:209], v[70:73]
	v_mfma_f32_16x16x32_bf16 v[42:45], v[172:175], v[214:217], v[42:45]
	v_mfma_f32_16x16x32_bf16 v[46:49], v[180:183], v[214:217], v[46:49]
	s_barrier
; #define PG8_STAGE_A(bufoff, base_, nx_, kb_, h_) do { if (GATHER) { if (nx_) PG8_STAGE_G(bufoff, kb_, goN, h_); else PG8_STAGE_G(bufoff, kb_, goC, h_); } \
;         else PG8_STAGE(bufoff, (base_) + (kb_) + (h_) * hstep, voffA); } while (0)
; #define PG8_STAGE(bufoff, gbase, voff) do { _Pragma("unroll") for (int _i = 0; _i < 2; ++_i) \
;         __builtin_amdgcn_global_load_lds((const unsigned*)((const char*)(gbase) + (voff)[_i]), (LAS unsigned*)(lds + (bufoff) + ldsw + _i * 8192), 16, 0, 0); } while (0)
; #define PG8_LDA(dst, b, h) do { _Pragma("unroll") for (int m = 0; m < 4; ++m) _Pragma("unroll") for (int k = 0; k < 2; ++k) dst[m][k] = *(const LAS bf16x8*)(lds + PG8_SA(b, h) + aoff + m * 2048 + k * 1024); } while (0)
; #define PG8_MMA(ai, bj, At, Bt) do { __builtin_amdgcn_s_setprio(1); _Pragma("unroll") for (int m = 0; m < 4; ++m) _Pragma("unroll") for (int n = 0; n < 2; ++n) _Pragma("unroll") for (int k = 0; k < 2; ++k) \
;         acc[ai][bj][m][n] = __builtin_amdgcn_mfma_f32_16x16x32_bf16(Bt[n][k], At[m][k], acc[ai][bj][m][n], 0, 0, 0); __builtin_amdgcn_s_setprio(0); } while (0)
; #define PG8_WAIT_V(n) asm volatile("s_waitcnt vmcnt(" #n ")" ::: "memory")
; #define PG8_WAIT_L(n) asm volatile("s_waitcnt lgkmcnt(" #n ")" ::: "memory")
; #define PG8_BAR __builtin_amdgcn_s_barrier()
; #define PG8_SCHED __builtin_amdgcn_sched_barrier(0)
; template <class Epi, class Sched, bool GATHER = false>
; __device__ __forceinline__ void gemm_phase(LAS unsigned char* lds, const Gemm g, const Sched& S, const Epi& E, const int tid) {
;     ...
;         for (int t = 0; t < nt; t += 2) {
;             const bool last = (t == nt - 2);
;             const char* a1 = cA + (size_t)(t + 1) * kstep;
;             const char* a2 = last ? nA : cA + (size_t)(t + 2) * kstep; const char* b2 = last ? nB : cB + (size_t)(t + 2) * kstep;
;             const char* a3 = a2 + kstep; const char* b3 = b2 + kstep;
;     ...
;             PG8_LDA(At, 1, 1); PG8_STAGE(PG8_SB(1, 0), b3, voffB); PG8_STAGE(PG8_SB(1, 1), b3 + hstep, voffB); PG8_STAGE_A(PG8_SA(1, 0), (last ? nA : cA), last, kb3, 0);
;             PG8_WAIT_V(8); PG8_WAIT_L(0); PG8_BAR; PG8_MMA(1, 0, At, B0); PG8_MMA(1, 1, At, B1); PG8_BAR; PG8_SCHED;
	s_add_i32 s40, s42, s50
	v_lshl_add_u64 v[218:219], v[218:219], 0, s[0:1]
	s_mov_b32 m0, s40
	ds_read_b128 v[184:187], v151 offset:49152
	ds_read_b128 v[188:191], v151 offset:50176
	ds_read_b128 v[192:195], v151 offset:51200
	ds_read_b128 v[196:199], v151 offset:52224
	ds_read_b128 v[202:205], v151 offset:53248
	ds_read_b128 v[206:209], v151 offset:54272
	ds_read_b128 v[210:213], v151 offset:55296
	ds_read_b128 v[214:217], v151 offset:56320
	global_load_lds_dwordx4 v[218:219], off
	s_add_i32 m0, s40, 0x2000
	s_add_u32 s38, s38, 0x80080
	v_lshl_add_u64 v[218:219], v[220:221], 0, s[0:1]
	s_addc_u32 s39, s39, 0
	s_add_i32 s40, s43, s50
	global_load_lds_dwordx4 v[218:219], off
	v_lshl_add_u64 v[218:219], s[38:39], 0, v[140:141]
	s_mov_b32 m0, s40
	s_nop 0
	global_load_lds_dwordx4 v[218:219], off
	v_lshl_add_u64 v[218:219], s[38:39], 0, v[136:137]
	s_add_i32 m0, s40, 0x2000
	s_nop 0
	global_load_lds_dwordx4 v[218:219], off
	v_lshl_add_u64 v[218:219], v[222:223], 0, s[0:1]
	s_mov_b32 m0, s33
	s_nop 0
	global_load_lds_dwordx4 v[218:219], off
	v_lshl_add_u64 v[218:219], v[224:225], 0, s[0:1]
	s_mov_b32 m0, s55
	s_nop 0
	global_load_lds_dwordx4 v[218:219], off
	s_waitcnt vmcnt(8)
	s_waitcnt lgkmcnt(0)
	s_barrier
	v_mfma_f32_16x16x32_bf16 v[30:33], v[152:155], v[184:187], v[30:33]
	v_mfma_f32_16x16x32_bf16 v[26:29], v[160:163], v[184:187], v[26:29]
	v_mfma_f32_16x16x32_bf16 v[14:17], v[152:155], v[192:195], v[14:17]
	v_mfma_f32_16x16x32_bf16 v[10:13], v[160:163], v[192:195], v[10:13]
	v_mfma_f32_16x16x32_bf16 v[6:9], v[152:155], v[202:205], v[6:9]
	v_mfma_f32_16x16x32_bf16 v[78:81], v[160:163], v[202:205], v[78:81]
	v_mfma_f32_16x16x32_bf16 v[62:65], v[152:155], v[210:213], v[62:65]
	v_mfma_f32_16x16x32_bf16 v[54:57], v[160:163], v[210:213], v[54:57]
	v_mfma_f32_16x16x32_bf16 v[30:33], v[156:159], v[188:191], v[30:33]
	v_mfma_f32_16x16x32_bf16 v[26:29], v[164:167], v[188:191], v[26:29]
	v_mfma_f32_16x16x32_bf16 v[14:17], v[156:159], v[196:199], v[14:17]
	v_mfma_f32_16x16x32_bf16 v[10:13], v[164:167], v[196:199], v[10:13]
	v_mfma_f32_16x16x32_bf16 v[6:9], v[156:159], v[206:209], v[6:9]
	v_mfma_f32_16x16x32_bf16 v[78:81], v[164:167], v[206:209], v[78:81]
	v_mfma_f32_16x16x32_bf16 v[62:65], v[156:159], v[214:217], v[62:65]
	v_mfma_f32_16x16x32_bf16 v[54:57], v[164:167], v[214:217], v[54:57]
	v_mfma_f32_16x16x32_bf16 v[130:133], v[168:171], v[184:187], v[130:133]
	v_mfma_f32_16x16x32_bf16 v[126:129], v[176:179], v[184:187], v[126:129]
	v_mfma_f32_16x16x32_bf16 v[118:121], v[168:171], v[192:195], v[118:121]
	v_mfma_f32_16x16x32_bf16 v[114:117], v[176:179], v[192:195], v[114:117]
	v_mfma_f32_16x16x32_bf16 v[102:105], v[168:171], v[202:205], v[102:105]
	v_mfma_f32_16x16x32_bf16 v[98:101], v[176:179], v[202:205], v[98:101]
	v_mfma_f32_16x16x32_bf16 v[86:89], v[168:171], v[210:213], v[86:89]
	v_mfma_f32_16x16x32_bf16 v[82:85], v[176:179], v[210:213], v[82:85]
	v_mfma_f32_16x16x32_bf16 v[130:133], v[172:175], v[188:191], v[130:133]
	v_mfma_f32_16x16x32_bf16 v[126:129], v[180:183], v[188:191], v[126:129]
	v_mfma_f32_16x16x32_bf16 v[118:121], v[172:175], v[196:199], v[118:121]
	v_mfma_f32_16x16x32_bf16 v[114:117], v[180:183], v[196:199], v[114:117]
	v_mfma_f32_16x16x32_bf16 v[102:105], v[172:175], v[206:209], v[102:105]
	v_mfma_f32_16x16x32_bf16 v[98:101], v[180:183], v[206:209], v[98:101]
	v_mfma_f32_16x16x32_bf16 v[86:89], v[172:175], v[214:217], v[86:89]
	v_mfma_f32_16x16x32_bf16 v[82:85], v[180:183], v[214:217], v[82:85]
	s_barrier
	s_add_i32 s61, s61, 2
	s_cmp_gt_u32 s61, 29
	s_mov_b64 s[40:41], s[36:37]
	s_cbranch_scc1 .Lpeel2_exit
.LBB0_1367:
	s_add_u32 s62, s59, s40
	s_addc_u32 s63, s60, s41
	s_add_u32 s36, s40, 0x100
	s_addc_u32 s37, s41, 0
	s_cmp_eq_u32 s61, 28
	s_cselect_b64 s[42:43], -1, 0
	s_and_b64 s[38:39], s[42:43], exec
	s_cselect_b32 s39, s21, s63
	s_cselect_b32 s38, s23, s62
	s_cselect_b32 s62, 0, s36
	s_add_i32 s63, 0, 0x10000
	v_add_u32_e32 v2, s63, v135
	s_add_i32 s64, 0, 0x14000
	ds_read_b128 v[152:155], v2
	ds_read_b128 v[156:159], v2 offset:1024
	ds_read_b128 v[160:163], v2 offset:2048
	ds_read_b128 v[164:167], v2 offset:3072
	v_add_u32_e32 v2, s64, v135
	ds_read_b128 v[168:171], v2
	ds_read_b128 v[172:175], v2 offset:1024
	ds_read_b128 v[176:179], v2 offset:2048
	ds_read_b128 v[180:183], v2 offset:3072
	v_lshl_add_u64 v[218:219], v[4:5], 0, s[40:41]
	s_add_i32 m0, s31, 0xc000
	ds_read_b128 v[184:187], v151
	ds_read_b128 v[188:191], v151 offset:1024
	ds_read_b128 v[192:195], v151 offset:2048
	ds_read_b128 v[196:199], v151 offset:3072
	ds_read_b128 v[202:205], v151 offset:4096
	ds_read_b128 v[206:209], v151 offset:5120
	ds_read_b128 v[210:213], v151 offset:6144
	ds_read_b128 v[214:217], v151 offset:7168
	global_load_lds_dwordx4 v[218:219], off
	v_lshl_add_u64 v[218:219], v[148:149], 0, s[40:41]
	s_add_i32 m0, s31, 0xe000
	s_nop 0
	global_load_lds_dwordx4 v[218:219], off
	s_waitcnt vmcnt(8)
	s_waitcnt lgkmcnt(0)
	s_barrier
; #define PG8_STAGE_A(bufoff, base_, nx_, kb_, h_) do { if (GATHER) { if (nx_) PG8_STAGE_G(bufoff, kb_, goN, h_); else PG8_STAGE_G(bufoff, kb_, goC, h_); } \
;         else PG8_STAGE(bufoff, (base_) + (kb_) + (h_) * hstep, voffA); } while (0)
; #define PG8_STAGE(bufoff, gbase, voff) do { _Pragma("unroll") for (int _i = 0; _i < 2; ++_i) \
;         __builtin_amdgcn_global_load_lds((const unsigned*)((const char*)(gbase) + (voff)[_i]), (LAS unsigned*)(lds + (bufoff) + ldsw + _i * 8192), 16, 0, 0); } while (0)
; #define PG8_LDA(dst, b, h) do { _Pragma("unroll") for (int m = 0; m < 4; ++m) _Pragma("unroll") for (int k = 0; k < 2; ++k) dst[m][k] = *(const LAS bf16x8*)(lds + PG8_SA(b, h) + aoff + m * 2048 + k * 1024); } while (0)
; #define PG8_LDB(dst, b, h) do { _Pragma("unroll") for (int n = 0; n < 2; ++n) _Pragma("unroll") for (int k = 0; k < 2; ++k) dst[n][k] = *(const LAS bf16x8*)(lds + PG8_SB(b, h) + boff + n * 2048 + k * 1024); } while (0)
; #define PG8_WAIT_V(n) asm volatile("s_waitcnt vmcnt(" #n ")" ::: "memory")
; #define PG8_WAIT_L(n) asm volatile("s_waitcnt lgkmcnt(" #n ")" ::: "memory")
; template <class Epi, class Sched, bool GATHER = false>
; __device__ __forceinline__ void gemm_phase(LAS unsigned char* lds, const Gemm g, const Sched& S, const Epi& E, const int tid) {
;     ...
;             PG8_LDB(B0, 0, 0); PG8_LDB(B1, 0, 1); PG8_SCHED; PG8_LDA(At, 0, 0); PG8_STAGE_A(PG8_SA(1, 1), cA, false, kb1, 1);
;             PG8_WAIT_V(8); PG8_WAIT_L(0); PG8_BAR; PG8_MMA(0, 0, At, B0); PG8_MMA(0, 1, At, B1); PG8_BAR; PG8_SCHED;
;             PG8_LDA(At, 0, 1); PG8_STAGE(PG8_SB(0, 0), b2, voffB); PG8_STAGE(PG8_SB(0, 1), b2 + hstep, voffB); PG8_STAGE_A(PG8_SA(0, 0), (last ? nA : cA), last, kb2, 0);
;             PG8_WAIT_V(8); PG8_WAIT_L(0); PG8_BAR; PG8_MMA(1, 0, At, B0); PG8_MMA(1, 1, At, B1); PG8_BAR; PG8_SCHED;
;             PG8_LDB(B0, 1, 0); PG8_LDB(B1, 1, 1); PG8_SCHED; PG8_LDA(At, 1, 0); PG8_STAGE_A(PG8_SA(0, 1), (last ? nA : cA), last, kb2, 1);
;             PG8_WAIT_V(8); PG8_WAIT_L(0); PG8_BAR; PG8_MMA(0, 0, At, B0); PG8_MMA(0, 1, At, B1); PG8_BAR; PG8_SCHED;
;             PG8_LDA(At, 1, 1); PG8_STAGE(PG8_SB(1, 0), b3, voffB); PG8_STAGE(PG8_SB(1, 1), b3 + hstep, voffB); PG8_STAGE_A(PG8_SA(1, 0), (last ? nA : cA), last, kb3, 0);
;             PG8_WAIT_V(8); PG8_WAIT_L(0); PG8_BAR; PG8_MMA(1, 0, At, B0); PG8_MMA(1, 1, At, B1); PG8_BAR; PG8_SCHED;
	v_mfma_f32_16x16x32_bf16 v[122:125], v[152:155], v[184:187], v[122:125]
	v_mfma_f32_16x16x32_bf16 v[74:77], v[160:163], v[184:187], v[74:77]
	v_mfma_f32_16x16x32_bf16 v[58:61], v[152:155], v[192:195], v[58:61]
	v_mfma_f32_16x16x32_bf16 v[50:53], v[160:163], v[192:195], v[50:53]
	v_mfma_f32_16x16x32_bf16 v[38:41], v[152:155], v[202:205], v[38:41]
	v_mfma_f32_16x16x32_bf16 v[34:37], v[160:163], v[202:205], v[34:37]
	v_mfma_f32_16x16x32_bf16 v[22:25], v[152:155], v[210:213], v[22:25]
	v_mfma_f32_16x16x32_bf16 v[18:21], v[160:163], v[210:213], v[18:21]
	v_mfma_f32_16x16x32_bf16 v[122:125], v[156:159], v[188:191], v[122:125]
	v_mfma_f32_16x16x32_bf16 v[74:77], v[164:167], v[188:191], v[74:77]
	v_mfma_f32_16x16x32_bf16 v[58:61], v[156:159], v[196:199], v[58:61]
	v_mfma_f32_16x16x32_bf16 v[50:53], v[164:167], v[196:199], v[50:53]
	v_mfma_f32_16x16x32_bf16 v[38:41], v[156:159], v[206:209], v[38:41]
	v_mfma_f32_16x16x32_bf16 v[34:37], v[164:167], v[206:209], v[34:37]
	v_mfma_f32_16x16x32_bf16 v[22:25], v[156:159], v[214:217], v[22:25]
	v_mfma_f32_16x16x32_bf16 v[18:21], v[164:167], v[214:217], v[18:21]
	v_mfma_f32_16x16x32_bf16 v[106:109], v[168:171], v[184:187], v[106:109]
	v_mfma_f32_16x16x32_bf16 v[110:113], v[176:179], v[184:187], v[110:113]
	v_mfma_f32_16x16x32_bf16 v[90:93], v[168:171], v[192:195], v[90:93]
	v_mfma_f32_16x16x32_bf16 v[94:97], v[176:179], v[192:195], v[94:97]
	v_mfma_f32_16x16x32_bf16 v[66:69], v[168:171], v[202:205], v[66:69]
	v_mfma_f32_16x16x32_bf16 v[70:73], v[176:179], v[202:205], v[70:73]
	v_mfma_f32_16x16x32_bf16 v[42:45], v[168:171], v[210:213], v[42:45]
	v_mfma_f32_16x16x32_bf16 v[46:49], v[176:179], v[210:213], v[46:49]
	v_mfma_f32_16x16x32_bf16 v[106:109], v[172:175], v[188:191], v[106:109]
	v_mfma_f32_16x16x32_bf16 v[110:113], v[180:183], v[188:191], v[110:113]
	v_mfma_f32_16x16x32_bf16 v[90:93], v[172:175], v[196:199], v[90:93]
	v_mfma_f32_16x16x32_bf16 v[94:97], v[180:183], v[196:199], v[94:97]
	v_mfma_f32_16x16x32_bf16 v[66:69], v[172:175], v[206:209], v[66:69]
	v_mfma_f32_16x16x32_bf16 v[70:73], v[180:183], v[206:209], v[70:73]
	v_mfma_f32_16x16x32_bf16 v[42:45], v[172:175], v[214:217], v[42:45]
	v_mfma_f32_16x16x32_bf16 v[46:49], v[180:183], v[214:217], v[46:49]
	s_barrier
	s_add_i32 s40, s63, s50
	v_lshl_add_u64 v[218:219], s[38:39], 0, v[140:141]
	s_mov_b32 m0, s40
	ds_read_b128 v[184:187], v151 offset:16384
	ds_read_b128 v[188:191], v151 offset:17408
	ds_read_b128 v[192:195], v151 offset:18432
	ds_read_b128 v[196:199], v151 offset:19456
	ds_read_b128 v[202:205], v151 offset:20480
	ds_read_b128 v[206:209], v151 offset:21504
	ds_read_b128 v[210:213], v151 offset:22528
	ds_read_b128 v[214:217], v151 offset:23552
	global_load_lds_dwordx4 v[218:219], off
	s_add_i32 m0, s40, 0x2000
	s_add_u32 s40, s38, 0x80000
	v_lshl_add_u64 v[220:221], s[38:39], 0, v[136:137]
	s_addc_u32 s41, s39, 0
	s_add_i32 s63, s64, s50
	global_load_lds_dwordx4 v[220:221], off
	v_lshl_add_u64 v[222:223], s[40:41], 0, v[140:141]
	s_mov_b32 m0, s63
	s_nop 0
	global_load_lds_dwordx4 v[222:223], off
	v_lshl_add_u64 v[222:223], s[40:41], 0, v[136:137]
	s_add_i32 m0, s63, 0x2000
	s_and_b64 s[40:41], s[8:9], s[42:43]
	s_and_b64 s[40:41], s[40:41], exec
	s_cselect_b32 s40, s24, s34
	s_cselect_b32 s41, s25, s35
	s_add_u32 s40, s40, s62
	s_addc_u32 s41, s41, 0
	global_load_lds_dwordx4 v[222:223], off
	v_lshl_add_u64 v[222:223], s[40:41], 0, v[142:143]
	s_mov_b32 m0, s31
	v_lshl_add_u64 v[224:225], s[40:41], 0, v[138:139]
	global_load_lds_dwordx4 v[222:223], off
	s_mov_b32 m0, s52
	s_nop 0
	global_load_lds_dwordx4 v[224:225], off
	s_waitcnt vmcnt(8)
	s_waitcnt lgkmcnt(0)
	s_barrier
	v_mfma_f32_16x16x32_bf16 v[30:33], v[152:155], v[184:187], v[30:33]
	v_mfma_f32_16x16x32_bf16 v[26:29], v[160:163], v[184:187], v[26:29]
	v_mfma_f32_16x16x32_bf16 v[14:17], v[152:155], v[192:195], v[14:17]
	v_mfma_f32_16x16x32_bf16 v[10:13], v[160:163], v[192:195], v[10:13]
	v_mfma_f32_16x16x32_bf16 v[6:9], v[152:155], v[202:205], v[6:9]
	v_mfma_f32_16x16x32_bf16 v[78:81], v[160:163], v[202:205], v[78:81]
	v_mfma_f32_16x16x32_bf16 v[62:65], v[152:155], v[210:213], v[62:65]
	v_mfma_f32_16x16x32_bf16 v[54:57], v[160:163], v[210:213], v[54:57]
	v_mfma_f32_16x16x32_bf16 v[30:33], v[156:159], v[188:191], v[30:33]
	v_mfma_f32_16x16x32_bf16 v[26:29], v[164:167], v[188:191], v[26:29]
	v_mfma_f32_16x16x32_bf16 v[14:17], v[156:159], v[196:199], v[14:17]
	v_mfma_f32_16x16x32_bf16 v[10:13], v[164:167], v[196:199], v[10:13]
	v_mfma_f32_16x16x32_bf16 v[6:9], v[156:159], v[206:209], v[6:9]
	v_mfma_f32_16x16x32_bf16 v[78:81], v[164:167], v[206:209], v[78:81]
	v_mfma_f32_16x16x32_bf16 v[62:65], v[156:159], v[214:217], v[62:65]
	v_mfma_f32_16x16x32_bf16 v[54:57], v[164:167], v[214:217], v[54:57]
	v_mfma_f32_16x16x32_bf16 v[130:133], v[168:171], v[184:187], v[130:133]
	v_mfma_f32_16x16x32_bf16 v[126:129], v[176:179], v[184:187], v[126:129]
	v_mfma_f32_16x16x32_bf16 v[118:121], v[168:171], v[192:195], v[118:121]
	v_mfma_f32_16x16x32_bf16 v[114:117], v[176:179], v[192:195], v[114:117]
	v_mfma_f32_16x16x32_bf16 v[102:105], v[168:171], v[202:205], v[102:105]
	v_mfma_f32_16x16x32_bf16 v[98:101], v[176:179], v[202:205], v[98:101]
	v_mfma_f32_16x16x32_bf16 v[86:89], v[168:171], v[210:213], v[86:89]
	v_mfma_f32_16x16x32_bf16 v[82:85], v[176:179], v[210:213], v[82:85]
	v_mfma_f32_16x16x32_bf16 v[130:133], v[172:175], v[188:191], v[130:133]
	v_mfma_f32_16x16x32_bf16 v[126:129], v[180:183], v[188:191], v[126:129]
	v_mfma_f32_16x16x32_bf16 v[118:121], v[172:175], v[196:199], v[118:121]
	v_mfma_f32_16x16x32_bf16 v[114:117], v[180:183], v[196:199], v[114:117]
	v_mfma_f32_16x16x32_bf16 v[102:105], v[172:175], v[206:209], v[102:105]
	v_mfma_f32_16x16x32_bf16 v[98:101], v[180:183], v[206:209], v[98:101]
	v_mfma_f32_16x16x32_bf16 v[86:89], v[172:175], v[214:217], v[86:89]
	v_mfma_f32_16x16x32_bf16 v[82:85], v[180:183], v[214:217], v[82:85]
	s_barrier
; #define PG8_STAGE_A(bufoff, base_, nx_, kb_, h_) do { if (GATHER) { if (nx_) PG8_STAGE_G(bufoff, kb_, goN, h_); else PG8_STAGE_G(bufoff, kb_, goC, h_); } \
;         else PG8_STAGE(bufoff, (base_) + (kb_) + (h_) * hstep, voffA); } while (0)
; #define PG8_STAGE(bufoff, gbase, voff) do { _Pragma("unroll") for (int _i = 0; _i < 2; ++_i) \
;         __builtin_amdgcn_global_load_lds((const unsigned*)((const char*)(gbase) + (voff)[_i]), (LAS unsigned*)(lds + (bufoff) + ldsw + _i * 8192), 16, 0, 0); } while (0)
; #define PG8_LDA(dst, b, h) do { _Pragma("unroll") for (int m = 0; m < 4; ++m) _Pragma("unroll") for (int k = 0; k < 2; ++k) dst[m][k] = *(const LAS bf16x8*)(lds + PG8_SA(b, h) + aoff + m * 2048 + k * 1024); } while (0)
; #define PG8_LDB(dst, b, h) do { _Pragma("unroll") for (int n = 0; n < 2; ++n) _Pragma("unroll") for (int k = 0; k < 2; ++k) dst[n][k] = *(const LAS bf16x8*)(lds + PG8_SB(b, h) + boff + n * 2048 + k * 1024); } while (0)
; #define PG8_MMA(ai, bj, At, Bt) do { __builtin_amdgcn_s_setprio(1); _Pragma("unroll") for (int m = 0; m < 4; ++m) _Pragma("unroll") for (int n = 0; n < 2; ++n) _Pragma("unroll") for (int k = 0; k < 2; ++k) \
;         acc[ai][bj][m][n] = __builtin_amdgcn_mfma_f32_16x16x32_bf16(Bt[n][k], At[m][k], acc[ai][bj][m][n], 0, 0, 0); __builtin_amdgcn_s_setprio(0); } while (0)
; #define PG8_WAIT_V(n) asm volatile("s_waitcnt vmcnt(" #n ")" ::: "memory")
; #define PG8_WAIT_L(n) asm volatile("s_waitcnt lgkmcnt(" #n ")" ::: "memory")
; #define PG8_BAR __builtin_amdgcn_s_barrier()
; #define PG8_SCHED __builtin_amdgcn_sched_barrier(0)
; template <class Epi, class Sched, bool GATHER = false>
; __device__ __forceinline__ void gemm_phase(LAS unsigned char* lds, const Gemm g, const Sched& S, const Epi& E, const int tid) {
;     ...
;             PG8_LDB(B0, 1, 0); PG8_LDB(B1, 1, 1); PG8_SCHED; PG8_LDA(At, 1, 0); PG8_STAGE_A(PG8_SA(0, 1), (last ? nA : cA), last, kb2, 1);
;             PG8_WAIT_V(8); PG8_WAIT_L(0); PG8_BAR; PG8_MMA(0, 0, At, B0); PG8_MMA(0, 1, At, B1); PG8_BAR; PG8_SCHED;
;             PG8_LDA(At, 1, 1); PG8_STAGE(PG8_SB(1, 0), b3, voffB); PG8_STAGE(PG8_SB(1, 1), b3 + hstep, voffB); PG8_STAGE_A(PG8_SA(1, 0), (last ? nA : cA), last, kb3, 0);
;             PG8_WAIT_V(8); PG8_WAIT_L(0); PG8_BAR; PG8_MMA(1, 0, At, B0); PG8_MMA(1, 1, At, B1); PG8_BAR; PG8_SCHED;
	s_add_i32 s42, 0, 0x18000
	v_add_u32_e32 v2, s42, v135
	s_add_i32 s43, 0, 0x1c000
	ds_read_b128 v[152:155], v2
	ds_read_b128 v[156:159], v2 offset:1024
	ds_read_b128 v[160:163], v2 offset:2048
	ds_read_b128 v[164:167], v2 offset:3072
	v_add_u32_e32 v2, s43, v135
	ds_read_b128 v[168:171], v2
	ds_read_b128 v[172:175], v2 offset:1024
	ds_read_b128 v[176:179], v2 offset:2048
	ds_read_b128 v[180:183], v2 offset:3072
	s_add_u32 s40, s40, 0x80000
	s_addc_u32 s41, s41, 0
	s_mov_b32 m0, s53
	v_lshl_add_u64 v[226:227], s[40:41], 0, v[142:143]
	ds_read_b128 v[184:187], v151 offset:32768
	ds_read_b128 v[188:191], v151 offset:33792
	ds_read_b128 v[192:195], v151 offset:34816
	ds_read_b128 v[196:199], v151 offset:35840
	ds_read_b128 v[202:205], v151 offset:36864
	ds_read_b128 v[206:209], v151 offset:37888
	ds_read_b128 v[210:213], v151 offset:38912
	ds_read_b128 v[214:217], v151 offset:39936
	global_load_lds_dwordx4 v[226:227], off
	v_lshl_add_u64 v[226:227], s[40:41], 0, v[138:139]
	s_mov_b32 m0, s54
	s_nop 0
	global_load_lds_dwordx4 v[226:227], off
	s_waitcnt vmcnt(8)
	s_waitcnt lgkmcnt(0)
	s_barrier
	v_mfma_f32_16x16x32_bf16 v[122:125], v[152:155], v[184:187], v[122:125]
	v_mfma_f32_16x16x32_bf16 v[74:77], v[160:163], v[184:187], v[74:77]
	v_mfma_f32_16x16x32_bf16 v[58:61], v[152:155], v[192:195], v[58:61]
	v_mfma_f32_16x16x32_bf16 v[50:53], v[160:163], v[192:195], v[50:53]
	v_mfma_f32_16x16x32_bf16 v[38:41], v[152:155], v[202:205], v[38:41]
	v_mfma_f32_16x16x32_bf16 v[34:37], v[160:163], v[202:205], v[34:37]
	v_mfma_f32_16x16x32_bf16 v[22:25], v[152:155], v[210:213], v[22:25]
	v_mfma_f32_16x16x32_bf16 v[18:21], v[160:163], v[210:213], v[18:21]
	v_mfma_f32_16x16x32_bf16 v[122:125], v[156:159], v[188:191], v[122:125]
	v_mfma_f32_16x16x32_bf16 v[74:77], v[164:167], v[188:191], v[74:77]
	v_mfma_f32_16x16x32_bf16 v[58:61], v[156:159], v[196:199], v[58:61]
	v_mfma_f32_16x16x32_bf16 v[50:53], v[164:167], v[196:199], v[50:53]
	v_mfma_f32_16x16x32_bf16 v[38:41], v[156:159], v[206:209], v[38:41]
	v_mfma_f32_16x16x32_bf16 v[34:37], v[164:167], v[206:209], v[34:37]
	v_mfma_f32_16x16x32_bf16 v[22:25], v[156:159], v[214:217], v[22:25]
	v_mfma_f32_16x16x32_bf16 v[18:21], v[164:167], v[214:217], v[18:21]
	v_mfma_f32_16x16x32_bf16 v[106:109], v[168:171], v[184:187], v[106:109]
	v_mfma_f32_16x16x32_bf16 v[110:113], v[176:179], v[184:187], v[110:113]
	v_mfma_f32_16x16x32_bf16 v[90:93], v[168:171], v[192:195], v[90:93]
	v_mfma_f32_16x16x32_bf16 v[94:97], v[176:179], v[192:195], v[94:97]
	v_mfma_f32_16x16x32_bf16 v[66:69], v[168:171], v[202:205], v[66:69]
	v_mfma_f32_16x16x32_bf16 v[70:73], v[176:179], v[202:205], v[70:73]
	v_mfma_f32_16x16x32_bf16 v[42:45], v[168:171], v[210:213], v[42:45]
	v_mfma_f32_16x16x32_bf16 v[46:49], v[176:179], v[210:213], v[46:49]
	v_mfma_f32_16x16x32_bf16 v[106:109], v[172:175], v[188:191], v[106:109]
	v_mfma_f32_16x16x32_bf16 v[110:113], v[180:183], v[188:191], v[110:113]
	v_mfma_f32_16x16x32_bf16 v[90:93], v[172:175], v[196:199], v[90:93]
	v_mfma_f32_16x16x32_bf16 v[94:97], v[180:183], v[196:199], v[94:97]
	v_mfma_f32_16x16x32_bf16 v[66:69], v[172:175], v[206:209], v[66:69]
	v_mfma_f32_16x16x32_bf16 v[70:73], v[180:183], v[206:209], v[70:73]
	v_mfma_f32_16x16x32_bf16 v[42:45], v[172:175], v[214:217], v[42:45]
	v_mfma_f32_16x16x32_bf16 v[46:49], v[180:183], v[214:217], v[46:49]
	s_barrier
	s_add_i32 s40, s42, s50
	v_lshl_add_u64 v[218:219], v[218:219], 0, s[0:1]
	s_mov_b32 m0, s40
	ds_read_b128 v[184:187], v151 offset:49152
	ds_read_b128 v[188:191], v151 offset:50176
	ds_read_b128 v[192:195], v151 offset:51200
	ds_read_b128 v[196:199], v151 offset:52224
	ds_read_b128 v[202:205], v151 offset:53248
	ds_read_b128 v[206:209], v151 offset:54272
	ds_read_b128 v[210:213], v151 offset:55296
	ds_read_b128 v[214:217], v151 offset:56320
	global_load_lds_dwordx4 v[218:219], off
	s_add_i32 m0, s40, 0x2000
	s_add_u32 s38, s38, 0x80080
	v_lshl_add_u64 v[218:219], v[220:221], 0, s[0:1]
	s_addc_u32 s39, s39, 0
	s_add_i32 s40, s43, s50
	global_load_lds_dwordx4 v[218:219], off
	v_lshl_add_u64 v[218:219], s[38:39], 0, v[140:141]
	s_mov_b32 m0, s40
	s_nop 0
	global_load_lds_dwordx4 v[218:219], off
	v_lshl_add_u64 v[218:219], s[38:39], 0, v[136:137]
	s_add_i32 m0, s40, 0x2000
	s_nop 0
	global_load_lds_dwordx4 v[218:219], off
	v_lshl_add_u64 v[218:219], v[222:223], 0, s[0:1]
	s_mov_b32 m0, s33
	s_nop 0
	global_load_lds_dwordx4 v[218:219], off
	v_lshl_add_u64 v[218:219], v[224:225], 0, s[0:1]
	s_mov_b32 m0, s55
	s_nop 0
	global_load_lds_dwordx4 v[218:219], off
	s_waitcnt vmcnt(8)
	s_waitcnt lgkmcnt(0)
	s_barrier
	v_mfma_f32_16x16x32_bf16 v[30:33], v[152:155], v[184:187], v[30:33]
	v_mfma_f32_16x16x32_bf16 v[26:29], v[160:163], v[184:187], v[26:29]
	v_mfma_f32_16x16x32_bf16 v[14:17], v[152:155], v[192:195], v[14:17]
	v_mfma_f32_16x16x32_bf16 v[10:13], v[160:163], v[192:195], v[10:13]
	v_mfma_f32_16x16x32_bf16 v[6:9], v[152:155], v[202:205], v[6:9]
	v_mfma_f32_16x16x32_bf16 v[78:81], v[160:163], v[202:205], v[78:81]
	v_mfma_f32_16x16x32_bf16 v[62:65], v[152:155], v[210:213], v[62:65]
	v_mfma_f32_16x16x32_bf16 v[54:57], v[160:163], v[210:213], v[54:57]
	v_mfma_f32_16x16x32_bf16 v[30:33], v[156:159], v[188:191], v[30:33]
	v_mfma_f32_16x16x32_bf16 v[26:29], v[164:167], v[188:191], v[26:29]
	v_mfma_f32_16x16x32_bf16 v[14:17], v[156:159], v[196:199], v[14:17]
	v_mfma_f32_16x16x32_bf16 v[10:13], v[164:167], v[196:199], v[10:13]
	v_mfma_f32_16x16x32_bf16 v[6:9], v[156:159], v[206:209], v[6:9]
	v_mfma_f32_16x16x32_bf16 v[78:81], v[164:167], v[206:209], v[78:81]
	v_mfma_f32_16x16x32_bf16 v[62:65], v[156:159], v[214:217], v[62:65]
	v_mfma_f32_16x16x32_bf16 v[54:57], v[164:167], v[214:217], v[54:57]
	v_mfma_f32_16x16x32_bf16 v[130:133], v[168:171], v[184:187], v[130:133]
	v_mfma_f32_16x16x32_bf16 v[126:129], v[176:179], v[184:187], v[126:129]
	v_mfma_f32_16x16x32_bf16 v[118:121], v[168:171], v[192:195], v[118:121]
	v_mfma_f32_16x16x32_bf16 v[114:117], v[176:179], v[192:195], v[114:117]
	v_mfma_f32_16x16x32_bf16 v[102:105], v[168:171], v[202:205], v[102:105]
	v_mfma_f32_16x16x32_bf16 v[98:101], v[176:179], v[202:205], v[98:101]
	v_mfma_f32_16x16x32_bf16 v[86:89], v[168:171], v[210:213], v[86:89]
	v_mfma_f32_16x16x32_bf16 v[82:85], v[176:179], v[210:213], v[82:85]
	v_mfma_f32_16x16x32_bf16 v[130:133], v[172:175], v[188:191], v[130:133]
	v_mfma_f32_16x16x32_bf16 v[126:129], v[180:183], v[188:191], v[126:129]
	v_mfma_f32_16x16x32_bf16 v[118:121], v[172:175], v[196:199], v[118:121]
	v_mfma_f32_16x16x32_bf16 v[114:117], v[180:183], v[196:199], v[114:117]
	v_mfma_f32_16x16x32_bf16 v[102:105], v[172:175], v[206:209], v[102:105]
	v_mfma_f32_16x16x32_bf16 v[98:101], v[180:183], v[206:209], v[98:101]
	v_mfma_f32_16x16x32_bf16 v[86:89], v[172:175], v[214:217], v[86:89]
	v_mfma_f32_16x16x32_bf16 v[82:85], v[180:183], v[214:217], v[82:85]
	s_barrier
	s_add_i32 s61, s61, 2
	s_cmp_gt_u32 s61, 29
	s_mov_b64 s[40:41], s[36:37]
	s_cbranch_scc0 .LBB0_1367

; template <class Epi, class Sched, bool GATHER = false>
; __device__ __forceinline__ void gemm_phase(LAS unsigned char* lds, const Gemm g, const Sched& S, const Epi& E, const int tid) {
;     ...
;         const bool has_next = S.next(ui + 1, nxt);
;         const char* nA = has_next ? (const char*)g.A + (size_t)nxt.pm * tstep : cA; const char* nB = has_next ? (const char*)g.Bt + (size_t)nxt.pb * tstep : cB;
;         if (GATHER && has_next && wid < 4) __builtin_amdgcn_global_load_lds((const unsigned*)(g.rowmap + nxt.rb + tid), (LAS unsigned*)(lds + STAGE_BYTES + ((ui + 1) & 1) * 1024 + wid * 256), 4, 0, 0);
;         for (int t = 0; t < nt; t += 2) {
;             const bool last = (t == nt - 2);
;             const char* a1 = cA + (size_t)(t + 1) * kstep;
;             const char* a2 = last ? nA : cA + (size_t)(t + 2) * kstep; const char* b2 = last ? nB : cB + (size_t)(t + 2) * kstep;
;             const char* a3 = a2 + kstep; const char* b3 = b2 + kstep;
;     ...
;             PG8_LDB(B0, 0, 0); PG8_SCHED; PG8_LDA(At, 0, 0); PG8_STAGE(PG8_SA(1, 1), a1 + hstep, voffA);
;             PG8_WAIT_L(8); PG8_BAR; PG8_WAIT_L(0); PG8_MMA(0, 0, At, B0); PG8_BAR; PG8_SCHED;
;             PG8_LDB(B1, 0, 1); PG8_STAGE(PG8_SB(0, 0), b2, voffB);
;             PG8_BAR; PG8_WAIT_L(0); PG8_MMA(0, 1, At, B1); PG8_BAR;
;             PG8_LDA(At, 0, 1); PG8_STAGE(PG8_SA(0, 0), a2, voffA);
;             PG8_BAR; PG8_WAIT_L(0); PG8_MMA(1, 0, At, B0); PG8_BAR; PG8_SCHED;
;             PG8_STAGE(PG8_SB(0, 1), b2 + hstep, voffB);
;             PG8_WAIT_V(6); PG8_BAR; PG8_MMA(1, 1, At, B1); PG8_BAR;
;             PG8_LDB(B0, 1, 0); PG8_SCHED; PG8_LDA(At, 1, 0); PG8_STAGE(PG8_SA(0, 1), a2 + hstep, voffA);
;             PG8_WAIT_L(8); PG8_BAR; PG8_WAIT_L(0); PG8_MMA(0, 0, At, B0); PG8_BAR; PG8_SCHED;
;             PG8_LDB(B1, 1, 1); PG8_STAGE(PG8_SB(1, 0), b3, voffB);
;             PG8_BAR; PG8_WAIT_L(0); PG8_MMA(0, 1, At, B1); PG8_BAR;
;             PG8_LDA(At, 1, 1); PG8_STAGE(PG8_SA(1, 0), a3, voffA);
;             PG8_BAR; PG8_WAIT_L(0); PG8_MMA(1, 0, At, B0); PG8_BAR; PG8_SCHED;
;             PG8_STAGE(PG8_SB(1, 1), b3 + hstep, voffB);
;             PG8_WAIT_V(6); PG8_BAR; PG8_MMA(1, 1, At, B1); PG8_BAR;
;     ...
;             if (GATHER && last && has_next) {
;                 const LAS int* ib_ = (const LAS int*)(lds + STAGE_BYTES + ((ui + 1) & 1) * 1024);
; #pragma unroll
.LBB0_1482:
	s_add_u32 s56, s28, 0x100
	s_addc_u32 s57, s29, 0
	s_add_u32 s28, s14, 0x160080
	s_addc_u32 s29, s15, 0
	v_lshl_add_u64 v[4:5], s[28:29], 0, v[142:143]
	v_lshl_add_u64 v[146:147], s[28:29], 0, v[144:145]
	s_mov_b32 s58, -2
	s_mov_b64 s[34:35], 0
	s_add_u32 s28, s34, 0x100
	s_addc_u32 s29, s35, 0
	s_add_u32 s30, s56, s34
	s_addc_u32 s31, s57, s35
	s_add_i32 s59, 0, 0x10000
	s_add_i32 s60, 0, 0x14000
	v_add_u32_e32 v2, s59, v149
	ds_read_b128 v[152:155], v2
	ds_read_b128 v[156:159], v2 offset:1024
	ds_read_b128 v[160:163], v2 offset:2048
	ds_read_b128 v[164:167], v2 offset:3072
	v_add_u32_e32 v2, s60, v149
	ds_read_b128 v[168:171], v2
	ds_read_b128 v[172:175], v2 offset:1024
	ds_read_b128 v[176:179], v2 offset:2048
	ds_read_b128 v[180:183], v2 offset:3072
	s_add_i32 s62, s59, s33
	s_add_i32 m0, s44, 0xc000
	s_add_i32 s61, s44, 0xe000
	s_add_i32 s59, s62, 0x2000
	s_cmpk_eq_i32 s58, 0x54
	s_cselect_b32 s31, s25, s31
	s_cselect_b32 s30, s24, s30
	v_lshl_add_u64 v[218:219], v[4:5], 0, s[34:35]
	ds_read_b128 v[184:187], v151
	ds_read_b128 v[188:191], v151 offset:1024
	ds_read_b128 v[192:195], v151 offset:2048
	ds_read_b128 v[196:199], v151 offset:3072
	ds_read_b128 v[202:205], v151 offset:4096
	ds_read_b128 v[206:209], v151 offset:5120
	ds_read_b128 v[210:213], v151 offset:6144
	ds_read_b128 v[214:217], v151 offset:7168
	global_load_lds_dwordx4 v[218:219], off
	v_lshl_add_u64 v[218:219], v[146:147], 0, s[34:35]
	s_mov_b32 m0, s61
	s_nop 0
	global_load_lds_dwordx4 v[218:219], off
	s_waitcnt vmcnt(8)
	s_waitcnt lgkmcnt(0)
	s_barrier
	v_mfma_f32_16x16x32_bf16 v[86:89], v[152:155], v[184:187], 0
	v_mfma_f32_16x16x32_bf16 v[18:21], v[160:163], v[184:187], 0
	v_mfma_f32_16x16x32_bf16 v[6:9], v[152:155], v[192:195], 0
	v_mfma_f32_16x16x32_bf16 v[22:25], v[160:163], v[192:195], 0
	v_mfma_f32_16x16x32_bf16 v[10:13], v[152:155], v[202:205], 0
	v_mfma_f32_16x16x32_bf16 v[26:29], v[160:163], v[202:205], 0
	v_mfma_f32_16x16x32_bf16 v[14:17], v[152:155], v[210:213], 0
	v_mfma_f32_16x16x32_bf16 v[30:33], v[160:163], v[210:213], 0
	v_mfma_f32_16x16x32_bf16 v[86:89], v[156:159], v[188:191], v[86:89]
	v_mfma_f32_16x16x32_bf16 v[18:21], v[164:167], v[188:191], v[18:21]
	v_mfma_f32_16x16x32_bf16 v[6:9], v[156:159], v[196:199], v[6:9]
	v_mfma_f32_16x16x32_bf16 v[22:25], v[164:167], v[196:199], v[22:25]
	v_mfma_f32_16x16x32_bf16 v[10:13], v[156:159], v[206:209], v[10:13]
	v_mfma_f32_16x16x32_bf16 v[26:29], v[164:167], v[206:209], v[26:29]
	v_mfma_f32_16x16x32_bf16 v[14:17], v[156:159], v[214:217], v[14:17]
	v_mfma_f32_16x16x32_bf16 v[30:33], v[164:167], v[214:217], v[30:33]
	v_mfma_f32_16x16x32_bf16 v[34:37], v[168:171], v[184:187], 0
	v_mfma_f32_16x16x32_bf16 v[50:53], v[176:179], v[184:187], 0
	v_mfma_f32_16x16x32_bf16 v[38:41], v[168:171], v[192:195], 0
	v_mfma_f32_16x16x32_bf16 v[54:57], v[176:179], v[192:195], 0
	v_mfma_f32_16x16x32_bf16 v[42:45], v[168:171], v[202:205], 0
	v_mfma_f32_16x16x32_bf16 v[62:65], v[176:179], v[202:205], 0
	v_mfma_f32_16x16x32_bf16 v[46:49], v[168:171], v[210:213], 0
	v_mfma_f32_16x16x32_bf16 v[70:73], v[176:179], v[210:213], 0
	v_mfma_f32_16x16x32_bf16 v[34:37], v[172:175], v[188:191], v[34:37]
	v_mfma_f32_16x16x32_bf16 v[50:53], v[180:183], v[188:191], v[50:53]
	v_mfma_f32_16x16x32_bf16 v[38:41], v[172:175], v[196:199], v[38:41]
	v_mfma_f32_16x16x32_bf16 v[54:57], v[180:183], v[196:199], v[54:57]
	v_mfma_f32_16x16x32_bf16 v[42:45], v[172:175], v[206:209], v[42:45]
	v_mfma_f32_16x16x32_bf16 v[62:65], v[180:183], v[206:209], v[62:65]
	v_mfma_f32_16x16x32_bf16 v[46:49], v[172:175], v[214:217], v[46:49]
	v_mfma_f32_16x16x32_bf16 v[70:73], v[180:183], v[214:217], v[70:73]
	s_barrier
	s_mov_b32 m0, s62
	v_lshl_add_u64 v[218:219], s[30:31], 0, v[136:137]
	ds_read_b128 v[184:187], v151 offset:16384
	ds_read_b128 v[188:191], v151 offset:17408
	ds_read_b128 v[192:195], v151 offset:18432
	ds_read_b128 v[196:199], v151 offset:19456
	ds_read_b128 v[202:205], v151 offset:20480
	ds_read_b128 v[206:209], v151 offset:21504
	ds_read_b128 v[210:213], v151 offset:22528
	ds_read_b128 v[214:217], v151 offset:23552
	global_load_lds_dwordx4 v[218:219], off
	s_mov_b32 m0, s59
	s_cselect_b32 s59, 0, s29
	s_cselect_b32 s61, 0, s28
	s_cselect_b32 s62, s11, s15
	s_cselect_b32 s63, s10, s14
	s_add_u32 s34, s30, 0x160000
	v_lshl_add_u64 v[220:221], s[30:31], 0, v[140:141]
	s_addc_u32 s35, s31, 0
	s_add_i32 s60, s60, s33
	global_load_lds_dwordx4 v[220:221], off
	v_lshl_add_u64 v[222:223], s[34:35], 0, v[136:137]
	s_mov_b32 m0, s60
	s_nop 0
	global_load_lds_dwordx4 v[222:223], off
	s_add_i32 m0, s60, 0x2000
	v_lshl_add_u64 v[222:223], s[34:35], 0, v[140:141]
	s_add_u32 s34, s63, s61
	s_addc_u32 s35, s62, s59
	global_load_lds_dwordx4 v[222:223], off
	v_lshl_add_u64 v[222:223], s[34:35], 0, v[134:135]
	s_mov_b32 m0, s44
	v_lshl_add_u64 v[224:225], s[34:35], 0, v[138:139]
	global_load_lds_dwordx4 v[222:223], off
	s_mov_b32 m0, s45
	s_nop 0
	global_load_lds_dwordx4 v[224:225], off
	s_waitcnt vmcnt(8)
	s_waitcnt lgkmcnt(0)
	s_barrier
; #define PG8_STAGE_A(bufoff, base_, nx_, kb_, h_) do { if (GATHER) { if (nx_) PG8_STAGE_G(bufoff, kb_, goN, h_); else PG8_STAGE_G(bufoff, kb_, goC, h_); } \
;         else PG8_STAGE(bufoff, (base_) + (kb_) + (h_) * hstep, voffA); } while (0)
; #define PG8_STAGE(bufoff, gbase, voff) do { _Pragma("unroll") for (int _i = 0; _i < 2; ++_i) \
;         __builtin_amdgcn_global_load_lds((const unsigned*)((const char*)(gbase) + (voff)[_i]), (LAS unsigned*)(lds + (bufoff) + ldsw + _i * 8192), 16, 0, 0); } while (0)
; #define PG8_LDA(dst, b, h) do { _Pragma("unroll") for (int m = 0; m < 4; ++m) _Pragma("unroll") for (int k = 0; k < 2; ++k) dst[m][k] = *(const LAS bf16x8*)(lds + PG8_SA(b, h) + aoff + m * 2048 + k * 1024); } while (0)
; #define PG8_LDB(dst, b, h) do { _Pragma("unroll") for (int n = 0; n < 2; ++n) _Pragma("unroll") for (int k = 0; k < 2; ++k) dst[n][k] = *(const LAS bf16x8*)(lds + PG8_SB(b, h) + boff + n * 2048 + k * 1024); } while (0)
; #define PG8_WAIT_V(n) asm volatile("s_waitcnt vmcnt(" #n ")" ::: "memory")
; #define PG8_WAIT_L(n) asm volatile("s_waitcnt lgkmcnt(" #n ")" ::: "memory")
; template <class Epi, class Sched, bool GATHER = false>
; __device__ __forceinline__ void gemm_phase(LAS unsigned char* lds, const Gemm g, const Sched& S, const Epi& E, const int tid) {
;     ...
;             PG8_LDB(B0, 0, 0); PG8_LDB(B1, 0, 1); PG8_SCHED; PG8_LDA(At, 0, 0); PG8_STAGE_A(PG8_SA(1, 1), cA, false, kb1, 1);
;             PG8_WAIT_V(8); PG8_WAIT_L(0); PG8_BAR; PG8_MMA(0, 0, At, B0); PG8_MMA(0, 1, At, B1); PG8_BAR; PG8_SCHED;
;             PG8_LDA(At, 0, 1); PG8_STAGE(PG8_SB(0, 0), b2, voffB); PG8_STAGE(PG8_SB(0, 1), b2 + hstep, voffB); PG8_STAGE_A(PG8_SA(0, 0), (last ? nA : cA), last, kb2, 0);
;             PG8_WAIT_V(8); PG8_WAIT_L(0); PG8_BAR; PG8_MMA(1, 0, At, B0); PG8_MMA(1, 1, At, B1); PG8_BAR; PG8_SCHED;
;             PG8_LDB(B0, 1, 0); PG8_LDB(B1, 1, 1); PG8_SCHED; PG8_LDA(At, 1, 0); PG8_STAGE_A(PG8_SA(0, 1), (last ? nA : cA), last, kb2, 1);
;             PG8_WAIT_V(8); PG8_WAIT_L(0); PG8_BAR; PG8_MMA(0, 0, At, B0); PG8_MMA(0, 1, At, B1); PG8_BAR; PG8_SCHED;
;             PG8_LDA(At, 1, 1); PG8_STAGE(PG8_SB(1, 0), b3, voffB); PG8_STAGE(PG8_SB(1, 1), b3 + hstep, voffB); PG8_STAGE_A(PG8_SA(1, 0), (last ? nA : cA), last, kb3, 0);
;             PG8_WAIT_V(8); PG8_WAIT_L(0); PG8_BAR; PG8_MMA(1, 0, At, B0); PG8_MMA(1, 1, At, B1); PG8_BAR; PG8_SCHED;
	v_mfma_f32_16x16x32_bf16 v[58:61], v[152:155], v[184:187], 0
	v_mfma_f32_16x16x32_bf16 v[78:81], v[160:163], v[184:187], 0
	v_mfma_f32_16x16x32_bf16 v[66:69], v[152:155], v[192:195], 0
	v_mfma_f32_16x16x32_bf16 v[82:85], v[160:163], v[192:195], 0
	v_mfma_f32_16x16x32_bf16 v[74:77], v[152:155], v[202:205], 0
	v_mfma_f32_16x16x32_bf16 v[98:101], v[160:163], v[202:205], 0
	v_mfma_f32_16x16x32_bf16 v[90:93], v[152:155], v[210:213], 0
	v_mfma_f32_16x16x32_bf16 v[94:97], v[160:163], v[210:213], 0
	v_mfma_f32_16x16x32_bf16 v[58:61], v[156:159], v[188:191], v[58:61]
	v_mfma_f32_16x16x32_bf16 v[78:81], v[164:167], v[188:191], v[78:81]
	v_mfma_f32_16x16x32_bf16 v[66:69], v[156:159], v[196:199], v[66:69]
	v_mfma_f32_16x16x32_bf16 v[82:85], v[164:167], v[196:199], v[82:85]
	v_mfma_f32_16x16x32_bf16 v[74:77], v[156:159], v[206:209], v[74:77]
	v_mfma_f32_16x16x32_bf16 v[98:101], v[164:167], v[206:209], v[98:101]
	v_mfma_f32_16x16x32_bf16 v[90:93], v[156:159], v[214:217], v[90:93]
	v_mfma_f32_16x16x32_bf16 v[94:97], v[164:167], v[214:217], v[94:97]
	v_mfma_f32_16x16x32_bf16 v[114:117], v[168:171], v[184:187], 0
	v_mfma_f32_16x16x32_bf16 v[130:133], v[176:179], v[184:187], 0
	v_mfma_f32_16x16x32_bf16 v[110:113], v[168:171], v[192:195], 0
	v_mfma_f32_16x16x32_bf16 v[126:129], v[176:179], v[192:195], 0
	v_mfma_f32_16x16x32_bf16 v[106:109], v[168:171], v[202:205], 0
	v_mfma_f32_16x16x32_bf16 v[122:125], v[176:179], v[202:205], 0
	v_mfma_f32_16x16x32_bf16 v[102:105], v[168:171], v[210:213], 0
	v_mfma_f32_16x16x32_bf16 v[118:121], v[176:179], v[210:213], 0
	v_mfma_f32_16x16x32_bf16 v[114:117], v[172:175], v[188:191], v[114:117]
	v_mfma_f32_16x16x32_bf16 v[130:133], v[180:183], v[188:191], v[130:133]
	v_mfma_f32_16x16x32_bf16 v[110:113], v[172:175], v[196:199], v[110:113]
	v_mfma_f32_16x16x32_bf16 v[126:129], v[180:183], v[196:199], v[126:129]
	v_mfma_f32_16x16x32_bf16 v[106:109], v[172:175], v[206:209], v[106:109]
	v_mfma_f32_16x16x32_bf16 v[122:125], v[180:183], v[206:209], v[122:125]
	v_mfma_f32_16x16x32_bf16 v[102:105], v[172:175], v[214:217], v[102:105]
	v_mfma_f32_16x16x32_bf16 v[118:121], v[180:183], v[214:217], v[118:121]
	s_barrier
	s_add_i32 s59, 0, 0x18000
	v_add_u32_e32 v2, s59, v149
	s_add_i32 s60, 0, 0x1c000
	ds_read_b128 v[152:155], v2
	ds_read_b128 v[156:159], v2 offset:1024
	ds_read_b128 v[160:163], v2 offset:2048
	ds_read_b128 v[164:167], v2 offset:3072
	v_add_u32_e32 v2, s60, v149
	ds_read_b128 v[168:171], v2
	ds_read_b128 v[172:175], v2 offset:1024
	ds_read_b128 v[176:179], v2 offset:2048
	ds_read_b128 v[180:183], v2 offset:3072
	s_add_u32 s34, s34, 0x160000
	s_addc_u32 s35, s35, 0
	s_mov_b32 m0, s46
	v_lshl_add_u64 v[226:227], s[34:35], 0, v[134:135]
	ds_read_b128 v[184:187], v151 offset:32768
	ds_read_b128 v[188:191], v151 offset:33792
	ds_read_b128 v[192:195], v151 offset:34816
	ds_read_b128 v[196:199], v151 offset:35840
	ds_read_b128 v[202:205], v151 offset:36864
	ds_read_b128 v[206:209], v151 offset:37888
	ds_read_b128 v[210:213], v151 offset:38912
	ds_read_b128 v[214:217], v151 offset:39936
	global_load_lds_dwordx4 v[226:227], off
	v_lshl_add_u64 v[226:227], s[34:35], 0, v[138:139]
	s_mov_b32 m0, s47
	s_nop 0
	global_load_lds_dwordx4 v[226:227], off
	s_waitcnt vmcnt(8)
	s_waitcnt lgkmcnt(0)
	s_barrier
	v_mfma_f32_16x16x32_bf16 v[86:89], v[152:155], v[184:187], v[86:89]
	v_mfma_f32_16x16x32_bf16 v[18:21], v[160:163], v[184:187], v[18:21]
	v_mfma_f32_16x16x32_bf16 v[6:9], v[152:155], v[192:195], v[6:9]
	v_mfma_f32_16x16x32_bf16 v[22:25], v[160:163], v[192:195], v[22:25]
	v_mfma_f32_16x16x32_bf16 v[10:13], v[152:155], v[202:205], v[10:13]
	v_mfma_f32_16x16x32_bf16 v[26:29], v[160:163], v[202:205], v[26:29]
	v_mfma_f32_16x16x32_bf16 v[14:17], v[152:155], v[210:213], v[14:17]
	v_mfma_f32_16x16x32_bf16 v[30:33], v[160:163], v[210:213], v[30:33]
	v_mfma_f32_16x16x32_bf16 v[86:89], v[156:159], v[188:191], v[86:89]
	v_mfma_f32_16x16x32_bf16 v[18:21], v[164:167], v[188:191], v[18:21]
	v_mfma_f32_16x16x32_bf16 v[6:9], v[156:159], v[196:199], v[6:9]
	v_mfma_f32_16x16x32_bf16 v[22:25], v[164:167], v[196:199], v[22:25]
	v_mfma_f32_16x16x32_bf16 v[10:13], v[156:159], v[206:209], v[10:13]
	v_mfma_f32_16x16x32_bf16 v[26:29], v[164:167], v[206:209], v[26:29]
	v_mfma_f32_16x16x32_bf16 v[14:17], v[156:159], v[214:217], v[14:17]
	v_mfma_f32_16x16x32_bf16 v[30:33], v[164:167], v[214:217], v[30:33]
	v_mfma_f32_16x16x32_bf16 v[34:37], v[168:171], v[184:187], v[34:37]
	v_mfma_f32_16x16x32_bf16 v[50:53], v[176:179], v[184:187], v[50:53]
	v_mfma_f32_16x16x32_bf16 v[38:41], v[168:171], v[192:195], v[38:41]
	v_mfma_f32_16x16x32_bf16 v[54:57], v[176:179], v[192:195], v[54:57]
	v_mfma_f32_16x16x32_bf16 v[42:45], v[168:171], v[202:205], v[42:45]
	v_mfma_f32_16x16x32_bf16 v[62:65], v[176:179], v[202:205], v[62:65]
	v_mfma_f32_16x16x32_bf16 v[46:49], v[168:171], v[210:213], v[46:49]
	v_mfma_f32_16x16x32_bf16 v[70:73], v[176:179], v[210:213], v[70:73]
	v_mfma_f32_16x16x32_bf16 v[34:37], v[172:175], v[188:191], v[34:37]
	v_mfma_f32_16x16x32_bf16 v[50:53], v[180:183], v[188:191], v[50:53]
	v_mfma_f32_16x16x32_bf16 v[38:41], v[172:175], v[196:199], v[38:41]
	v_mfma_f32_16x16x32_bf16 v[54:57], v[180:183], v[196:199], v[54:57]
	v_mfma_f32_16x16x32_bf16 v[42:45], v[172:175], v[206:209], v[42:45]
	v_mfma_f32_16x16x32_bf16 v[62:65], v[180:183], v[206:209], v[62:65]
	v_mfma_f32_16x16x32_bf16 v[46:49], v[172:175], v[214:217], v[46:49]
	v_mfma_f32_16x16x32_bf16 v[70:73], v[180:183], v[214:217], v[70:73]
	s_barrier
; #define PG8_STAGE_A(bufoff, base_, nx_, kb_, h_) do { if (GATHER) { if (nx_) PG8_STAGE_G(bufoff, kb_, goN, h_); else PG8_STAGE_G(bufoff, kb_, goC, h_); } \
;         else PG8_STAGE(bufoff, (base_) + (kb_) + (h_) * hstep, voffA); } while (0)
; #define PG8_STAGE(bufoff, gbase, voff) do { _Pragma("unroll") for (int _i = 0; _i < 2; ++_i) \
;         __builtin_amdgcn_global_load_lds((const unsigned*)((const char*)(gbase) + (voff)[_i]), (LAS unsigned*)(lds + (bufoff) + ldsw + _i * 8192), 16, 0, 0); } while (0)
; #define PG8_LDA(dst, b, h) do { _Pragma("unroll") for (int m = 0; m < 4; ++m) _Pragma("unroll") for (int k = 0; k < 2; ++k) dst[m][k] = *(const LAS bf16x8*)(lds + PG8_SA(b, h) + aoff + m * 2048 + k * 1024); } while (0)
; #define PG8_MMA(ai, bj, At, Bt) do { __builtin_amdgcn_s_setprio(1); _Pragma("unroll") for (int m = 0; m < 4; ++m) _Pragma("unroll") for (int n = 0; n < 2; ++n) _Pragma("unroll") for (int k = 0; k < 2; ++k) \
;         acc[ai][bj][m][n] = __builtin_amdgcn_mfma_f32_16x16x32_bf16(Bt[n][k], At[m][k], acc[ai][bj][m][n], 0, 0, 0); __builtin_amdgcn_s_setprio(0); } while (0)
; #define PG8_WAIT_V(n) asm volatile("s_waitcnt vmcnt(" #n ")" ::: "memory")
; #define PG8_WAIT_L(n) asm volatile("s_waitcnt lgkmcnt(" #n ")" ::: "memory")
; #define PG8_BAR __builtin_amdgcn_s_barrier()
; #define PG8_SCHED __builtin_amdgcn_sched_barrier(0)
; template <class Epi, class Sched, bool GATHER = false>
; __device__ __forceinline__ void gemm_phase(LAS unsigned char* lds, const Gemm g, const Sched& S, const Epi& E, const int tid) {
;     ...
;         for (int t = 0; t < nt; t += 2) {
;             const bool last = (t == nt - 2);
;             const char* a1 = cA + (size_t)(t + 1) * kstep;
;             const char* a2 = last ? nA : cA + (size_t)(t + 2) * kstep; const char* b2 = last ? nB : cB + (size_t)(t + 2) * kstep;
;             const char* a3 = a2 + kstep; const char* b3 = b2 + kstep;
;     ...
;             PG8_LDA(At, 1, 1); PG8_STAGE(PG8_SB(1, 0), b3, voffB); PG8_STAGE(PG8_SB(1, 1), b3 + hstep, voffB); PG8_STAGE_A(PG8_SA(1, 0), (last ? nA : cA), last, kb3, 0);
;             PG8_WAIT_V(8); PG8_WAIT_L(0); PG8_BAR; PG8_MMA(1, 0, At, B0); PG8_MMA(1, 1, At, B1); PG8_BAR; PG8_SCHED;
	s_add_i32 s34, s59, s33
	v_lshl_add_u64 v[218:219], v[218:219], 0, s[0:1]
	s_mov_b32 m0, s34
	ds_read_b128 v[184:187], v151 offset:49152
	ds_read_b128 v[188:191], v151 offset:50176
	ds_read_b128 v[192:195], v151 offset:51200
	ds_read_b128 v[196:199], v151 offset:52224
	ds_read_b128 v[202:205], v151 offset:53248
	ds_read_b128 v[206:209], v151 offset:54272
	ds_read_b128 v[210:213], v151 offset:55296
	ds_read_b128 v[214:217], v151 offset:56320
	global_load_lds_dwordx4 v[218:219], off
	s_add_i32 m0, s34, 0x2000
	s_add_u32 s30, s30, 0x160080
	v_lshl_add_u64 v[218:219], v[220:221], 0, s[0:1]
	s_addc_u32 s31, s31, 0
	s_add_i32 s34, s60, s33
	global_load_lds_dwordx4 v[218:219], off
	v_lshl_add_u64 v[218:219], s[30:31], 0, v[136:137]
	s_mov_b32 m0, s34
	s_nop 0
	global_load_lds_dwordx4 v[218:219], off
	v_lshl_add_u64 v[218:219], s[30:31], 0, v[140:141]
	s_add_i32 m0, s34, 0x2000
	s_nop 0
	global_load_lds_dwordx4 v[218:219], off
	v_lshl_add_u64 v[218:219], v[222:223], 0, s[0:1]
	s_mov_b32 m0, s48
	s_nop 0
	global_load_lds_dwordx4 v[218:219], off
	v_lshl_add_u64 v[218:219], v[224:225], 0, s[0:1]
	s_mov_b32 m0, s49
	s_nop 0
	global_load_lds_dwordx4 v[218:219], off
	s_waitcnt vmcnt(8)
	s_waitcnt lgkmcnt(0)
	s_barrier
	v_mfma_f32_16x16x32_bf16 v[58:61], v[152:155], v[184:187], v[58:61]
	v_mfma_f32_16x16x32_bf16 v[78:81], v[160:163], v[184:187], v[78:81]
	v_mfma_f32_16x16x32_bf16 v[66:69], v[152:155], v[192:195], v[66:69]
	v_mfma_f32_16x16x32_bf16 v[82:85], v[160:163], v[192:195], v[82:85]
	v_mfma_f32_16x16x32_bf16 v[74:77], v[152:155], v[202:205], v[74:77]
	v_mfma_f32_16x16x32_bf16 v[98:101], v[160:163], v[202:205], v[98:101]
	v_mfma_f32_16x16x32_bf16 v[90:93], v[152:155], v[210:213], v[90:93]
	v_mfma_f32_16x16x32_bf16 v[94:97], v[160:163], v[210:213], v[94:97]
	v_mfma_f32_16x16x32_bf16 v[58:61], v[156:159], v[188:191], v[58:61]
	v_mfma_f32_16x16x32_bf16 v[78:81], v[164:167], v[188:191], v[78:81]
	v_mfma_f32_16x16x32_bf16 v[66:69], v[156:159], v[196:199], v[66:69]
	v_mfma_f32_16x16x32_bf16 v[82:85], v[164:167], v[196:199], v[82:85]
	v_mfma_f32_16x16x32_bf16 v[74:77], v[156:159], v[206:209], v[74:77]
	v_mfma_f32_16x16x32_bf16 v[98:101], v[164:167], v[206:209], v[98:101]
	v_mfma_f32_16x16x32_bf16 v[90:93], v[156:159], v[214:217], v[90:93]
	v_mfma_f32_16x16x32_bf16 v[94:97], v[164:167], v[214:217], v[94:97]
	v_mfma_f32_16x16x32_bf16 v[114:117], v[168:171], v[184:187], v[114:117]
	v_mfma_f32_16x16x32_bf16 v[130:133], v[176:179], v[184:187], v[130:133]
	v_mfma_f32_16x16x32_bf16 v[110:113], v[168:171], v[192:195], v[110:113]
	v_mfma_f32_16x16x32_bf16 v[126:129], v[176:179], v[192:195], v[126:129]
	v_mfma_f32_16x16x32_bf16 v[106:109], v[168:171], v[202:205], v[106:109]
	v_mfma_f32_16x16x32_bf16 v[122:125], v[176:179], v[202:205], v[122:125]
	v_mfma_f32_16x16x32_bf16 v[102:105], v[168:171], v[210:213], v[102:105]
	v_mfma_f32_16x16x32_bf16 v[118:121], v[176:179], v[210:213], v[118:121]
	v_mfma_f32_16x16x32_bf16 v[114:117], v[172:175], v[188:191], v[114:117]
	v_mfma_f32_16x16x32_bf16 v[130:133], v[180:183], v[188:191], v[130:133]
	v_mfma_f32_16x16x32_bf16 v[110:113], v[172:175], v[196:199], v[110:113]
	v_mfma_f32_16x16x32_bf16 v[126:129], v[180:183], v[196:199], v[126:129]
	v_mfma_f32_16x16x32_bf16 v[106:109], v[172:175], v[206:209], v[106:109]
	v_mfma_f32_16x16x32_bf16 v[122:125], v[180:183], v[206:209], v[122:125]
	v_mfma_f32_16x16x32_bf16 v[102:105], v[172:175], v[214:217], v[102:105]
	v_mfma_f32_16x16x32_bf16 v[118:121], v[180:183], v[214:217], v[118:121]
	s_barrier
	s_add_i32 s58, s58, 2
	s_cmpk_gt_u32 s58, 0x55
	s_mov_b64 s[34:35], s[28:29]
	s_cbranch_scc1 .Lpeel3_exit
.LBB0_1483:
	s_add_u32 s28, s34, 0x100
	s_addc_u32 s29, s35, 0
	s_add_u32 s30, s56, s34
	s_addc_u32 s31, s57, s35
	s_add_i32 s59, 0, 0x10000
	s_add_i32 s60, 0, 0x14000
	v_add_u32_e32 v2, s59, v149
	ds_read_b128 v[152:155], v2
	ds_read_b128 v[156:159], v2 offset:1024
	ds_read_b128 v[160:163], v2 offset:2048
	ds_read_b128 v[164:167], v2 offset:3072
	v_add_u32_e32 v2, s60, v149
	ds_read_b128 v[168:171], v2
	ds_read_b128 v[172:175], v2 offset:1024
	ds_read_b128 v[176:179], v2 offset:2048
	ds_read_b128 v[180:183], v2 offset:3072
	s_add_i32 s62, s59, s33
	s_add_i32 m0, s44, 0xc000
	s_add_i32 s61, s44, 0xe000
	s_add_i32 s59, s62, 0x2000
	s_cmpk_eq_i32 s58, 0x54
	s_cselect_b32 s31, s25, s31
	s_cselect_b32 s30, s24, s30
	v_lshl_add_u64 v[218:219], v[4:5], 0, s[34:35]
	ds_read_b128 v[184:187], v151
	ds_read_b128 v[188:191], v151 offset:1024
	ds_read_b128 v[192:195], v151 offset:2048
	ds_read_b128 v[196:199], v151 offset:3072
	ds_read_b128 v[202:205], v151 offset:4096
	ds_read_b128 v[206:209], v151 offset:5120
	ds_read_b128 v[210:213], v151 offset:6144
	ds_read_b128 v[214:217], v151 offset:7168
	global_load_lds_dwordx4 v[218:219], off
	v_lshl_add_u64 v[218:219], v[146:147], 0, s[34:35]
	s_mov_b32 m0, s61
	s_nop 0
	global_load_lds_dwordx4 v[218:219], off
	s_waitcnt vmcnt(8)
	s_waitcnt lgkmcnt(0)
	s_barrier
; #define PG8_STAGE_A(bufoff, base_, nx_, kb_, h_) do { if (GATHER) { if (nx_) PG8_STAGE_G(bufoff, kb_, goN, h_); else PG8_STAGE_G(bufoff, kb_, goC, h_); } \
;         else PG8_STAGE(bufoff, (base_) + (kb_) + (h_) * hstep, voffA); } while (0)
; #define PG8_STAGE(bufoff, gbase, voff) do { _Pragma("unroll") for (int _i = 0; _i < 2; ++_i) \
;         __builtin_amdgcn_global_load_lds((const unsigned*)((const char*)(gbase) + (voff)[_i]), (LAS unsigned*)(lds + (bufoff) + ldsw + _i * 8192), 16, 0, 0); } while (0)
; #define PG8_LDA(dst, b, h) do { _Pragma("unroll") for (int m = 0; m < 4; ++m) _Pragma("unroll") for (int k = 0; k < 2; ++k) dst[m][k] = *(const LAS bf16x8*)(lds + PG8_SA(b, h) + aoff + m * 2048 + k * 1024); } while (0)
; #define PG8_LDB(dst, b, h) do { _Pragma("unroll") for (int n = 0; n < 2; ++n) _Pragma("unroll") for (int k = 0; k < 2; ++k) dst[n][k] = *(const LAS bf16x8*)(lds + PG8_SB(b, h) + boff + n * 2048 + k * 1024); } while (0)
; #define PG8_WAIT_V(n) asm volatile("s_waitcnt vmcnt(" #n ")" ::: "memory")
; #define PG8_WAIT_L(n) asm volatile("s_waitcnt lgkmcnt(" #n ")" ::: "memory")
; template <class Epi, class Sched, bool GATHER = false>
; __device__ __forceinline__ void gemm_phase(LAS unsigned char* lds, const Gemm g, const Sched& S, const Epi& E, const int tid) {
;     ...
;             PG8_LDB(B0, 0, 0); PG8_LDB(B1, 0, 1); PG8_SCHED; PG8_LDA(At, 0, 0); PG8_STAGE_A(PG8_SA(1, 1), cA, false, kb1, 1);
;             PG8_WAIT_V(8); PG8_WAIT_L(0); PG8_BAR; PG8_MMA(0, 0, At, B0); PG8_MMA(0, 1, At, B1); PG8_BAR; PG8_SCHED;
;             PG8_LDA(At, 0, 1); PG8_STAGE(PG8_SB(0, 0), b2, voffB); PG8_STAGE(PG8_SB(0, 1), b2 + hstep, voffB); PG8_STAGE_A(PG8_SA(0, 0), (last ? nA : cA), last, kb2, 0);
;             PG8_WAIT_V(8); PG8_WAIT_L(0); PG8_BAR; PG8_MMA(1, 0, At, B0); PG8_MMA(1, 1, At, B1); PG8_BAR; PG8_SCHED;
;             PG8_LDB(B0, 1, 0); PG8_LDB(B1, 1, 1); PG8_SCHED; PG8_LDA(At, 1, 0); PG8_STAGE_A(PG8_SA(0, 1), (last ? nA : cA), last, kb2, 1);
;             PG8_WAIT_V(8); PG8_WAIT_L(0); PG8_BAR; PG8_MMA(0, 0, At, B0); PG8_MMA(0, 1, At, B1); PG8_BAR; PG8_SCHED;
;             PG8_LDA(At, 1, 1); PG8_STAGE(PG8_SB(1, 0), b3, voffB); PG8_STAGE(PG8_SB(1, 1), b3 + hstep, voffB); PG8_STAGE_A(PG8_SA(1, 0), (last ? nA : cA), last, kb3, 0);
;             PG8_WAIT_V(8); PG8_WAIT_L(0); PG8_BAR; PG8_MMA(1, 0, At, B0); PG8_MMA(1, 1, At, B1); PG8_BAR; PG8_SCHED;
	v_mfma_f32_16x16x32_bf16 v[86:89], v[152:155], v[184:187], v[86:89]
	v_mfma_f32_16x16x32_bf16 v[18:21], v[160:163], v[184:187], v[18:21]
	v_mfma_f32_16x16x32_bf16 v[6:9], v[152:155], v[192:195], v[6:9]
	v_mfma_f32_16x16x32_bf16 v[22:25], v[160:163], v[192:195], v[22:25]
	v_mfma_f32_16x16x32_bf16 v[10:13], v[152:155], v[202:205], v[10:13]
	v_mfma_f32_16x16x32_bf16 v[26:29], v[160:163], v[202:205], v[26:29]
	v_mfma_f32_16x16x32_bf16 v[14:17], v[152:155], v[210:213], v[14:17]
	v_mfma_f32_16x16x32_bf16 v[30:33], v[160:163], v[210:213], v[30:33]
	v_mfma_f32_16x16x32_bf16 v[86:89], v[156:159], v[188:191], v[86:89]
	v_mfma_f32_16x16x32_bf16 v[18:21], v[164:167], v[188:191], v[18:21]
	v_mfma_f32_16x16x32_bf16 v[6:9], v[156:159], v[196:199], v[6:9]
	v_mfma_f32_16x16x32_bf16 v[22:25], v[164:167], v[196:199], v[22:25]
	v_mfma_f32_16x16x32_bf16 v[10:13], v[156:159], v[206:209], v[10:13]
	v_mfma_f32_16x16x32_bf16 v[26:29], v[164:167], v[206:209], v[26:29]
	v_mfma_f32_16x16x32_bf16 v[14:17], v[156:159], v[214:217], v[14:17]
	v_mfma_f32_16x16x32_bf16 v[30:33], v[164:167], v[214:217], v[30:33]
	v_mfma_f32_16x16x32_bf16 v[34:37], v[168:171], v[184:187], v[34:37]
	v_mfma_f32_16x16x32_bf16 v[50:53], v[176:179], v[184:187], v[50:53]
	v_mfma_f32_16x16x32_bf16 v[38:41], v[168:171], v[192:195], v[38:41]
	v_mfma_f32_16x16x32_bf16 v[54:57], v[176:179], v[192:195], v[54:57]
	v_mfma_f32_16x16x32_bf16 v[42:45], v[168:171], v[202:205], v[42:45]
	v_mfma_f32_16x16x32_bf16 v[62:65], v[176:179], v[202:205], v[62:65]
	v_mfma_f32_16x16x32_bf16 v[46:49], v[168:171], v[210:213], v[46:49]
	v_mfma_f32_16x16x32_bf16 v[70:73], v[176:179], v[210:213], v[70:73]
	v_mfma_f32_16x16x32_bf16 v[34:37], v[172:175], v[188:191], v[34:37]
	v_mfma_f32_16x16x32_bf16 v[50:53], v[180:183], v[188:191], v[50:53]
	v_mfma_f32_16x16x32_bf16 v[38:41], v[172:175], v[196:199], v[38:41]
	v_mfma_f32_16x16x32_bf16 v[54:57], v[180:183], v[196:199], v[54:57]
	v_mfma_f32_16x16x32_bf16 v[42:45], v[172:175], v[206:209], v[42:45]
	v_mfma_f32_16x16x32_bf16 v[62:65], v[180:183], v[206:209], v[62:65]
	v_mfma_f32_16x16x32_bf16 v[46:49], v[172:175], v[214:217], v[46:49]
	v_mfma_f32_16x16x32_bf16 v[70:73], v[180:183], v[214:217], v[70:73]
	s_barrier
	s_mov_b32 m0, s62
	v_lshl_add_u64 v[218:219], s[30:31], 0, v[136:137]
	ds_read_b128 v[184:187], v151 offset:16384
	ds_read_b128 v[188:191], v151 offset:17408
	ds_read_b128 v[192:195], v151 offset:18432
	ds_read_b128 v[196:199], v151 offset:19456
	ds_read_b128 v[202:205], v151 offset:20480
	ds_read_b128 v[206:209], v151 offset:21504
	ds_read_b128 v[210:213], v151 offset:22528
	ds_read_b128 v[214:217], v151 offset:23552
	global_load_lds_dwordx4 v[218:219], off
	s_mov_b32 m0, s59
	s_cselect_b32 s59, 0, s29
	s_cselect_b32 s61, 0, s28
	s_cselect_b32 s62, s11, s15
	s_cselect_b32 s63, s10, s14
	s_add_u32 s34, s30, 0x160000
	v_lshl_add_u64 v[220:221], s[30:31], 0, v[140:141]
	s_addc_u32 s35, s31, 0
	s_add_i32 s60, s60, s33
	global_load_lds_dwordx4 v[220:221], off
	v_lshl_add_u64 v[222:223], s[34:35], 0, v[136:137]
	s_mov_b32 m0, s60
	s_nop 0
	global_load_lds_dwordx4 v[222:223], off
	s_add_i32 m0, s60, 0x2000
	v_lshl_add_u64 v[222:223], s[34:35], 0, v[140:141]
	s_add_u32 s34, s63, s61
	s_addc_u32 s35, s62, s59
	global_load_lds_dwordx4 v[222:223], off
	v_lshl_add_u64 v[222:223], s[34:35], 0, v[134:135]
	s_mov_b32 m0, s44
	v_lshl_add_u64 v[224:225], s[34:35], 0, v[138:139]
	global_load_lds_dwordx4 v[222:223], off
	s_mov_b32 m0, s45
	s_nop 0
	global_load_lds_dwordx4 v[224:225], off
	s_waitcnt vmcnt(8)
	s_waitcnt lgkmcnt(0)
	s_barrier
	v_mfma_f32_16x16x32_bf16 v[58:61], v[152:155], v[184:187], v[58:61]
	v_mfma_f32_16x16x32_bf16 v[78:81], v[160:163], v[184:187], v[78:81]
	v_mfma_f32_16x16x32_bf16 v[66:69], v[152:155], v[192:195], v[66:69]
	v_mfma_f32_16x16x32_bf16 v[82:85], v[160:163], v[192:195], v[82:85]
	v_mfma_f32_16x16x32_bf16 v[74:77], v[152:155], v[202:205], v[74:77]
	v_mfma_f32_16x16x32_bf16 v[98:101], v[160:163], v[202:205], v[98:101]
	v_mfma_f32_16x16x32_bf16 v[90:93], v[152:155], v[210:213], v[90:93]
	v_mfma_f32_16x16x32_bf16 v[94:97], v[160:163], v[210:213], v[94:97]
	v_mfma_f32_16x16x32_bf16 v[58:61], v[156:159], v[188:191], v[58:61]
	v_mfma_f32_16x16x32_bf16 v[78:81], v[164:167], v[188:191], v[78:81]
	v_mfma_f32_16x16x32_bf16 v[66:69], v[156:159], v[196:199], v[66:69]
	v_mfma_f32_16x16x32_bf16 v[82:85], v[164:167], v[196:199], v[82:85]
	v_mfma_f32_16x16x32_bf16 v[74:77], v[156:159], v[206:209], v[74:77]
	v_mfma_f32_16x16x32_bf16 v[98:101], v[164:167], v[206:209], v[98:101]
	v_mfma_f32_16x16x32_bf16 v[90:93], v[156:159], v[214:217], v[90:93]
	v_mfma_f32_16x16x32_bf16 v[94:97], v[164:167], v[214:217], v[94:97]
	v_mfma_f32_16x16x32_bf16 v[114:117], v[168:171], v[184:187], v[114:117]
	v_mfma_f32_16x16x32_bf16 v[130:133], v[176:179], v[184:187], v[130:133]
	v_mfma_f32_16x16x32_bf16 v[110:113], v[168:171], v[192:195], v[110:113]
	v_mfma_f32_16x16x32_bf16 v[126:129], v[176:179], v[192:195], v[126:129]
	v_mfma_f32_16x16x32_bf16 v[106:109], v[168:171], v[202:205], v[106:109]
	v_mfma_f32_16x16x32_bf16 v[122:125], v[176:179], v[202:205], v[122:125]
	v_mfma_f32_16x16x32_bf16 v[102:105], v[168:171], v[210:213], v[102:105]
	v_mfma_f32_16x16x32_bf16 v[118:121], v[176:179], v[210:213], v[118:121]
	v_mfma_f32_16x16x32_bf16 v[114:117], v[172:175], v[188:191], v[114:117]
	v_mfma_f32_16x16x32_bf16 v[130:133], v[180:183], v[188:191], v[130:133]
	v_mfma_f32_16x16x32_bf16 v[110:113], v[172:175], v[196:199], v[110:113]
	v_mfma_f32_16x16x32_bf16 v[126:129], v[180:183], v[196:199], v[126:129]
	v_mfma_f32_16x16x32_bf16 v[106:109], v[172:175], v[206:209], v[106:109]
	v_mfma_f32_16x16x32_bf16 v[122:125], v[180:183], v[206:209], v[122:125]
	v_mfma_f32_16x16x32_bf16 v[102:105], v[172:175], v[214:217], v[102:105]
	v_mfma_f32_16x16x32_bf16 v[118:121], v[180:183], v[214:217], v[118:121]
	s_barrier
; #define PG8_STAGE_A(bufoff, base_, nx_, kb_, h_) do { if (GATHER) { if (nx_) PG8_STAGE_G(bufoff, kb_, goN, h_); else PG8_STAGE_G(bufoff, kb_, goC, h_); } \
;         else PG8_STAGE(bufoff, (base_) + (kb_) + (h_) * hstep, voffA); } while (0)
; #define PG8_STAGE(bufoff, gbase, voff) do { _Pragma("unroll") for (int _i = 0; _i < 2; ++_i) \
;         __builtin_amdgcn_global_load_lds((const unsigned*)((const char*)(gbase) + (voff)[_i]), (LAS unsigned*)(lds + (bufoff) + ldsw + _i * 8192), 16, 0, 0); } while (0)
; #define PG8_LDA(dst, b, h) do { _Pragma("unroll") for (int m = 0; m < 4; ++m) _Pragma("unroll") for (int k = 0; k < 2; ++k) dst[m][k] = *(const LAS bf16x8*)(lds + PG8_SA(b, h) + aoff + m * 2048 + k * 1024); } while (0)
; #define PG8_LDB(dst, b, h) do { _Pragma("unroll") for (int n = 0; n < 2; ++n) _Pragma("unroll") for (int k = 0; k < 2; ++k) dst[n][k] = *(const LAS bf16x8*)(lds + PG8_SB(b, h) + boff + n * 2048 + k * 1024); } while (0)
; #define PG8_MMA(ai, bj, At, Bt) do { __builtin_amdgcn_s_setprio(1); _Pragma("unroll") for (int m = 0; m < 4; ++m) _Pragma("unroll") for (int n = 0; n < 2; ++n) _Pragma("unroll") for (int k = 0; k < 2; ++k) \
;         acc[ai][bj][m][n] = __builtin_amdgcn_mfma_f32_16x16x32_bf16(Bt[n][k], At[m][k], acc[ai][bj][m][n], 0, 0, 0); __builtin_amdgcn_s_setprio(0); } while (0)
; #define PG8_WAIT_V(n) asm volatile("s_waitcnt vmcnt(" #n ")" ::: "memory")
; #define PG8_WAIT_L(n) asm volatile("s_waitcnt lgkmcnt(" #n ")" ::: "memory")
; #define PG8_BAR __builtin_amdgcn_s_barrier()
; #define PG8_SCHED __builtin_amdgcn_sched_barrier(0)
; template <class Epi, class Sched, bool GATHER = false>
; __device__ __forceinline__ void gemm_phase(LAS unsigned char* lds, const Gemm g, const Sched& S, const Epi& E, const int tid) {
;     ...
;             PG8_LDB(B0, 1, 0); PG8_LDB(B1, 1, 1); PG8_SCHED; PG8_LDA(At, 1, 0); PG8_STAGE_A(PG8_SA(0, 1), (last ? nA : cA), last, kb2, 1);
;             PG8_WAIT_V(8); PG8_WAIT_L(0); PG8_BAR; PG8_MMA(0, 0, At, B0); PG8_MMA(0, 1, At, B1); PG8_BAR; PG8_SCHED;
;             PG8_LDA(At, 1, 1); PG8_STAGE(PG8_SB(1, 0), b3, voffB); PG8_STAGE(PG8_SB(1, 1), b3 + hstep, voffB); PG8_STAGE_A(PG8_SA(1, 0), (last ? nA : cA), last, kb3, 0);
;             PG8_WAIT_V(8); PG8_WAIT_L(0); PG8_BAR; PG8_MMA(1, 0, At, B0); PG8_MMA(1, 1, At, B1); PG8_BAR; PG8_SCHED;
	s_add_i32 s59, 0, 0x18000
	v_add_u32_e32 v2, s59, v149
	s_add_i32 s60, 0, 0x1c000
	ds_read_b128 v[152:155], v2
	ds_read_b128 v[156:159], v2 offset:1024
	ds_read_b128 v[160:163], v2 offset:2048
	ds_read_b128 v[164:167], v2 offset:3072
	v_add_u32_e32 v2, s60, v149
	ds_read_b128 v[168:171], v2
	ds_read_b128 v[172:175], v2 offset:1024
	ds_read_b128 v[176:179], v2 offset:2048
	ds_read_b128 v[180:183], v2 offset:3072
	s_add_u32 s34, s34, 0x160000
	s_addc_u32 s35, s35, 0
	s_mov_b32 m0, s46
	v_lshl_add_u64 v[226:227], s[34:35], 0, v[134:135]
	ds_read_b128 v[184:187], v151 offset:32768
	ds_read_b128 v[188:191], v151 offset:33792
	ds_read_b128 v[192:195], v151 offset:34816
	ds_read_b128 v[196:199], v151 offset:35840
	ds_read_b128 v[202:205], v151 offset:36864
	ds_read_b128 v[206:209], v151 offset:37888
	ds_read_b128 v[210:213], v151 offset:38912
	ds_read_b128 v[214:217], v151 offset:39936
	global_load_lds_dwordx4 v[226:227], off
	v_lshl_add_u64 v[226:227], s[34:35], 0, v[138:139]
	s_mov_b32 m0, s47
	s_nop 0
	global_load_lds_dwordx4 v[226:227], off
	s_waitcnt vmcnt(8)
	s_waitcnt lgkmcnt(0)
	s_barrier
	v_mfma_f32_16x16x32_bf16 v[86:89], v[152:155], v[184:187], v[86:89]
	v_mfma_f32_16x16x32_bf16 v[18:21], v[160:163], v[184:187], v[18:21]
	v_mfma_f32_16x16x32_bf16 v[6:9], v[152:155], v[192:195], v[6:9]
	v_mfma_f32_16x16x32_bf16 v[22:25], v[160:163], v[192:195], v[22:25]
	v_mfma_f32_16x16x32_bf16 v[10:13], v[152:155], v[202:205], v[10:13]
	v_mfma_f32_16x16x32_bf16 v[26:29], v[160:163], v[202:205], v[26:29]
	v_mfma_f32_16x16x32_bf16 v[14:17], v[152:155], v[210:213], v[14:17]
	v_mfma_f32_16x16x32_bf16 v[30:33], v[160:163], v[210:213], v[30:33]
	v_mfma_f32_16x16x32_bf16 v[86:89], v[156:159], v[188:191], v[86:89]
	v_mfma_f32_16x16x32_bf16 v[18:21], v[164:167], v[188:191], v[18:21]
	v_mfma_f32_16x16x32_bf16 v[6:9], v[156:159], v[196:199], v[6:9]
	v_mfma_f32_16x16x32_bf16 v[22:25], v[164:167], v[196:199], v[22:25]
	v_mfma_f32_16x16x32_bf16 v[10:13], v[156:159], v[206:209], v[10:13]
	v_mfma_f32_16x16x32_bf16 v[26:29], v[164:167], v[206:209], v[26:29]
	v_mfma_f32_16x16x32_bf16 v[14:17], v[156:159], v[214:217], v[14:17]
	v_mfma_f32_16x16x32_bf16 v[30:33], v[164:167], v[214:217], v[30:33]
	v_mfma_f32_16x16x32_bf16 v[34:37], v[168:171], v[184:187], v[34:37]
	v_mfma_f32_16x16x32_bf16 v[50:53], v[176:179], v[184:187], v[50:53]
	v_mfma_f32_16x16x32_bf16 v[38:41], v[168:171], v[192:195], v[38:41]
	v_mfma_f32_16x16x32_bf16 v[54:57], v[176:179], v[192:195], v[54:57]
	v_mfma_f32_16x16x32_bf16 v[42:45], v[168:171], v[202:205], v[42:45]
	v_mfma_f32_16x16x32_bf16 v[62:65], v[176:179], v[202:205], v[62:65]
	v_mfma_f32_16x16x32_bf16 v[46:49], v[168:171], v[210:213], v[46:49]
	v_mfma_f32_16x16x32_bf16 v[70:73], v[176:179], v[210:213], v[70:73]
	v_mfma_f32_16x16x32_bf16 v[34:37], v[172:175], v[188:191], v[34:37]
	v_mfma_f32_16x16x32_bf16 v[50:53], v[180:183], v[188:191], v[50:53]
	v_mfma_f32_16x16x32_bf16 v[38:41], v[172:175], v[196:199], v[38:41]
	v_mfma_f32_16x16x32_bf16 v[54:57], v[180:183], v[196:199], v[54:57]
	v_mfma_f32_16x16x32_bf16 v[42:45], v[172:175], v[206:209], v[42:45]
	v_mfma_f32_16x16x32_bf16 v[62:65], v[180:183], v[206:209], v[62:65]
	v_mfma_f32_16x16x32_bf16 v[46:49], v[172:175], v[214:217], v[46:49]
	v_mfma_f32_16x16x32_bf16 v[70:73], v[180:183], v[214:217], v[70:73]
	s_barrier
	s_add_i32 s34, s59, s33
	v_lshl_add_u64 v[218:219], v[218:219], 0, s[0:1]
	s_mov_b32 m0, s34
	ds_read_b128 v[184:187], v151 offset:49152
	ds_read_b128 v[188:191], v151 offset:50176
	ds_read_b128 v[192:195], v151 offset:51200
	ds_read_b128 v[196:199], v151 offset:52224
	ds_read_b128 v[202:205], v151 offset:53248
	ds_read_b128 v[206:209], v151 offset:54272
	ds_read_b128 v[210:213], v151 offset:55296
	ds_read_b128 v[214:217], v151 offset:56320
	global_load_lds_dwordx4 v[218:219], off
	s_add_i32 m0, s34, 0x2000
	s_add_u32 s30, s30, 0x160080
	v_lshl_add_u64 v[218:219], v[220:221], 0, s[0:1]
	s_addc_u32 s31, s31, 0
	s_add_i32 s34, s60, s33
	global_load_lds_dwordx4 v[218:219], off
	v_lshl_add_u64 v[218:219], s[30:31], 0, v[136:137]
	s_mov_b32 m0, s34
	s_nop 0
	global_load_lds_dwordx4 v[218:219], off
	v_lshl_add_u64 v[218:219], s[30:31], 0, v[140:141]
	s_add_i32 m0, s34, 0x2000
	s_nop 0
	global_load_lds_dwordx4 v[218:219], off
	v_lshl_add_u64 v[218:219], v[222:223], 0, s[0:1]
	s_mov_b32 m0, s48
	s_nop 0
	global_load_lds_dwordx4 v[218:219], off
	v_lshl_add_u64 v[218:219], v[224:225], 0, s[0:1]
	s_mov_b32 m0, s49
	s_nop 0
	global_load_lds_dwordx4 v[218:219], off
	s_waitcnt vmcnt(8)
	s_waitcnt lgkmcnt(0)
	s_barrier
	v_mfma_f32_16x16x32_bf16 v[58:61], v[152:155], v[184:187], v[58:61]
	v_mfma_f32_16x16x32_bf16 v[78:81], v[160:163], v[184:187], v[78:81]
	v_mfma_f32_16x16x32_bf16 v[66:69], v[152:155], v[192:195], v[66:69]
	v_mfma_f32_16x16x32_bf16 v[82:85], v[160:163], v[192:195], v[82:85]
	v_mfma_f32_16x16x32_bf16 v[74:77], v[152:155], v[202:205], v[74:77]
	v_mfma_f32_16x16x32_bf16 v[98:101], v[160:163], v[202:205], v[98:101]
	v_mfma_f32_16x16x32_bf16 v[90:93], v[152:155], v[210:213], v[90:93]
	v_mfma_f32_16x16x32_bf16 v[94:97], v[160:163], v[210:213], v[94:97]
	v_mfma_f32_16x16x32_bf16 v[58:61], v[156:159], v[188:191], v[58:61]
	v_mfma_f32_16x16x32_bf16 v[78:81], v[164:167], v[188:191], v[78:81]
	v_mfma_f32_16x16x32_bf16 v[66:69], v[156:159], v[196:199], v[66:69]
	v_mfma_f32_16x16x32_bf16 v[82:85], v[164:167], v[196:199], v[82:85]
	v_mfma_f32_16x16x32_bf16 v[74:77], v[156:159], v[206:209], v[74:77]
	v_mfma_f32_16x16x32_bf16 v[98:101], v[164:167], v[206:209], v[98:101]
	v_mfma_f32_16x16x32_bf16 v[90:93], v[156:159], v[214:217], v[90:93]
	v_mfma_f32_16x16x32_bf16 v[94:97], v[164:167], v[214:217], v[94:97]
	v_mfma_f32_16x16x32_bf16 v[114:117], v[168:171], v[184:187], v[114:117]
	v_mfma_f32_16x16x32_bf16 v[130:133], v[176:179], v[184:187], v[130:133]
	v_mfma_f32_16x16x32_bf16 v[110:113], v[168:171], v[192:195], v[110:113]
	v_mfma_f32_16x16x32_bf16 v[126:129], v[176:179], v[192:195], v[126:129]
	v_mfma_f32_16x16x32_bf16 v[106:109], v[168:171], v[202:205], v[106:109]
	v_mfma_f32_16x16x32_bf16 v[122:125], v[176:179], v[202:205], v[122:125]
	v_mfma_f32_16x16x32_bf16 v[102:105], v[168:171], v[210:213], v[102:105]
	v_mfma_f32_16x16x32_bf16 v[118:121], v[176:179], v[210:213], v[118:121]
	v_mfma_f32_16x16x32_bf16 v[114:117], v[172:175], v[188:191], v[114:117]
	v_mfma_f32_16x16x32_bf16 v[130:133], v[180:183], v[188:191], v[130:133]
	v_mfma_f32_16x16x32_bf16 v[110:113], v[172:175], v[196:199], v[110:113]
	v_mfma_f32_16x16x32_bf16 v[126:129], v[180:183], v[196:199], v[126:129]
	v_mfma_f32_16x16x32_bf16 v[106:109], v[172:175], v[206:209], v[106:109]
	v_mfma_f32_16x16x32_bf16 v[122:125], v[180:183], v[206:209], v[122:125]
	v_mfma_f32_16x16x32_bf16 v[102:105], v[172:175], v[214:217], v[102:105]
	v_mfma_f32_16x16x32_bf16 v[118:121], v[180:183], v[214:217], v[118:121]
	s_barrier
	s_add_i32 s58, s58, 2
	s_cmpk_gt_u32 s58, 0x55
	s_mov_b64 s[34:35], s[28:29]
	s_cbranch_scc0 .LBB0_1483

; template <class Epi, class Sched, bool GATHER = false>
; __device__ __forceinline__ void gemm_phase(LAS unsigned char* lds, const Gemm g, const Sched& S, const Epi& E, const int tid) {
;     ...
;         const bool has_next = S.next(ui + 1, nxt);
;         const char* nA = has_next ? (const char*)g.A + (size_t)nxt.pm * tstep : cA; const char* nB = has_next ? (const char*)g.Bt + (size_t)nxt.pb * tstep : cB;
;         if (GATHER && has_next && wid < 4) __builtin_amdgcn_global_load_lds((const unsigned*)(g.rowmap + nxt.rb + tid), (LAS unsigned*)(lds + STAGE_BYTES + ((ui + 1) & 1) * 1024 + wid * 256), 4, 0, 0);
;         for (int t = 0; t < nt; t += 2) {
;             const bool last = (t == nt - 2);
;             const char* a1 = cA + (size_t)(t + 1) * kstep;
;             const char* a2 = last ? nA : cA + (size_t)(t + 2) * kstep; const char* b2 = last ? nB : cB + (size_t)(t + 2) * kstep;
;             const char* a3 = a2 + kstep; const char* b3 = b2 + kstep;
;     ...
;             PG8_LDB(B0, 0, 0); PG8_SCHED; PG8_LDA(At, 0, 0); PG8_STAGE(PG8_SA(1, 1), a1 + hstep, voffA);
;             PG8_WAIT_L(8); PG8_BAR; PG8_WAIT_L(0); PG8_MMA(0, 0, At, B0); PG8_BAR; PG8_SCHED;
;             PG8_LDB(B1, 0, 1); PG8_STAGE(PG8_SB(0, 0), b2, voffB);
;             PG8_BAR; PG8_WAIT_L(0); PG8_MMA(0, 1, At, B1); PG8_BAR;
;             PG8_LDA(At, 0, 1); PG8_STAGE(PG8_SA(0, 0), a2, voffA);
;             PG8_BAR; PG8_WAIT_L(0); PG8_MMA(1, 0, At, B0); PG8_BAR; PG8_SCHED;
;             PG8_STAGE(PG8_SB(0, 1), b2 + hstep, voffB);
;             PG8_WAIT_V(6); PG8_BAR; PG8_MMA(1, 1, At, B1); PG8_BAR;
;             PG8_LDB(B0, 1, 0); PG8_SCHED; PG8_LDA(At, 1, 0); PG8_STAGE(PG8_SA(0, 1), a2 + hstep, voffA);
;             PG8_WAIT_L(8); PG8_BAR; PG8_WAIT_L(0); PG8_MMA(0, 0, At, B0); PG8_BAR; PG8_SCHED;
;             PG8_LDB(B1, 1, 1); PG8_STAGE(PG8_SB(1, 0), b3, voffB);
;             PG8_BAR; PG8_WAIT_L(0); PG8_MMA(0, 1, At, B1); PG8_BAR;
;             PG8_LDA(At, 1, 1); PG8_STAGE(PG8_SA(1, 0), a3, voffA);
;             PG8_BAR; PG8_WAIT_L(0); PG8_MMA(1, 0, At, B0); PG8_BAR; PG8_SCHED;
;             PG8_STAGE(PG8_SB(1, 1), b3 + hstep, voffB);
;             PG8_WAIT_V(6); PG8_BAR; PG8_MMA(1, 1, At, B1); PG8_BAR;
;     ...
;             if (GATHER && last && has_next) {
;                 const LAS int* ib_ = (const LAS int*)(lds + STAGE_BYTES + ((ui + 1) & 1) * 1024);
; #pragma unroll
.LBB0_1504:
	s_mov_b64 s[30:31], 0x100
	v_lshl_add_u64 v[4:5], v[4:5], 0, s[30:31]
	s_add_u32 s30, s28, 0xb0080
	s_addc_u32 s31, s29, 0
	v_lshl_add_u64 v[148:149], s[30:31], 0, v[142:143]
	v_lshl_add_u64 v[150:151], s[30:31], 0, v[144:145]
	s_mov_b32 s63, -2
	s_mov_b64 s[34:35], 0
	s_mov_b64 s[76:77], 0xb0080
	s_add_u32 s30, s34, 0x100
	s_addc_u32 s31, s35, 0
	s_add_i32 s64, 0, 0x10000
	s_add_i32 s65, 0, 0x14000
	v_add_u32_e32 v2, s64, v153
	ds_read_b128 v[158:161], v2
	ds_read_b128 v[162:165], v2 offset:1024
	ds_read_b128 v[166:169], v2 offset:2048
	ds_read_b128 v[170:173], v2 offset:3072
	v_add_u32_e32 v2, s65, v153
	ds_read_b128 v[174:177], v2
	ds_read_b128 v[178:181], v2 offset:1024
	ds_read_b128 v[182:185], v2 offset:2048
	ds_read_b128 v[186:189], v2 offset:3072
	s_add_i32 s67, s64, s48
	s_add_i32 m0, s51, 0xc000
	s_add_i32 s66, s51, 0xe000
	s_add_i32 s68, s67, 0x2000
	s_cmp_eq_u32 s63, 40
	v_lshl_add_u64 v[190:191], v[4:5], 0, s[34:35]
	s_cselect_b64 vcc, -1, 0
	v_cndmask_b32_e32 v199, v191, v147, vcc
	v_cndmask_b32_e32 v198, v190, v146, vcc
	s_cselect_b32 s64, 0, s30
	v_lshl_add_u64 v[226:227], v[148:149], 0, s[34:35]
	ds_read_b128 v[190:193], v155
	ds_read_b128 v[194:197], v155 offset:1024
	ds_read_b128 v[202:205], v155 offset:2048
	ds_read_b128 v[206:209], v155 offset:3072
	ds_read_b128 v[210:213], v155 offset:4096
	ds_read_b128 v[214:217], v155 offset:5120
	ds_read_b128 v[218:221], v155 offset:6144
	ds_read_b128 v[222:225], v155 offset:7168
	global_load_lds_dwordx4 v[226:227], off
	v_lshl_add_u64 v[226:227], v[150:151], 0, s[34:35]
	s_mov_b32 m0, s66
	s_nop 0
	global_load_lds_dwordx4 v[226:227], off
	s_waitcnt vmcnt(8)
	s_waitcnt lgkmcnt(0)
	s_barrier
	v_mfma_f32_16x16x32_bf16 v[90:93], v[158:161], v[190:193], 0
	v_mfma_f32_16x16x32_bf16 v[18:21], v[166:169], v[190:193], 0
	v_mfma_f32_16x16x32_bf16 v[6:9], v[158:161], v[202:205], 0
	v_mfma_f32_16x16x32_bf16 v[22:25], v[166:169], v[202:205], 0
	v_mfma_f32_16x16x32_bf16 v[10:13], v[158:161], v[210:213], 0
	v_mfma_f32_16x16x32_bf16 v[26:29], v[166:169], v[210:213], 0
	v_mfma_f32_16x16x32_bf16 v[14:17], v[158:161], v[218:221], 0
	v_mfma_f32_16x16x32_bf16 v[30:33], v[166:169], v[218:221], 0
	v_mfma_f32_16x16x32_bf16 v[90:93], v[162:165], v[194:197], v[90:93]
	v_mfma_f32_16x16x32_bf16 v[18:21], v[170:173], v[194:197], v[18:21]
	v_mfma_f32_16x16x32_bf16 v[6:9], v[162:165], v[206:209], v[6:9]
	v_mfma_f32_16x16x32_bf16 v[22:25], v[170:173], v[206:209], v[22:25]
	v_mfma_f32_16x16x32_bf16 v[10:13], v[162:165], v[214:217], v[10:13]
	v_mfma_f32_16x16x32_bf16 v[26:29], v[170:173], v[214:217], v[26:29]
	v_mfma_f32_16x16x32_bf16 v[14:17], v[162:165], v[222:225], v[14:17]
	v_mfma_f32_16x16x32_bf16 v[30:33], v[170:173], v[222:225], v[30:33]
	v_mfma_f32_16x16x32_bf16 v[34:37], v[174:177], v[190:193], 0
	v_mfma_f32_16x16x32_bf16 v[50:53], v[182:185], v[190:193], 0
	v_mfma_f32_16x16x32_bf16 v[38:41], v[174:177], v[202:205], 0
	v_mfma_f32_16x16x32_bf16 v[54:57], v[182:185], v[202:205], 0
	v_mfma_f32_16x16x32_bf16 v[42:45], v[174:177], v[210:213], 0
	v_mfma_f32_16x16x32_bf16 v[62:65], v[182:185], v[210:213], 0
	v_mfma_f32_16x16x32_bf16 v[46:49], v[174:177], v[218:221], 0
	v_mfma_f32_16x16x32_bf16 v[70:73], v[182:185], v[218:221], 0
	v_mfma_f32_16x16x32_bf16 v[34:37], v[178:181], v[194:197], v[34:37]
	v_mfma_f32_16x16x32_bf16 v[50:53], v[186:189], v[194:197], v[50:53]
	v_mfma_f32_16x16x32_bf16 v[38:41], v[178:181], v[206:209], v[38:41]
	v_mfma_f32_16x16x32_bf16 v[54:57], v[186:189], v[206:209], v[54:57]
	v_mfma_f32_16x16x32_bf16 v[42:45], v[178:181], v[214:217], v[42:45]
	v_mfma_f32_16x16x32_bf16 v[62:65], v[186:189], v[214:217], v[62:65]
	v_mfma_f32_16x16x32_bf16 v[46:49], v[178:181], v[222:225], v[46:49]
	v_mfma_f32_16x16x32_bf16 v[70:73], v[186:189], v[222:225], v[70:73]
	s_barrier
	s_mov_b32 m0, s67
	v_lshl_add_u64 v[226:227], v[198:199], 0, v[138:139]
	ds_read_b128 v[190:193], v155 offset:16384
	ds_read_b128 v[194:197], v155 offset:17408
	ds_read_b128 v[202:205], v155 offset:18432
	ds_read_b128 v[206:209], v155 offset:19456
	ds_read_b128 v[210:213], v155 offset:20480
	ds_read_b128 v[214:217], v155 offset:21504
	ds_read_b128 v[218:221], v155 offset:22528
	ds_read_b128 v[222:225], v155 offset:23552
	global_load_lds_dwordx4 v[226:227], off
	v_lshl_add_u64 v[228:229], v[198:199], 0, v[134:135]
	s_mov_b32 m0, s68
	s_cselect_b32 s35, s11, s29
	s_cselect_b32 s34, s10, s28
	v_lshl_add_u64 v[230:231], v[198:199], 0, s[72:73]
	s_add_i32 s65, s65, s48
	global_load_lds_dwordx4 v[228:229], off
	v_lshl_add_u64 v[232:233], v[230:231], 0, v[138:139]
	s_mov_b32 m0, s65
	v_lshl_add_u64 v[230:231], v[230:231], 0, v[134:135]
	global_load_lds_dwordx4 v[232:233], off
	s_add_i32 m0, s65, 0x2000
	s_add_u32 s34, s34, s64
	s_addc_u32 s35, s35, 0
	global_load_lds_dwordx4 v[230:231], off
	v_lshl_add_u64 v[230:231], s[34:35], 0, v[140:141]
	s_mov_b32 m0, s51
	v_lshl_add_u64 v[232:233], s[34:35], 0, v[136:137]
	global_load_lds_dwordx4 v[230:231], off
	s_mov_b32 m0, s52
	s_nop 0
	global_load_lds_dwordx4 v[232:233], off
	s_waitcnt vmcnt(8)
	s_waitcnt lgkmcnt(0)
	s_barrier
; #define PG8_STAGE_A(bufoff, base_, nx_, kb_, h_) do { if (GATHER) { if (nx_) PG8_STAGE_G(bufoff, kb_, goN, h_); else PG8_STAGE_G(bufoff, kb_, goC, h_); } \
;         else PG8_STAGE(bufoff, (base_) + (kb_) + (h_) * hstep, voffA); } while (0)
; #define PG8_STAGE(bufoff, gbase, voff) do { _Pragma("unroll") for (int _i = 0; _i < 2; ++_i) \
;         __builtin_amdgcn_global_load_lds((const unsigned*)((const char*)(gbase) + (voff)[_i]), (LAS unsigned*)(lds + (bufoff) + ldsw + _i * 8192), 16, 0, 0); } while (0)
; #define PG8_LDA(dst, b, h) do { _Pragma("unroll") for (int m = 0; m < 4; ++m) _Pragma("unroll") for (int k = 0; k < 2; ++k) dst[m][k] = *(const LAS bf16x8*)(lds + PG8_SA(b, h) + aoff + m * 2048 + k * 1024); } while (0)
; #define PG8_LDB(dst, b, h) do { _Pragma("unroll") for (int n = 0; n < 2; ++n) _Pragma("unroll") for (int k = 0; k < 2; ++k) dst[n][k] = *(const LAS bf16x8*)(lds + PG8_SB(b, h) + boff + n * 2048 + k * 1024); } while (0)
; #define PG8_WAIT_V(n) asm volatile("s_waitcnt vmcnt(" #n ")" ::: "memory")
; #define PG8_WAIT_L(n) asm volatile("s_waitcnt lgkmcnt(" #n ")" ::: "memory")
; template <class Epi, class Sched, bool GATHER = false>
; __device__ __forceinline__ void gemm_phase(LAS unsigned char* lds, const Gemm g, const Sched& S, const Epi& E, const int tid) {
;     ...
;             PG8_LDB(B0, 0, 0); PG8_LDB(B1, 0, 1); PG8_SCHED; PG8_LDA(At, 0, 0); PG8_STAGE_A(PG8_SA(1, 1), cA, false, kb1, 1);
;             PG8_WAIT_V(8); PG8_WAIT_L(0); PG8_BAR; PG8_MMA(0, 0, At, B0); PG8_MMA(0, 1, At, B1); PG8_BAR; PG8_SCHED;
;             PG8_LDA(At, 0, 1); PG8_STAGE(PG8_SB(0, 0), b2, voffB); PG8_STAGE(PG8_SB(0, 1), b2 + hstep, voffB); PG8_STAGE_A(PG8_SA(0, 0), (last ? nA : cA), last, kb2, 0);
;             PG8_WAIT_V(8); PG8_WAIT_L(0); PG8_BAR; PG8_MMA(1, 0, At, B0); PG8_MMA(1, 1, At, B1); PG8_BAR; PG8_SCHED;
;             PG8_LDB(B0, 1, 0); PG8_LDB(B1, 1, 1); PG8_SCHED; PG8_LDA(At, 1, 0); PG8_STAGE_A(PG8_SA(0, 1), (last ? nA : cA), last, kb2, 1);
;             PG8_WAIT_V(8); PG8_WAIT_L(0); PG8_BAR; PG8_MMA(0, 0, At, B0); PG8_MMA(0, 1, At, B1); PG8_BAR; PG8_SCHED;
;             PG8_LDA(At, 1, 1); PG8_STAGE(PG8_SB(1, 0), b3, voffB); PG8_STAGE(PG8_SB(1, 1), b3 + hstep, voffB); PG8_STAGE_A(PG8_SA(1, 0), (last ? nA : cA), last, kb3, 0);
;             PG8_WAIT_V(8); PG8_WAIT_L(0); PG8_BAR; PG8_MMA(1, 0, At, B0); PG8_MMA(1, 1, At, B1); PG8_BAR; PG8_SCHED;
	v_mfma_f32_16x16x32_bf16 v[58:61], v[158:161], v[190:193], 0
	v_mfma_f32_16x16x32_bf16 v[78:81], v[166:169], v[190:193], 0
	v_mfma_f32_16x16x32_bf16 v[66:69], v[158:161], v[202:205], 0
	v_mfma_f32_16x16x32_bf16 v[82:85], v[166:169], v[202:205], 0
	v_mfma_f32_16x16x32_bf16 v[74:77], v[158:161], v[210:213], 0
	v_mfma_f32_16x16x32_bf16 v[86:89], v[166:169], v[210:213], 0
	v_mfma_f32_16x16x32_bf16 v[94:97], v[158:161], v[218:221], 0
	v_mfma_f32_16x16x32_bf16 v[98:101], v[166:169], v[218:221], 0
	v_mfma_f32_16x16x32_bf16 v[58:61], v[162:165], v[194:197], v[58:61]
	v_mfma_f32_16x16x32_bf16 v[78:81], v[170:173], v[194:197], v[78:81]
	v_mfma_f32_16x16x32_bf16 v[66:69], v[162:165], v[206:209], v[66:69]
	v_mfma_f32_16x16x32_bf16 v[82:85], v[170:173], v[206:209], v[82:85]
	v_mfma_f32_16x16x32_bf16 v[74:77], v[162:165], v[214:217], v[74:77]
	v_mfma_f32_16x16x32_bf16 v[86:89], v[170:173], v[214:217], v[86:89]
	v_mfma_f32_16x16x32_bf16 v[94:97], v[162:165], v[222:225], v[94:97]
	v_mfma_f32_16x16x32_bf16 v[98:101], v[170:173], v[222:225], v[98:101]
	v_mfma_f32_16x16x32_bf16 v[114:117], v[174:177], v[190:193], 0
	v_mfma_f32_16x16x32_bf16 v[130:133], v[182:185], v[190:193], 0
	v_mfma_f32_16x16x32_bf16 v[110:113], v[174:177], v[202:205], 0
	v_mfma_f32_16x16x32_bf16 v[126:129], v[182:185], v[202:205], 0
	v_mfma_f32_16x16x32_bf16 v[106:109], v[174:177], v[210:213], 0
	v_mfma_f32_16x16x32_bf16 v[122:125], v[182:185], v[210:213], 0
	v_mfma_f32_16x16x32_bf16 v[102:105], v[174:177], v[218:221], 0
	v_mfma_f32_16x16x32_bf16 v[118:121], v[182:185], v[218:221], 0
	v_mfma_f32_16x16x32_bf16 v[114:117], v[178:181], v[194:197], v[114:117]
	v_mfma_f32_16x16x32_bf16 v[130:133], v[186:189], v[194:197], v[130:133]
	v_mfma_f32_16x16x32_bf16 v[110:113], v[178:181], v[206:209], v[110:113]
	v_mfma_f32_16x16x32_bf16 v[126:129], v[186:189], v[206:209], v[126:129]
	v_mfma_f32_16x16x32_bf16 v[106:109], v[178:181], v[214:217], v[106:109]
	v_mfma_f32_16x16x32_bf16 v[122:125], v[186:189], v[214:217], v[122:125]
	v_mfma_f32_16x16x32_bf16 v[102:105], v[178:181], v[222:225], v[102:105]
	v_mfma_f32_16x16x32_bf16 v[118:121], v[186:189], v[222:225], v[118:121]
	s_barrier
	s_add_i32 s64, 0, 0x18000
	v_add_u32_e32 v2, s64, v153
	s_add_i32 s65, 0, 0x1c000
	ds_read_b128 v[158:161], v2
	ds_read_b128 v[162:165], v2 offset:1024
	ds_read_b128 v[166:169], v2 offset:2048
	ds_read_b128 v[170:173], v2 offset:3072
	v_add_u32_e32 v2, s65, v153
	ds_read_b128 v[174:177], v2
	ds_read_b128 v[178:181], v2 offset:1024
	ds_read_b128 v[182:185], v2 offset:2048
	ds_read_b128 v[186:189], v2 offset:3072
	s_add_u32 s34, s34, 0xb0000
	s_addc_u32 s35, s35, 0
	s_mov_b32 m0, s53
	v_lshl_add_u64 v[234:235], s[34:35], 0, v[140:141]
	ds_read_b128 v[190:193], v155 offset:32768
	ds_read_b128 v[194:197], v155 offset:33792
	ds_read_b128 v[202:205], v155 offset:34816
	ds_read_b128 v[206:209], v155 offset:35840
	ds_read_b128 v[210:213], v155 offset:36864
	ds_read_b128 v[214:217], v155 offset:37888
	ds_read_b128 v[218:221], v155 offset:38912
	ds_read_b128 v[222:225], v155 offset:39936
	global_load_lds_dwordx4 v[234:235], off
	v_lshl_add_u64 v[234:235], s[34:35], 0, v[136:137]
	s_mov_b32 m0, s54
	s_nop 0
	global_load_lds_dwordx4 v[234:235], off
	s_waitcnt vmcnt(8)
	s_waitcnt lgkmcnt(0)
	s_barrier
	v_mfma_f32_16x16x32_bf16 v[90:93], v[158:161], v[190:193], v[90:93]
	v_mfma_f32_16x16x32_bf16 v[18:21], v[166:169], v[190:193], v[18:21]
	v_mfma_f32_16x16x32_bf16 v[6:9], v[158:161], v[202:205], v[6:9]
	v_mfma_f32_16x16x32_bf16 v[22:25], v[166:169], v[202:205], v[22:25]
	v_mfma_f32_16x16x32_bf16 v[10:13], v[158:161], v[210:213], v[10:13]
	v_mfma_f32_16x16x32_bf16 v[26:29], v[166:169], v[210:213], v[26:29]
	v_mfma_f32_16x16x32_bf16 v[14:17], v[158:161], v[218:221], v[14:17]
	v_mfma_f32_16x16x32_bf16 v[30:33], v[166:169], v[218:221], v[30:33]
	v_mfma_f32_16x16x32_bf16 v[90:93], v[162:165], v[194:197], v[90:93]
	v_mfma_f32_16x16x32_bf16 v[18:21], v[170:173], v[194:197], v[18:21]
	v_mfma_f32_16x16x32_bf16 v[6:9], v[162:165], v[206:209], v[6:9]
	v_mfma_f32_16x16x32_bf16 v[22:25], v[170:173], v[206:209], v[22:25]
	v_mfma_f32_16x16x32_bf16 v[10:13], v[162:165], v[214:217], v[10:13]
	v_mfma_f32_16x16x32_bf16 v[26:29], v[170:173], v[214:217], v[26:29]
	v_mfma_f32_16x16x32_bf16 v[14:17], v[162:165], v[222:225], v[14:17]
	v_mfma_f32_16x16x32_bf16 v[30:33], v[170:173], v[222:225], v[30:33]
	v_mfma_f32_16x16x32_bf16 v[34:37], v[174:177], v[190:193], v[34:37]
	v_mfma_f32_16x16x32_bf16 v[50:53], v[182:185], v[190:193], v[50:53]
	v_mfma_f32_16x16x32_bf16 v[38:41], v[174:177], v[202:205], v[38:41]
	v_mfma_f32_16x16x32_bf16 v[54:57], v[182:185], v[202:205], v[54:57]
	v_mfma_f32_16x16x32_bf16 v[42:45], v[174:177], v[210:213], v[42:45]
	v_mfma_f32_16x16x32_bf16 v[62:65], v[182:185], v[210:213], v[62:65]
	v_mfma_f32_16x16x32_bf16 v[46:49], v[174:177], v[218:221], v[46:49]
	v_mfma_f32_16x16x32_bf16 v[70:73], v[182:185], v[218:221], v[70:73]
	v_mfma_f32_16x16x32_bf16 v[34:37], v[178:181], v[194:197], v[34:37]
	v_mfma_f32_16x16x32_bf16 v[50:53], v[186:189], v[194:197], v[50:53]
	v_mfma_f32_16x16x32_bf16 v[38:41], v[178:181], v[206:209], v[38:41]
	v_mfma_f32_16x16x32_bf16 v[54:57], v[186:189], v[206:209], v[54:57]
	v_mfma_f32_16x16x32_bf16 v[42:45], v[178:181], v[214:217], v[42:45]
	v_mfma_f32_16x16x32_bf16 v[62:65], v[186:189], v[214:217], v[62:65]
	v_mfma_f32_16x16x32_bf16 v[46:49], v[178:181], v[222:225], v[46:49]
	v_mfma_f32_16x16x32_bf16 v[70:73], v[186:189], v[222:225], v[70:73]
	s_barrier
; #define PG8_STAGE_A(bufoff, base_, nx_, kb_, h_) do { if (GATHER) { if (nx_) PG8_STAGE_G(bufoff, kb_, goN, h_); else PG8_STAGE_G(bufoff, kb_, goC, h_); } \
;         else PG8_STAGE(bufoff, (base_) + (kb_) + (h_) * hstep, voffA); } while (0)
; #define PG8_STAGE(bufoff, gbase, voff) do { _Pragma("unroll") for (int _i = 0; _i < 2; ++_i) \
;         __builtin_amdgcn_global_load_lds((const unsigned*)((const char*)(gbase) + (voff)[_i]), (LAS unsigned*)(lds + (bufoff) + ldsw + _i * 8192), 16, 0, 0); } while (0)
; #define PG8_LDA(dst, b, h) do { _Pragma("unroll") for (int m = 0; m < 4; ++m) _Pragma("unroll") for (int k = 0; k < 2; ++k) dst[m][k] = *(const LAS bf16x8*)(lds + PG8_SA(b, h) + aoff + m * 2048 + k * 1024); } while (0)
; #define PG8_MMA(ai, bj, At, Bt) do { __builtin_amdgcn_s_setprio(1); _Pragma("unroll") for (int m = 0; m < 4; ++m) _Pragma("unroll") for (int n = 0; n < 2; ++n) _Pragma("unroll") for (int k = 0; k < 2; ++k) \
;         acc[ai][bj][m][n] = __builtin_amdgcn_mfma_f32_16x16x32_bf16(Bt[n][k], At[m][k], acc[ai][bj][m][n], 0, 0, 0); __builtin_amdgcn_s_setprio(0); } while (0)
; #define PG8_WAIT_V(n) asm volatile("s_waitcnt vmcnt(" #n ")" ::: "memory")
; #define PG8_WAIT_L(n) asm volatile("s_waitcnt lgkmcnt(" #n ")" ::: "memory")
; #define PG8_BAR __builtin_amdgcn_s_barrier()
; #define PG8_SCHED __builtin_amdgcn_sched_barrier(0)
; template <class Epi, class Sched, bool GATHER = false>
; __device__ __forceinline__ void gemm_phase(LAS unsigned char* lds, const Gemm g, const Sched& S, const Epi& E, const int tid) {
;     ...
;         for (int t = 0; t < nt; t += 2) {
;             const bool last = (t == nt - 2);
;             const char* a1 = cA + (size_t)(t + 1) * kstep;
;             const char* a2 = last ? nA : cA + (size_t)(t + 2) * kstep; const char* b2 = last ? nB : cB + (size_t)(t + 2) * kstep;
;             const char* a3 = a2 + kstep; const char* b3 = b2 + kstep;
;     ...
;             PG8_LDA(At, 1, 1); PG8_STAGE(PG8_SB(1, 0), b3, voffB); PG8_STAGE(PG8_SB(1, 1), b3 + hstep, voffB); PG8_STAGE_A(PG8_SA(1, 0), (last ? nA : cA), last, kb3, 0);
;             PG8_WAIT_V(8); PG8_WAIT_L(0); PG8_BAR; PG8_MMA(1, 0, At, B0); PG8_MMA(1, 1, At, B1); PG8_BAR; PG8_SCHED;
	s_add_i32 s34, s64, s48
	v_lshl_add_u64 v[226:227], v[226:227], 0, s[0:1]
	s_mov_b32 m0, s34
	ds_read_b128 v[190:193], v155 offset:49152
	ds_read_b128 v[194:197], v155 offset:50176
	ds_read_b128 v[202:205], v155 offset:51200
	ds_read_b128 v[206:209], v155 offset:52224
	ds_read_b128 v[210:213], v155 offset:53248
	ds_read_b128 v[214:217], v155 offset:54272
	ds_read_b128 v[218:221], v155 offset:55296
	ds_read_b128 v[222:225], v155 offset:56320
	global_load_lds_dwordx4 v[226:227], off
	v_lshl_add_u64 v[226:227], v[228:229], 0, s[0:1]
	s_add_i32 m0, s34, 0x2000
	v_lshl_add_u64 v[198:199], v[198:199], 0, s[76:77]
	s_add_i32 s34, s65, s48
	global_load_lds_dwordx4 v[226:227], off
	v_lshl_add_u64 v[226:227], v[198:199], 0, v[138:139]
	s_mov_b32 m0, s34
	v_lshl_add_u64 v[198:199], v[198:199], 0, v[134:135]
	global_load_lds_dwordx4 v[226:227], off
	s_add_i32 m0, s34, 0x2000
	s_nop 0
	global_load_lds_dwordx4 v[198:199], off
	v_lshl_add_u64 v[198:199], v[230:231], 0, s[0:1]
	s_mov_b32 m0, s55
	s_nop 0
	global_load_lds_dwordx4 v[198:199], off
	v_lshl_add_u64 v[198:199], v[232:233], 0, s[0:1]
	s_mov_b32 m0, s56
	s_nop 0
	global_load_lds_dwordx4 v[198:199], off
	s_waitcnt vmcnt(8)
	s_waitcnt lgkmcnt(0)
	s_barrier
	v_mfma_f32_16x16x32_bf16 v[58:61], v[158:161], v[190:193], v[58:61]
	v_mfma_f32_16x16x32_bf16 v[78:81], v[166:169], v[190:193], v[78:81]
	v_mfma_f32_16x16x32_bf16 v[66:69], v[158:161], v[202:205], v[66:69]
	v_mfma_f32_16x16x32_bf16 v[82:85], v[166:169], v[202:205], v[82:85]
	v_mfma_f32_16x16x32_bf16 v[74:77], v[158:161], v[210:213], v[74:77]
	v_mfma_f32_16x16x32_bf16 v[86:89], v[166:169], v[210:213], v[86:89]
	v_mfma_f32_16x16x32_bf16 v[94:97], v[158:161], v[218:221], v[94:97]
	v_mfma_f32_16x16x32_bf16 v[98:101], v[166:169], v[218:221], v[98:101]
	v_mfma_f32_16x16x32_bf16 v[58:61], v[162:165], v[194:197], v[58:61]
	v_mfma_f32_16x16x32_bf16 v[78:81], v[170:173], v[194:197], v[78:81]
	v_mfma_f32_16x16x32_bf16 v[66:69], v[162:165], v[206:209], v[66:69]
	v_mfma_f32_16x16x32_bf16 v[82:85], v[170:173], v[206:209], v[82:85]
	v_mfma_f32_16x16x32_bf16 v[74:77], v[162:165], v[214:217], v[74:77]
	v_mfma_f32_16x16x32_bf16 v[86:89], v[170:173], v[214:217], v[86:89]
	v_mfma_f32_16x16x32_bf16 v[94:97], v[162:165], v[222:225], v[94:97]
	v_mfma_f32_16x16x32_bf16 v[98:101], v[170:173], v[222:225], v[98:101]
	v_mfma_f32_16x16x32_bf16 v[114:117], v[174:177], v[190:193], v[114:117]
	v_mfma_f32_16x16x32_bf16 v[130:133], v[182:185], v[190:193], v[130:133]
	v_mfma_f32_16x16x32_bf16 v[110:113], v[174:177], v[202:205], v[110:113]
	v_mfma_f32_16x16x32_bf16 v[126:129], v[182:185], v[202:205], v[126:129]
	v_mfma_f32_16x16x32_bf16 v[106:109], v[174:177], v[210:213], v[106:109]
	v_mfma_f32_16x16x32_bf16 v[122:125], v[182:185], v[210:213], v[122:125]
	v_mfma_f32_16x16x32_bf16 v[102:105], v[174:177], v[218:221], v[102:105]
	v_mfma_f32_16x16x32_bf16 v[118:121], v[182:185], v[218:221], v[118:121]
	v_mfma_f32_16x16x32_bf16 v[114:117], v[178:181], v[194:197], v[114:117]
	v_mfma_f32_16x16x32_bf16 v[130:133], v[186:189], v[194:197], v[130:133]
	v_mfma_f32_16x16x32_bf16 v[110:113], v[178:181], v[206:209], v[110:113]
	v_mfma_f32_16x16x32_bf16 v[126:129], v[186:189], v[206:209], v[126:129]
	v_mfma_f32_16x16x32_bf16 v[106:109], v[178:181], v[214:217], v[106:109]
	v_mfma_f32_16x16x32_bf16 v[122:125], v[186:189], v[214:217], v[122:125]
	v_mfma_f32_16x16x32_bf16 v[102:105], v[178:181], v[222:225], v[102:105]
	v_mfma_f32_16x16x32_bf16 v[118:121], v[186:189], v[222:225], v[118:121]
	s_barrier
	s_add_i32 s63, s63, 2
	s_cmp_gt_u32 s63, 41
	s_mov_b64 s[34:35], s[30:31]
	s_cbranch_scc1 .Lpeel4_exit
.LBB0_1505:
	s_add_u32 s30, s34, 0x100
	s_addc_u32 s31, s35, 0
	s_add_i32 s64, 0, 0x10000
	s_add_i32 s65, 0, 0x14000
	v_add_u32_e32 v2, s64, v153
	ds_read_b128 v[158:161], v2
	ds_read_b128 v[162:165], v2 offset:1024
	ds_read_b128 v[166:169], v2 offset:2048
	ds_read_b128 v[170:173], v2 offset:3072
	v_add_u32_e32 v2, s65, v153
	ds_read_b128 v[174:177], v2
	ds_read_b128 v[178:181], v2 offset:1024
	ds_read_b128 v[182:185], v2 offset:2048
	ds_read_b128 v[186:189], v2 offset:3072
	s_add_i32 s67, s64, s48
	s_add_i32 m0, s51, 0xc000
	s_add_i32 s66, s51, 0xe000
	s_add_i32 s68, s67, 0x2000
	s_cmp_eq_u32 s63, 40
	v_lshl_add_u64 v[190:191], v[4:5], 0, s[34:35]
	s_cselect_b64 vcc, -1, 0
	v_cndmask_b32_e32 v199, v191, v147, vcc
	v_cndmask_b32_e32 v198, v190, v146, vcc
	s_cselect_b32 s64, 0, s30
	v_lshl_add_u64 v[226:227], v[148:149], 0, s[34:35]
	ds_read_b128 v[190:193], v155
	ds_read_b128 v[194:197], v155 offset:1024
	ds_read_b128 v[202:205], v155 offset:2048
	ds_read_b128 v[206:209], v155 offset:3072
	ds_read_b128 v[210:213], v155 offset:4096
	ds_read_b128 v[214:217], v155 offset:5120
	ds_read_b128 v[218:221], v155 offset:6144
	ds_read_b128 v[222:225], v155 offset:7168
	global_load_lds_dwordx4 v[226:227], off
	v_lshl_add_u64 v[226:227], v[150:151], 0, s[34:35]
	s_mov_b32 m0, s66
	s_nop 0
	global_load_lds_dwordx4 v[226:227], off
	s_waitcnt vmcnt(8)
	s_waitcnt lgkmcnt(0)
	s_barrier
; #define PG8_STAGE_A(bufoff, base_, nx_, kb_, h_) do { if (GATHER) { if (nx_) PG8_STAGE_G(bufoff, kb_, goN, h_); else PG8_STAGE_G(bufoff, kb_, goC, h_); } \
;         else PG8_STAGE(bufoff, (base_) + (kb_) + (h_) * hstep, voffA); } while (0)
; #define PG8_STAGE(bufoff, gbase, voff) do { _Pragma("unroll") for (int _i = 0; _i < 2; ++_i) \
;         __builtin_amdgcn_global_load_lds((const unsigned*)((const char*)(gbase) + (voff)[_i]), (LAS unsigned*)(lds + (bufoff) + ldsw + _i * 8192), 16, 0, 0); } while (0)
; #define PG8_LDA(dst, b, h) do { _Pragma("unroll") for (int m = 0; m < 4; ++m) _Pragma("unroll") for (int k = 0; k < 2; ++k) dst[m][k] = *(const LAS bf16x8*)(lds + PG8_SA(b, h) + aoff + m * 2048 + k * 1024); } while (0)
; #define PG8_LDB(dst, b, h) do { _Pragma("unroll") for (int n = 0; n < 2; ++n) _Pragma("unroll") for (int k = 0; k < 2; ++k) dst[n][k] = *(const LAS bf16x8*)(lds + PG8_SB(b, h) + boff + n * 2048 + k * 1024); } while (0)
; #define PG8_WAIT_V(n) asm volatile("s_waitcnt vmcnt(" #n ")" ::: "memory")
; #define PG8_WAIT_L(n) asm volatile("s_waitcnt lgkmcnt(" #n ")" ::: "memory")
; template <class Epi, class Sched, bool GATHER = false>
; __device__ __forceinline__ void gemm_phase(LAS unsigned char* lds, const Gemm g, const Sched& S, const Epi& E, const int tid) {
;     ...
;             PG8_LDB(B0, 0, 0); PG8_LDB(B1, 0, 1); PG8_SCHED; PG8_LDA(At, 0, 0); PG8_STAGE_A(PG8_SA(1, 1), cA, false, kb1, 1);
;             PG8_WAIT_V(8); PG8_WAIT_L(0); PG8_BAR; PG8_MMA(0, 0, At, B0); PG8_MMA(0, 1, At, B1); PG8_BAR; PG8_SCHED;
;             PG8_LDA(At, 0, 1); PG8_STAGE(PG8_SB(0, 0), b2, voffB); PG8_STAGE(PG8_SB(0, 1), b2 + hstep, voffB); PG8_STAGE_A(PG8_SA(0, 0), (last ? nA : cA), last, kb2, 0);
;             PG8_WAIT_V(8); PG8_WAIT_L(0); PG8_BAR; PG8_MMA(1, 0, At, B0); PG8_MMA(1, 1, At, B1); PG8_BAR; PG8_SCHED;
;             PG8_LDB(B0, 1, 0); PG8_LDB(B1, 1, 1); PG8_SCHED; PG8_LDA(At, 1, 0); PG8_STAGE_A(PG8_SA(0, 1), (last ? nA : cA), last, kb2, 1);
;             PG8_WAIT_V(8); PG8_WAIT_L(0); PG8_BAR; PG8_MMA(0, 0, At, B0); PG8_MMA(0, 1, At, B1); PG8_BAR; PG8_SCHED;
;             PG8_LDA(At, 1, 1); PG8_STAGE(PG8_SB(1, 0), b3, voffB); PG8_STAGE(PG8_SB(1, 1), b3 + hstep, voffB); PG8_STAGE_A(PG8_SA(1, 0), (last ? nA : cA), last, kb3, 0);
;             PG8_WAIT_V(8); PG8_WAIT_L(0); PG8_BAR; PG8_MMA(1, 0, At, B0); PG8_MMA(1, 1, At, B1); PG8_BAR; PG8_SCHED;
	v_mfma_f32_16x16x32_bf16 v[90:93], v[158:161], v[190:193], v[90:93]
	v_mfma_f32_16x16x32_bf16 v[18:21], v[166:169], v[190:193], v[18:21]
	v_mfma_f32_16x16x32_bf16 v[6:9], v[158:161], v[202:205], v[6:9]
	v_mfma_f32_16x16x32_bf16 v[22:25], v[166:169], v[202:205], v[22:25]
	v_mfma_f32_16x16x32_bf16 v[10:13], v[158:161], v[210:213], v[10:13]
	v_mfma_f32_16x16x32_bf16 v[26:29], v[166:169], v[210:213], v[26:29]
	v_mfma_f32_16x16x32_bf16 v[14:17], v[158:161], v[218:221], v[14:17]
	v_mfma_f32_16x16x32_bf16 v[30:33], v[166:169], v[218:221], v[30:33]
	v_mfma_f32_16x16x32_bf16 v[90:93], v[162:165], v[194:197], v[90:93]
	v_mfma_f32_16x16x32_bf16 v[18:21], v[170:173], v[194:197], v[18:21]
	v_mfma_f32_16x16x32_bf16 v[6:9], v[162:165], v[206:209], v[6:9]
	v_mfma_f32_16x16x32_bf16 v[22:25], v[170:173], v[206:209], v[22:25]
	v_mfma_f32_16x16x32_bf16 v[10:13], v[162:165], v[214:217], v[10:13]
	v_mfma_f32_16x16x32_bf16 v[26:29], v[170:173], v[214:217], v[26:29]
	v_mfma_f32_16x16x32_bf16 v[14:17], v[162:165], v[222:225], v[14:17]
	v_mfma_f32_16x16x32_bf16 v[30:33], v[170:173], v[222:225], v[30:33]
	v_mfma_f32_16x16x32_bf16 v[34:37], v[174:177], v[190:193], v[34:37]
	v_mfma_f32_16x16x32_bf16 v[50:53], v[182:185], v[190:193], v[50:53]
	v_mfma_f32_16x16x32_bf16 v[38:41], v[174:177], v[202:205], v[38:41]
	v_mfma_f32_16x16x32_bf16 v[54:57], v[182:185], v[202:205], v[54:57]
	v_mfma_f32_16x16x32_bf16 v[42:45], v[174:177], v[210:213], v[42:45]
	v_mfma_f32_16x16x32_bf16 v[62:65], v[182:185], v[210:213], v[62:65]
	v_mfma_f32_16x16x32_bf16 v[46:49], v[174:177], v[218:221], v[46:49]
	v_mfma_f32_16x16x32_bf16 v[70:73], v[182:185], v[218:221], v[70:73]
	v_mfma_f32_16x16x32_bf16 v[34:37], v[178:181], v[194:197], v[34:37]
	v_mfma_f32_16x16x32_bf16 v[50:53], v[186:189], v[194:197], v[50:53]
	v_mfma_f32_16x16x32_bf16 v[38:41], v[178:181], v[206:209], v[38:41]
	v_mfma_f32_16x16x32_bf16 v[54:57], v[186:189], v[206:209], v[54:57]
	v_mfma_f32_16x16x32_bf16 v[42:45], v[178:181], v[214:217], v[42:45]
	v_mfma_f32_16x16x32_bf16 v[62:65], v[186:189], v[214:217], v[62:65]
	v_mfma_f32_16x16x32_bf16 v[46:49], v[178:181], v[222:225], v[46:49]
	v_mfma_f32_16x16x32_bf16 v[70:73], v[186:189], v[222:225], v[70:73]
	s_barrier
	s_mov_b32 m0, s67
	v_lshl_add_u64 v[226:227], v[198:199], 0, v[138:139]
	ds_read_b128 v[190:193], v155 offset:16384
	ds_read_b128 v[194:197], v155 offset:17408
	ds_read_b128 v[202:205], v155 offset:18432
	ds_read_b128 v[206:209], v155 offset:19456
	ds_read_b128 v[210:213], v155 offset:20480
	ds_read_b128 v[214:217], v155 offset:21504
	ds_read_b128 v[218:221], v155 offset:22528
	ds_read_b128 v[222:225], v155 offset:23552
	global_load_lds_dwordx4 v[226:227], off
	v_lshl_add_u64 v[228:229], v[198:199], 0, v[134:135]
	s_mov_b32 m0, s68
	s_cselect_b32 s35, s11, s29
	s_cselect_b32 s34, s10, s28
	v_lshl_add_u64 v[230:231], v[198:199], 0, s[72:73]
	s_add_i32 s65, s65, s48
	global_load_lds_dwordx4 v[228:229], off
	v_lshl_add_u64 v[232:233], v[230:231], 0, v[138:139]
	s_mov_b32 m0, s65
	v_lshl_add_u64 v[230:231], v[230:231], 0, v[134:135]
	global_load_lds_dwordx4 v[232:233], off
	s_add_i32 m0, s65, 0x2000
	s_add_u32 s34, s34, s64
	s_addc_u32 s35, s35, 0
	global_load_lds_dwordx4 v[230:231], off
	v_lshl_add_u64 v[230:231], s[34:35], 0, v[140:141]
	s_mov_b32 m0, s51
	v_lshl_add_u64 v[232:233], s[34:35], 0, v[136:137]
	global_load_lds_dwordx4 v[230:231], off
	s_mov_b32 m0, s52
	s_nop 0
	global_load_lds_dwordx4 v[232:233], off
	s_waitcnt vmcnt(8)
	s_waitcnt lgkmcnt(0)
	s_barrier
	v_mfma_f32_16x16x32_bf16 v[58:61], v[158:161], v[190:193], v[58:61]
	v_mfma_f32_16x16x32_bf16 v[78:81], v[166:169], v[190:193], v[78:81]
	v_mfma_f32_16x16x32_bf16 v[66:69], v[158:161], v[202:205], v[66:69]
	v_mfma_f32_16x16x32_bf16 v[82:85], v[166:169], v[202:205], v[82:85]
	v_mfma_f32_16x16x32_bf16 v[74:77], v[158:161], v[210:213], v[74:77]
	v_mfma_f32_16x16x32_bf16 v[86:89], v[166:169], v[210:213], v[86:89]
	v_mfma_f32_16x16x32_bf16 v[94:97], v[158:161], v[218:221], v[94:97]
	v_mfma_f32_16x16x32_bf16 v[98:101], v[166:169], v[218:221], v[98:101]
	v_mfma_f32_16x16x32_bf16 v[58:61], v[162:165], v[194:197], v[58:61]
	v_mfma_f32_16x16x32_bf16 v[78:81], v[170:173], v[194:197], v[78:81]
	v_mfma_f32_16x16x32_bf16 v[66:69], v[162:165], v[206:209], v[66:69]
	v_mfma_f32_16x16x32_bf16 v[82:85], v[170:173], v[206:209], v[82:85]
	v_mfma_f32_16x16x32_bf16 v[74:77], v[162:165], v[214:217], v[74:77]
	v_mfma_f32_16x16x32_bf16 v[86:89], v[170:173], v[214:217], v[86:89]
	v_mfma_f32_16x16x32_bf16 v[94:97], v[162:165], v[222:225], v[94:97]
	v_mfma_f32_16x16x32_bf16 v[98:101], v[170:173], v[222:225], v[98:101]
	v_mfma_f32_16x16x32_bf16 v[114:117], v[174:177], v[190:193], v[114:117]
	v_mfma_f32_16x16x32_bf16 v[130:133], v[182:185], v[190:193], v[130:133]
	v_mfma_f32_16x16x32_bf16 v[110:113], v[174:177], v[202:205], v[110:113]
	v_mfma_f32_16x16x32_bf16 v[126:129], v[182:185], v[202:205], v[126:129]
	v_mfma_f32_16x16x32_bf16 v[106:109], v[174:177], v[210:213], v[106:109]
	v_mfma_f32_16x16x32_bf16 v[122:125], v[182:185], v[210:213], v[122:125]
	v_mfma_f32_16x16x32_bf16 v[102:105], v[174:177], v[218:221], v[102:105]
	v_mfma_f32_16x16x32_bf16 v[118:121], v[182:185], v[218:221], v[118:121]
	v_mfma_f32_16x16x32_bf16 v[114:117], v[178:181], v[194:197], v[114:117]
	v_mfma_f32_16x16x32_bf16 v[130:133], v[186:189], v[194:197], v[130:133]
	v_mfma_f32_16x16x32_bf16 v[110:113], v[178:181], v[206:209], v[110:113]
	v_mfma_f32_16x16x32_bf16 v[126:129], v[186:189], v[206:209], v[126:129]
	v_mfma_f32_16x16x32_bf16 v[106:109], v[178:181], v[214:217], v[106:109]
	v_mfma_f32_16x16x32_bf16 v[122:125], v[186:189], v[214:217], v[122:125]
	v_mfma_f32_16x16x32_bf16 v[102:105], v[178:181], v[222:225], v[102:105]
	v_mfma_f32_16x16x32_bf16 v[118:121], v[186:189], v[222:225], v[118:121]
	s_barrier
; #define PG8_STAGE_A(bufoff, base_, nx_, kb_, h_) do { if (GATHER) { if (nx_) PG8_STAGE_G(bufoff, kb_, goN, h_); else PG8_STAGE_G(bufoff, kb_, goC, h_); } \
;         else PG8_STAGE(bufoff, (base_) + (kb_) + (h_) * hstep, voffA); } while (0)
; #define PG8_STAGE(bufoff, gbase, voff) do { _Pragma("unroll") for (int _i = 0; _i < 2; ++_i) \
;         __builtin_amdgcn_global_load_lds((const unsigned*)((const char*)(gbase) + (voff)[_i]), (LAS unsigned*)(lds + (bufoff) + ldsw + _i * 8192), 16, 0, 0); } while (0)
; #define PG8_LDA(dst, b, h) do { _Pragma("unroll") for (int m = 0; m < 4; ++m) _Pragma("unroll") for (int k = 0; k < 2; ++k) dst[m][k] = *(const LAS bf16x8*)(lds + PG8_SA(b, h) + aoff + m * 2048 + k * 1024); } while (0)
; #define PG8_LDB(dst, b, h) do { _Pragma("unroll") for (int n = 0; n < 2; ++n) _Pragma("unroll") for (int k = 0; k < 2; ++k) dst[n][k] = *(const LAS bf16x8*)(lds + PG8_SB(b, h) + boff + n * 2048 + k * 1024); } while (0)
; #define PG8_MMA(ai, bj, At, Bt) do { __builtin_amdgcn_s_setprio(1); _Pragma("unroll") for (int m = 0; m < 4; ++m) _Pragma("unroll") for (int n = 0; n < 2; ++n) _Pragma("unroll") for (int k = 0; k < 2; ++k) \
;         acc[ai][bj][m][n] = __builtin_amdgcn_mfma_f32_16x16x32_bf16(Bt[n][k], At[m][k], acc[ai][bj][m][n], 0, 0, 0); __builtin_amdgcn_s_setprio(0); } while (0)
; #define PG8_WAIT_V(n) asm volatile("s_waitcnt vmcnt(" #n ")" ::: "memory")
; #define PG8_WAIT_L(n) asm volatile("s_waitcnt lgkmcnt(" #n ")" ::: "memory")
; #define PG8_BAR __builtin_amdgcn_s_barrier()
; #define PG8_SCHED __builtin_amdgcn_sched_barrier(0)
; template <class Epi, class Sched, bool GATHER = false>
; __device__ __forceinline__ void gemm_phase(LAS unsigned char* lds, const Gemm g, const Sched& S, const Epi& E, const int tid) {
;     ...
;             PG8_LDB(B0, 1, 0); PG8_LDB(B1, 1, 1); PG8_SCHED; PG8_LDA(At, 1, 0); PG8_STAGE_A(PG8_SA(0, 1), (last ? nA : cA), last, kb2, 1);
;             PG8_WAIT_V(8); PG8_WAIT_L(0); PG8_BAR; PG8_MMA(0, 0, At, B0); PG8_MMA(0, 1, At, B1); PG8_BAR; PG8_SCHED;
;             PG8_LDA(At, 1, 1); PG8_STAGE(PG8_SB(1, 0), b3, voffB); PG8_STAGE(PG8_SB(1, 1), b3 + hstep, voffB); PG8_STAGE_A(PG8_SA(1, 0), (last ? nA : cA), last, kb3, 0);
;             PG8_WAIT_V(8); PG8_WAIT_L(0); PG8_BAR; PG8_MMA(1, 0, At, B0); PG8_MMA(1, 1, At, B1); PG8_BAR; PG8_SCHED;
	s_add_i32 s64, 0, 0x18000
	v_add_u32_e32 v2, s64, v153
	s_add_i32 s65, 0, 0x1c000
	ds_read_b128 v[158:161], v2
	ds_read_b128 v[162:165], v2 offset:1024
	ds_read_b128 v[166:169], v2 offset:2048
	ds_read_b128 v[170:173], v2 offset:3072
	v_add_u32_e32 v2, s65, v153
	ds_read_b128 v[174:177], v2
	ds_read_b128 v[178:181], v2 offset:1024
	ds_read_b128 v[182:185], v2 offset:2048
	ds_read_b128 v[186:189], v2 offset:3072
	s_add_u32 s34, s34, 0xb0000
	s_addc_u32 s35, s35, 0
	s_mov_b32 m0, s53
	v_lshl_add_u64 v[234:235], s[34:35], 0, v[140:141]
	ds_read_b128 v[190:193], v155 offset:32768
	ds_read_b128 v[194:197], v155 offset:33792
	ds_read_b128 v[202:205], v155 offset:34816
	ds_read_b128 v[206:209], v155 offset:35840
	ds_read_b128 v[210:213], v155 offset:36864
	ds_read_b128 v[214:217], v155 offset:37888
	ds_read_b128 v[218:221], v155 offset:38912
	ds_read_b128 v[222:225], v155 offset:39936
	global_load_lds_dwordx4 v[234:235], off
	v_lshl_add_u64 v[234:235], s[34:35], 0, v[136:137]
	s_mov_b32 m0, s54
	s_nop 0
	global_load_lds_dwordx4 v[234:235], off
	s_waitcnt vmcnt(8)
	s_waitcnt lgkmcnt(0)
	s_barrier
	v_mfma_f32_16x16x32_bf16 v[90:93], v[158:161], v[190:193], v[90:93]
	v_mfma_f32_16x16x32_bf16 v[18:21], v[166:169], v[190:193], v[18:21]
	v_mfma_f32_16x16x32_bf16 v[6:9], v[158:161], v[202:205], v[6:9]
	v_mfma_f32_16x16x32_bf16 v[22:25], v[166:169], v[202:205], v[22:25]
	v_mfma_f32_16x16x32_bf16 v[10:13], v[158:161], v[210:213], v[10:13]
	v_mfma_f32_16x16x32_bf16 v[26:29], v[166:169], v[210:213], v[26:29]
	v_mfma_f32_16x16x32_bf16 v[14:17], v[158:161], v[218:221], v[14:17]
	v_mfma_f32_16x16x32_bf16 v[30:33], v[166:169], v[218:221], v[30:33]
	v_mfma_f32_16x16x32_bf16 v[90:93], v[162:165], v[194:197], v[90:93]
	v_mfma_f32_16x16x32_bf16 v[18:21], v[170:173], v[194:197], v[18:21]
	v_mfma_f32_16x16x32_bf16 v[6:9], v[162:165], v[206:209], v[6:9]
	v_mfma_f32_16x16x32_bf16 v[22:25], v[170:173], v[206:209], v[22:25]
	v_mfma_f32_16x16x32_bf16 v[10:13], v[162:165], v[214:217], v[10:13]
	v_mfma_f32_16x16x32_bf16 v[26:29], v[170:173], v[214:217], v[26:29]
	v_mfma_f32_16x16x32_bf16 v[14:17], v[162:165], v[222:225], v[14:17]
	v_mfma_f32_16x16x32_bf16 v[30:33], v[170:173], v[222:225], v[30:33]
	v_mfma_f32_16x16x32_bf16 v[34:37], v[174:177], v[190:193], v[34:37]
	v_mfma_f32_16x16x32_bf16 v[50:53], v[182:185], v[190:193], v[50:53]
	v_mfma_f32_16x16x32_bf16 v[38:41], v[174:177], v[202:205], v[38:41]
	v_mfma_f32_16x16x32_bf16 v[54:57], v[182:185], v[202:205], v[54:57]
	v_mfma_f32_16x16x32_bf16 v[42:45], v[174:177], v[210:213], v[42:45]
	v_mfma_f32_16x16x32_bf16 v[62:65], v[182:185], v[210:213], v[62:65]
	v_mfma_f32_16x16x32_bf16 v[46:49], v[174:177], v[218:221], v[46:49]
	v_mfma_f32_16x16x32_bf16 v[70:73], v[182:185], v[218:221], v[70:73]
	v_mfma_f32_16x16x32_bf16 v[34:37], v[178:181], v[194:197], v[34:37]
	v_mfma_f32_16x16x32_bf16 v[50:53], v[186:189], v[194:197], v[50:53]
	v_mfma_f32_16x16x32_bf16 v[38:41], v[178:181], v[206:209], v[38:41]
	v_mfma_f32_16x16x32_bf16 v[54:57], v[186:189], v[206:209], v[54:57]
	v_mfma_f32_16x16x32_bf16 v[42:45], v[178:181], v[214:217], v[42:45]
	v_mfma_f32_16x16x32_bf16 v[62:65], v[186:189], v[214:217], v[62:65]
	v_mfma_f32_16x16x32_bf16 v[46:49], v[178:181], v[222:225], v[46:49]
	v_mfma_f32_16x16x32_bf16 v[70:73], v[186:189], v[222:225], v[70:73]
	s_barrier
	s_add_i32 s34, s64, s48
	v_lshl_add_u64 v[226:227], v[226:227], 0, s[0:1]
	s_mov_b32 m0, s34
	ds_read_b128 v[190:193], v155 offset:49152
	ds_read_b128 v[194:197], v155 offset:50176
	ds_read_b128 v[202:205], v155 offset:51200
	ds_read_b128 v[206:209], v155 offset:52224
	ds_read_b128 v[210:213], v155 offset:53248
	ds_read_b128 v[214:217], v155 offset:54272
	ds_read_b128 v[218:221], v155 offset:55296
	ds_read_b128 v[222:225], v155 offset:56320
	global_load_lds_dwordx4 v[226:227], off
	v_lshl_add_u64 v[226:227], v[228:229], 0, s[0:1]
	s_add_i32 m0, s34, 0x2000
	v_lshl_add_u64 v[198:199], v[198:199], 0, s[76:77]
	s_add_i32 s34, s65, s48
	global_load_lds_dwordx4 v[226:227], off
	v_lshl_add_u64 v[226:227], v[198:199], 0, v[138:139]
	s_mov_b32 m0, s34
	v_lshl_add_u64 v[198:199], v[198:199], 0, v[134:135]
	global_load_lds_dwordx4 v[226:227], off
	s_add_i32 m0, s34, 0x2000
	s_nop 0
	global_load_lds_dwordx4 v[198:199], off
	v_lshl_add_u64 v[198:199], v[230:231], 0, s[0:1]
	s_mov_b32 m0, s55
	s_nop 0
	global_load_lds_dwordx4 v[198:199], off
	v_lshl_add_u64 v[198:199], v[232:233], 0, s[0:1]
	s_mov_b32 m0, s56
	s_nop 0
	global_load_lds_dwordx4 v[198:199], off
	s_waitcnt vmcnt(8)
	s_waitcnt lgkmcnt(0)
	s_barrier
	v_mfma_f32_16x16x32_bf16 v[58:61], v[158:161], v[190:193], v[58:61]
	v_mfma_f32_16x16x32_bf16 v[78:81], v[166:169], v[190:193], v[78:81]
	v_mfma_f32_16x16x32_bf16 v[66:69], v[158:161], v[202:205], v[66:69]
	v_mfma_f32_16x16x32_bf16 v[82:85], v[166:169], v[202:205], v[82:85]
	v_mfma_f32_16x16x32_bf16 v[74:77], v[158:161], v[210:213], v[74:77]
	v_mfma_f32_16x16x32_bf16 v[86:89], v[166:169], v[210:213], v[86:89]
	v_mfma_f32_16x16x32_bf16 v[94:97], v[158:161], v[218:221], v[94:97]
	v_mfma_f32_16x16x32_bf16 v[98:101], v[166:169], v[218:221], v[98:101]
	v_mfma_f32_16x16x32_bf16 v[58:61], v[162:165], v[194:197], v[58:61]
	v_mfma_f32_16x16x32_bf16 v[78:81], v[170:173], v[194:197], v[78:81]
	v_mfma_f32_16x16x32_bf16 v[66:69], v[162:165], v[206:209], v[66:69]
	v_mfma_f32_16x16x32_bf16 v[82:85], v[170:173], v[206:209], v[82:85]
	v_mfma_f32_16x16x32_bf16 v[74:77], v[162:165], v[214:217], v[74:77]
	v_mfma_f32_16x16x32_bf16 v[86:89], v[170:173], v[214:217], v[86:89]
	v_mfma_f32_16x16x32_bf16 v[94:97], v[162:165], v[222:225], v[94:97]
	v_mfma_f32_16x16x32_bf16 v[98:101], v[170:173], v[222:225], v[98:101]
	v_mfma_f32_16x16x32_bf16 v[114:117], v[174:177], v[190:193], v[114:117]
	v_mfma_f32_16x16x32_bf16 v[130:133], v[182:185], v[190:193], v[130:133]
	v_mfma_f32_16x16x32_bf16 v[110:113], v[174:177], v[202:205], v[110:113]
	v_mfma_f32_16x16x32_bf16 v[126:129], v[182:185], v[202:205], v[126:129]
	v_mfma_f32_16x16x32_bf16 v[106:109], v[174:177], v[210:213], v[106:109]
	v_mfma_f32_16x16x32_bf16 v[122:125], v[182:185], v[210:213], v[122:125]
	v_mfma_f32_16x16x32_bf16 v[102:105], v[174:177], v[218:221], v[102:105]
	v_mfma_f32_16x16x32_bf16 v[118:121], v[182:185], v[218:221], v[118:121]
	v_mfma_f32_16x16x32_bf16 v[114:117], v[178:181], v[194:197], v[114:117]
	v_mfma_f32_16x16x32_bf16 v[130:133], v[186:189], v[194:197], v[130:133]
	v_mfma_f32_16x16x32_bf16 v[110:113], v[178:181], v[206:209], v[110:113]
	v_mfma_f32_16x16x32_bf16 v[126:129], v[186:189], v[206:209], v[126:129]
	v_mfma_f32_16x16x32_bf16 v[106:109], v[178:181], v[214:217], v[106:109]
	v_mfma_f32_16x16x32_bf16 v[122:125], v[186:189], v[214:217], v[122:125]
	v_mfma_f32_16x16x32_bf16 v[102:105], v[178:181], v[222:225], v[102:105]
	v_mfma_f32_16x16x32_bf16 v[118:121], v[186:189], v[222:225], v[118:121]
	s_barrier
	s_add_i32 s63, s63, 2
	s_cmp_gt_u32 s63, 41
	s_mov_b64 s[34:35], s[30:31]
	s_cbranch_scc0 .LBB0_1505
